# K-loops: removed the priority drop/raise pair in the middle of each 32-MFMA block (on top of the moved priority changes)
# speedup vs baseline: 1.0016x; 1.0016x over previous
.LBB0_276:
	s_or_b64 exec, exec, s[60:61]
	s_add_u32 s62, s56, 0x10000
	s_addc_u32 s63, s57, 0
	s_and_b64 s[60:61], s[34:35], exec
	s_cselect_b32 s67, s51, s63
	s_cselect_b32 s66, s50, s62
	s_add_u32 s62, s58, 0x10000
	s_addc_u32 s63, s59, 0
	s_and_b64 s[60:61], s[34:35], exec
	s_cselect_b32 s63, s53, s63
	s_cselect_b32 s62, s52, s62
	s_add_u32 s60, s66, 0x8000
	s_addc_u32 s61, s67, 0
	s_add_u32 s64, s62, 0x8000
	s_addc_u32 s65, s63, 0
	s_add_i32 s84, 0, 0x10000
	s_add_i32 s85, 0, 0x14000
	v_add_u32_e32 v132, s84, v141
	v_add_u32_e32 v133, s85, v141
	ds_read_b128 v[2:5], v132
	ds_read_b128 v[6:9], v132 offset:1024
	ds_read_b128 v[10:13], v132 offset:2048
	ds_read_b128 v[14:17], v132 offset:3072
	ds_read_b128 v[18:21], v133
	ds_read_b128 v[22:25], v133 offset:1024
	ds_read_b128 v[26:29], v133 offset:2048
	ds_read_b128 v[30:33], v133 offset:3072
	s_add_u32 s82, s56, 0xc000
	s_addc_u32 s83, s57, 0
	s_add_i32 s80, s15, 0xc000
	s_mov_b32 m0, s80
	s_add_i32 s81, s15, 0xe000
	ds_read_b128 v[34:37], v143
	ds_read_b128 v[38:41], v143 offset:1024
	ds_read_b128 v[42:45], v143 offset:2048
	ds_read_b128 v[46:49], v143 offset:3072
	ds_read_b128 v[50:53], v143 offset:4096
	ds_read_b128 v[54:57], v143 offset:5120
	ds_read_b128 v[58:61], v143 offset:6144
	ds_read_b128 v[62:65], v143 offset:7168
	s_nop 0
	global_load_lds_dwordx4 v137, s[82:83]
	s_mov_b32 m0, s81
	s_nop 0
	global_load_lds_dwordx4 v139, s[82:83]
	s_waitcnt vmcnt(8)
	s_waitcnt lgkmcnt(0)
	s_setprio 1
	s_barrier
	s_waitcnt lgkmcnt(0)
	v_mfma_f32_16x16x32_bf16 v[86:89], v[10:13], v[50:53], 0
	v_mfma_f32_16x16x32_bf16 v[90:93], v[14:17], v[54:57], v[86:89]
	v_mfma_f32_16x16x32_bf16 v[86:89], v[2:5], v[58:61], 0
	v_mfma_f32_16x16x32_bf16 v[66:69], v[2:5], v[34:37], 0
	v_mfma_f32_16x16x32_bf16 v[70:73], v[10:13], v[34:37], 0
	v_mfma_f32_16x16x32_bf16 v[74:77], v[2:5], v[42:45], 0
	v_mfma_f32_16x16x32_bf16 v[78:81], v[10:13], v[42:45], 0
	v_mfma_f32_16x16x32_bf16 v[82:85], v[2:5], v[50:53], 0
	v_mfma_f32_16x16x32_bf16 v[94:97], v[6:9], v[62:65], v[86:89]
	v_mfma_f32_16x16x32_bf16 v[86:89], v[10:13], v[58:61], 0
	v_mfma_f32_16x16x32_bf16 v[66:69], v[6:9], v[38:41], v[66:69]
	v_mfma_f32_16x16x32_bf16 v[70:73], v[14:17], v[38:41], v[70:73]
	v_mfma_f32_16x16x32_bf16 v[74:77], v[6:9], v[46:49], v[74:77]
	v_mfma_f32_16x16x32_bf16 v[78:81], v[14:17], v[46:49], v[78:81]
	v_mfma_f32_16x16x32_bf16 v[82:85], v[6:9], v[54:57], v[82:85]
	v_mfma_f32_16x16x32_bf16 v[106:109], v[14:17], v[62:65], v[86:89]
	v_mfma_f32_16x16x32_bf16 v[86:89], v[18:21], v[34:37], 0
	v_mfma_f32_16x16x32_bf16 v[34:37], v[26:29], v[34:37], 0
	v_mfma_f32_16x16x32_bf16 v[110:113], v[22:25], v[38:41], v[86:89]
	v_mfma_f32_16x16x32_bf16 v[34:37], v[30:33], v[38:41], v[34:37]
	v_mfma_f32_16x16x32_bf16 v[38:41], v[18:21], v[42:45], 0
	v_mfma_f32_16x16x32_bf16 v[42:45], v[26:29], v[42:45], 0
	v_mfma_f32_16x16x32_bf16 v[38:41], v[22:25], v[46:49], v[38:41]
	v_mfma_f32_16x16x32_bf16 v[42:45], v[30:33], v[46:49], v[42:45]
	v_mfma_f32_16x16x32_bf16 v[46:49], v[18:21], v[50:53], 0
	v_mfma_f32_16x16x32_bf16 v[50:53], v[26:29], v[50:53], 0
	v_mfma_f32_16x16x32_bf16 v[46:49], v[22:25], v[54:57], v[46:49]
	v_mfma_f32_16x16x32_bf16 v[50:53], v[30:33], v[54:57], v[50:53]
	v_mfma_f32_16x16x32_bf16 v[54:57], v[18:21], v[58:61], 0
	v_mfma_f32_16x16x32_bf16 v[144:147], v[22:25], v[62:65], v[54:57]
	v_mfma_f32_16x16x32_bf16 v[54:57], v[26:29], v[58:61], 0
	v_mfma_f32_16x16x32_bf16 v[58:61], v[30:33], v[62:65], v[54:57]
	s_barrier
	s_setprio 0
	s_add_i32 s82, s84, s14
	s_add_i32 s83, s82, 0x2000
	s_mov_b32 m0, s82
	s_add_u32 s86, s62, 0x4000
	s_nop 0
	ds_read_b128 v[54:57], v143 offset:16384
	ds_read_b128 v[62:65], v143 offset:17408
	ds_read_b128 v[86:89], v143 offset:18432
	ds_read_b128 v[98:101], v143 offset:19456
	ds_read_b128 v[102:105], v143 offset:20480
	ds_read_b128 v[114:117], v143 offset:21504
	ds_read_b128 v[118:121], v143 offset:22528
	ds_read_b128 v[122:125], v143 offset:23552
	s_addc_u32 s87, s63, 0
	global_load_lds_dwordx4 v138, s[62:63]
	s_mov_b32 m0, s83
	s_add_i32 s84, s85, s14
	s_add_i32 s85, s84, 0x2000
	global_load_lds_dwordx4 v140, s[62:63]
	s_mov_b32 m0, s84
	s_nop 0
	global_load_lds_dwordx4 v138, s[86:87]
	s_mov_b32 m0, s85
	s_nop 0
	global_load_lds_dwordx4 v140, s[86:87]
	s_mov_b32 m0, s15
	s_nop 0
	global_load_lds_dwordx4 v137, s[66:67]
	s_mov_b32 m0, s18
	s_nop 0
	global_load_lds_dwordx4 v139, s[66:67]
	s_waitcnt vmcnt(8)
	s_waitcnt lgkmcnt(0)
	s_setprio 1
	s_barrier
	s_waitcnt lgkmcnt(0)
	v_mfma_f32_16x16x32_bf16 v[126:129], v[2:5], v[54:57], 0
	v_mfma_f32_16x16x32_bf16 v[148:151], v[6:9], v[62:65], v[126:129]
	v_mfma_f32_16x16x32_bf16 v[126:129], v[10:13], v[54:57], 0
	v_mfma_f32_16x16x32_bf16 v[152:155], v[14:17], v[62:65], v[126:129]
	v_mfma_f32_16x16x32_bf16 v[126:129], v[2:5], v[86:89], 0
	v_mfma_f32_16x16x32_bf16 v[156:159], v[6:9], v[98:101], v[126:129]
	v_mfma_f32_16x16x32_bf16 v[126:129], v[10:13], v[86:89], 0
	v_mfma_f32_16x16x32_bf16 v[160:163], v[14:17], v[98:101], v[126:129]
	v_mfma_f32_16x16x32_bf16 v[126:129], v[2:5], v[102:105], 0
	v_mfma_f32_16x16x32_bf16 v[2:5], v[2:5], v[118:121], 0
	v_mfma_f32_16x16x32_bf16 v[164:167], v[6:9], v[114:117], v[126:129]
	v_mfma_f32_16x16x32_bf16 v[2:5], v[6:9], v[122:125], v[2:5]
	v_mfma_f32_16x16x32_bf16 v[6:9], v[10:13], v[118:121], 0
	v_mfma_f32_16x16x32_bf16 v[126:129], v[10:13], v[102:105], 0
	v_mfma_f32_16x16x32_bf16 v[10:13], v[14:17], v[122:125], v[6:9]
	v_mfma_f32_16x16x32_bf16 v[168:171], v[14:17], v[114:117], v[126:129]
	v_mfma_f32_16x16x32_bf16 v[6:9], v[18:21], v[54:57], 0
	v_mfma_f32_16x16x32_bf16 v[14:17], v[22:25], v[62:65], v[6:9]
	v_mfma_f32_16x16x32_bf16 v[6:9], v[26:29], v[54:57], 0
	v_mfma_f32_16x16x32_bf16 v[172:175], v[30:33], v[62:65], v[6:9]
	v_mfma_f32_16x16x32_bf16 v[6:9], v[18:21], v[86:89], 0
	v_mfma_f32_16x16x32_bf16 v[176:179], v[22:25], v[98:101], v[6:9]
	v_mfma_f32_16x16x32_bf16 v[6:9], v[26:29], v[86:89], 0
	v_mfma_f32_16x16x32_bf16 v[180:183], v[30:33], v[98:101], v[6:9]
	v_mfma_f32_16x16x32_bf16 v[6:9], v[18:21], v[102:105], 0
	v_mfma_f32_16x16x32_bf16 v[184:187], v[22:25], v[114:117], v[6:9]
	v_mfma_f32_16x16x32_bf16 v[6:9], v[26:29], v[102:105], 0
	v_mfma_f32_16x16x32_bf16 v[210:213], v[30:33], v[114:117], v[6:9]
	v_mfma_f32_16x16x32_bf16 v[6:9], v[18:21], v[118:121], 0
	v_mfma_f32_16x16x32_bf16 v[214:217], v[22:25], v[122:125], v[6:9]
	v_mfma_f32_16x16x32_bf16 v[6:9], v[26:29], v[118:121], 0
	v_mfma_f32_16x16x32_bf16 v[218:221], v[30:33], v[122:125], v[6:9]
	s_barrier
	s_setprio 0
	s_add_i32 s86, 0, 0x18000
	s_add_i32 s87, 0, 0x1c000
	v_add_u32_e32 v134, s86, v141
	v_add_u32_e32 v135, s87, v141
	s_nop 0
	ds_read_b128 v[6:9], v134
	ds_read_b128 v[26:29], v134 offset:1024
	ds_read_b128 v[30:33], v134 offset:2048
	ds_read_b128 v[222:225], v134 offset:3072
	ds_read_b128 v[236:239], v135
	ds_read_b128 v[240:243], v135 offset:1024
	ds_read_b128 v[244:247], v135 offset:2048
	ds_read_b128 v[232:235], v135 offset:3072
	s_add_u32 s66, s66, 0x4000
	s_addc_u32 s67, s67, 0
	s_mov_b32 m0, s20
	ds_read_b128 v[18:21], v143 offset:32768
	ds_read_b128 v[22:25], v143 offset:33792
	ds_read_b128 v[194:197], v143 offset:34816
	ds_read_b128 v[202:205], v143 offset:35840
	ds_read_b128 v[188:191], v143 offset:36864
	ds_read_b128 v[206:209], v143 offset:37888
	ds_read_b128 v[198:201], v143 offset:38912
	ds_read_b128 v[226:229], v143 offset:39936
	s_nop 0
	global_load_lds_dwordx4 v137, s[66:67]
	s_mov_b32 m0, s21
	s_nop 0
	global_load_lds_dwordx4 v139, s[66:67]
	s_waitcnt vmcnt(8)
	s_waitcnt lgkmcnt(0)
	s_setprio 1
	s_barrier
	s_waitcnt lgkmcnt(0)
	v_mfma_f32_16x16x32_bf16 v[54:57], v[6:9], v[18:21], v[66:69]
	v_mfma_f32_16x16x32_bf16 v[118:121], v[26:29], v[22:25], v[54:57]
	v_mfma_f32_16x16x32_bf16 v[54:57], v[30:33], v[18:21], v[70:73]
	v_mfma_f32_16x16x32_bf16 v[114:117], v[222:225], v[22:25], v[54:57]
	v_mfma_f32_16x16x32_bf16 v[54:57], v[6:9], v[194:197], v[74:77]
	v_mfma_f32_16x16x32_bf16 v[102:105], v[26:29], v[202:205], v[54:57]
	v_mfma_f32_16x16x32_bf16 v[54:57], v[30:33], v[194:197], v[78:81]
	v_mfma_f32_16x16x32_bf16 v[98:101], v[222:225], v[202:205], v[54:57]
	v_mfma_f32_16x16x32_bf16 v[54:57], v[6:9], v[188:191], v[82:85]
	v_mfma_f32_16x16x32_bf16 v[86:89], v[26:29], v[206:209], v[54:57]
	v_mfma_f32_16x16x32_bf16 v[54:57], v[30:33], v[188:191], v[90:93]
	v_mfma_f32_16x16x32_bf16 v[82:85], v[222:225], v[206:209], v[54:57]
	v_mfma_f32_16x16x32_bf16 v[54:57], v[6:9], v[198:201], v[94:97]
	v_mfma_f32_16x16x32_bf16 v[62:65], v[26:29], v[226:229], v[54:57]
	v_mfma_f32_16x16x32_bf16 v[54:57], v[30:33], v[198:201], v[106:109]
	v_mfma_f32_16x16x32_bf16 v[54:57], v[222:225], v[226:229], v[54:57]
	v_mfma_f32_16x16x32_bf16 v[66:69], v[236:239], v[18:21], v[110:113]
	v_mfma_f32_16x16x32_bf16 v[18:21], v[244:247], v[18:21], v[34:37]
	v_mfma_f32_16x16x32_bf16 v[122:125], v[232:235], v[22:25], v[18:21]
	v_mfma_f32_16x16x32_bf16 v[18:21], v[236:239], v[194:197], v[38:41]
	v_mfma_f32_16x16x32_bf16 v[110:113], v[240:243], v[202:205], v[18:21]
	v_mfma_f32_16x16x32_bf16 v[18:21], v[244:247], v[194:197], v[42:45]
	v_mfma_f32_16x16x32_bf16 v[106:109], v[232:235], v[202:205], v[18:21]
	v_mfma_f32_16x16x32_bf16 v[18:21], v[236:239], v[188:191], v[46:49]
	v_mfma_f32_16x16x32_bf16 v[94:97], v[240:243], v[206:209], v[18:21]
	v_mfma_f32_16x16x32_bf16 v[18:21], v[244:247], v[188:191], v[50:53]
	v_mfma_f32_16x16x32_bf16 v[90:93], v[232:235], v[206:209], v[18:21]
	v_mfma_f32_16x16x32_bf16 v[18:21], v[236:239], v[198:201], v[144:147]
	v_mfma_f32_16x16x32_bf16 v[78:81], v[240:243], v[226:229], v[18:21]
	v_mfma_f32_16x16x32_bf16 v[18:21], v[244:247], v[198:201], v[58:61]
	v_mfma_f32_16x16x32_bf16 v[126:129], v[240:243], v[22:25], v[66:69]
	v_mfma_f32_16x16x32_bf16 v[70:73], v[232:235], v[226:229], v[18:21]
	s_barrier
	s_setprio 0
	s_add_i32 s66, s86, s14
	s_add_i32 s67, s66, 0x2000
	s_mov_b32 m0, s66
	s_add_u32 s62, s62, 0xc000
	ds_read_b128 v[42:45], v143 offset:49152
	ds_read_b128 v[46:49], v143 offset:50176
	ds_read_b128 v[144:147], v143 offset:51200
	ds_read_b128 v[188:191], v143 offset:52224
	ds_read_b128 v[194:197], v143 offset:53248
	ds_read_b128 v[198:201], v143 offset:54272
	ds_read_b128 v[202:205], v143 offset:55296
	ds_read_b128 v[206:209], v143 offset:56320
	s_addc_u32 s63, s63, 0
	global_load_lds_dwordx4 v138, s[64:65]
	s_mov_b32 m0, s67
	s_add_i32 s86, s87, s14
	s_add_i32 s87, s86, 0x2000
	global_load_lds_dwordx4 v140, s[64:65]
	s_mov_b32 m0, s86
	s_nop 0
	global_load_lds_dwordx4 v138, s[62:63]
	s_mov_b32 m0, s87
	s_nop 0
	global_load_lds_dwordx4 v140, s[62:63]
	s_mov_b32 m0, s69
	s_nop 0
	global_load_lds_dwordx4 v137, s[60:61]
	s_mov_b32 m0, s70
	s_nop 0
	global_load_lds_dwordx4 v139, s[60:61]
	s_waitcnt vmcnt(8)
	s_waitcnt lgkmcnt(0)
	s_setprio 1
	s_barrier
	s_waitcnt lgkmcnt(0)
	v_mfma_f32_16x16x32_bf16 v[18:21], v[6:9], v[42:45], v[148:151]
	v_mfma_f32_16x16x32_bf16 v[58:61], v[26:29], v[46:49], v[18:21]
	v_mfma_f32_16x16x32_bf16 v[18:21], v[30:33], v[42:45], v[152:155]
	v_mfma_f32_16x16x32_bf16 v[50:53], v[222:225], v[46:49], v[18:21]
	v_mfma_f32_16x16x32_bf16 v[18:21], v[6:9], v[144:147], v[156:159]
	v_mfma_f32_16x16x32_bf16 v[38:41], v[26:29], v[188:191], v[18:21]
	v_mfma_f32_16x16x32_bf16 v[18:21], v[30:33], v[144:147], v[160:163]
	v_mfma_f32_16x16x32_bf16 v[34:37], v[222:225], v[188:191], v[18:21]
	v_mfma_f32_16x16x32_bf16 v[18:21], v[6:9], v[194:197], v[164:167]
	v_mfma_f32_16x16x32_bf16 v[2:5], v[6:9], v[202:205], v[2:5]
	v_mfma_f32_16x16x32_bf16 v[22:25], v[26:29], v[198:201], v[18:21]
	v_mfma_f32_16x16x32_bf16 v[18:21], v[30:33], v[194:197], v[168:171]
	v_mfma_f32_16x16x32_bf16 v[6:9], v[26:29], v[206:209], v[2:5]
	v_mfma_f32_16x16x32_bf16 v[2:5], v[30:33], v[202:205], v[10:13]
	v_mfma_f32_16x16x32_bf16 v[18:21], v[222:225], v[198:201], v[18:21]
	v_mfma_f32_16x16x32_bf16 v[2:5], v[222:225], v[206:209], v[2:5]
	v_mfma_f32_16x16x32_bf16 v[10:13], v[236:239], v[42:45], v[14:17]
	v_mfma_f32_16x16x32_bf16 v[74:77], v[240:243], v[46:49], v[10:13]
	v_mfma_f32_16x16x32_bf16 v[10:13], v[244:247], v[42:45], v[172:175]
	v_mfma_f32_16x16x32_bf16 v[66:69], v[232:235], v[46:49], v[10:13]
	v_mfma_f32_16x16x32_bf16 v[10:13], v[236:239], v[144:147], v[176:179]
	v_mfma_f32_16x16x32_bf16 v[46:49], v[240:243], v[188:191], v[10:13]
	v_mfma_f32_16x16x32_bf16 v[10:13], v[244:247], v[144:147], v[180:183]
	v_mfma_f32_16x16x32_bf16 v[42:45], v[232:235], v[188:191], v[10:13]
	v_mfma_f32_16x16x32_bf16 v[10:13], v[236:239], v[194:197], v[184:187]
	v_mfma_f32_16x16x32_bf16 v[30:33], v[240:243], v[198:201], v[10:13]
	v_mfma_f32_16x16x32_bf16 v[10:13], v[244:247], v[194:197], v[210:213]
	v_mfma_f32_16x16x32_bf16 v[26:29], v[232:235], v[198:201], v[10:13]
	v_mfma_f32_16x16x32_bf16 v[10:13], v[236:239], v[202:205], v[214:217]
	v_mfma_f32_16x16x32_bf16 v[14:17], v[240:243], v[206:209], v[10:13]
	v_mfma_f32_16x16x32_bf16 v[10:13], v[244:247], v[202:205], v[218:221]
	v_mfma_f32_16x16x32_bf16 v[10:13], v[232:235], v[206:209], v[10:13]
	s_barrier
	s_setprio 0
	s_andn2_b64 vcc, exec, s[44:45]
	s_cbranch_vccnz .LBB0_282
	s_lshl_b32 s60, s74, 10
	s_xor_b32 s88, s60, 0x400
	s_add_u32 s89, s58, 0x20000
	s_addc_u32 s90, s59, 0
	v_ashrrev_i32_e32 v131, 31, v130
	s_add_u32 s56, s56, 0x1c000
	v_lshl_add_u64 v[130:131], v[130:131], 3, s[26:27]
	s_addc_u32 s57, s57, 0
	s_mov_b32 s91, 4

.LBB0_280:
	s_or_b64 exec, exec, s[60:61]
	ds_read_b128 v[144:147], v132
	ds_read_b128 v[148:151], v132 offset:1024
	ds_read_b128 v[152:155], v132 offset:2048
	ds_read_b128 v[156:159], v132 offset:3072
	ds_read_b128 v[160:163], v133
	ds_read_b128 v[164:167], v133 offset:1024
	ds_read_b128 v[168:171], v133 offset:2048
	ds_read_b128 v[172:175], v133 offset:3072
	s_add_u32 s60, s56, 0x4000
	s_addc_u32 s61, s57, 0
	s_and_b64 s[58:59], s[58:59], exec
	s_cselect_b32 s64, s50, s60
	s_cselect_b32 s65, s51, s61
	s_cselect_b32 s61, s53, s90
	s_cselect_b32 s60, s52, s89
	s_add_u32 s58, s64, 0x8000
	s_addc_u32 s59, s65, 0
	s_add_u32 s62, s60, 0x8000
	s_addc_u32 s63, s61, 0
	s_mov_b32 m0, s80
	ds_read_b128 v[176:179], v143
	ds_read_b128 v[180:183], v143 offset:1024
	ds_read_b128 v[184:187], v143 offset:2048
	ds_read_b128 v[188:191], v143 offset:3072
	ds_read_b128 v[194:197], v143 offset:4096
	ds_read_b128 v[198:201], v143 offset:5120
	ds_read_b128 v[202:205], v143 offset:6144
	ds_read_b128 v[206:209], v143 offset:7168
	s_nop 0
	global_load_lds_dwordx4 v137, s[56:57]
	s_mov_b32 m0, s81
	s_nop 0
	global_load_lds_dwordx4 v139, s[56:57]
	s_waitcnt vmcnt(8)
	s_waitcnt lgkmcnt(0)
	s_setprio 1
	s_barrier
	s_waitcnt lgkmcnt(0)
	v_mfma_f32_16x16x32_bf16 v[118:121], v[144:147], v[176:179], v[118:121]
	v_mfma_f32_16x16x32_bf16 v[114:117], v[152:155], v[176:179], v[114:117]
	v_mfma_f32_16x16x32_bf16 v[102:105], v[144:147], v[184:187], v[102:105]
	v_mfma_f32_16x16x32_bf16 v[98:101], v[152:155], v[184:187], v[98:101]
	v_mfma_f32_16x16x32_bf16 v[86:89], v[144:147], v[194:197], v[86:89]
	v_mfma_f32_16x16x32_bf16 v[82:85], v[152:155], v[194:197], v[82:85]
	v_mfma_f32_16x16x32_bf16 v[62:65], v[144:147], v[202:205], v[62:65]
	v_mfma_f32_16x16x32_bf16 v[54:57], v[152:155], v[202:205], v[54:57]
	v_mfma_f32_16x16x32_bf16 v[118:121], v[148:151], v[180:183], v[118:121]
	v_mfma_f32_16x16x32_bf16 v[114:117], v[156:159], v[180:183], v[114:117]
	v_mfma_f32_16x16x32_bf16 v[102:105], v[148:151], v[188:191], v[102:105]
	v_mfma_f32_16x16x32_bf16 v[98:101], v[156:159], v[188:191], v[98:101]
	v_mfma_f32_16x16x32_bf16 v[86:89], v[148:151], v[198:201], v[86:89]
	v_mfma_f32_16x16x32_bf16 v[82:85], v[156:159], v[198:201], v[82:85]
	v_mfma_f32_16x16x32_bf16 v[62:65], v[148:151], v[206:209], v[62:65]
	v_mfma_f32_16x16x32_bf16 v[54:57], v[156:159], v[206:209], v[54:57]
	v_mfma_f32_16x16x32_bf16 v[126:129], v[160:163], v[176:179], v[126:129]
	v_mfma_f32_16x16x32_bf16 v[122:125], v[168:171], v[176:179], v[122:125]
	v_mfma_f32_16x16x32_bf16 v[110:113], v[160:163], v[184:187], v[110:113]
	v_mfma_f32_16x16x32_bf16 v[106:109], v[168:171], v[184:187], v[106:109]
	v_mfma_f32_16x16x32_bf16 v[94:97], v[160:163], v[194:197], v[94:97]
	v_mfma_f32_16x16x32_bf16 v[90:93], v[168:171], v[194:197], v[90:93]
	v_mfma_f32_16x16x32_bf16 v[78:81], v[160:163], v[202:205], v[78:81]
	v_mfma_f32_16x16x32_bf16 v[70:73], v[168:171], v[202:205], v[70:73]
	v_mfma_f32_16x16x32_bf16 v[126:129], v[164:167], v[180:183], v[126:129]
	v_mfma_f32_16x16x32_bf16 v[122:125], v[172:175], v[180:183], v[122:125]
	v_mfma_f32_16x16x32_bf16 v[110:113], v[164:167], v[188:191], v[110:113]
	v_mfma_f32_16x16x32_bf16 v[106:109], v[172:175], v[188:191], v[106:109]
	v_mfma_f32_16x16x32_bf16 v[94:97], v[164:167], v[198:201], v[94:97]
	v_mfma_f32_16x16x32_bf16 v[90:93], v[172:175], v[198:201], v[90:93]
	v_mfma_f32_16x16x32_bf16 v[78:81], v[164:167], v[206:209], v[78:81]
	v_mfma_f32_16x16x32_bf16 v[70:73], v[172:175], v[206:209], v[70:73]
	s_barrier
	s_setprio 0
	s_mov_b32 m0, s82
	ds_read_b128 v[176:179], v143 offset:16384
	ds_read_b128 v[180:183], v143 offset:17408
	ds_read_b128 v[184:187], v143 offset:18432
	ds_read_b128 v[188:191], v143 offset:19456
	ds_read_b128 v[194:197], v143 offset:20480
	ds_read_b128 v[198:201], v143 offset:21504
	ds_read_b128 v[202:205], v143 offset:22528
	ds_read_b128 v[206:209], v143 offset:23552
	s_add_u32 s92, s60, 0x4000
	global_load_lds_dwordx4 v138, s[60:61]
	s_mov_b32 m0, s83
	s_addc_u32 s93, s61, 0
	global_load_lds_dwordx4 v140, s[60:61]
	s_mov_b32 m0, s84
	s_nop 0
	global_load_lds_dwordx4 v138, s[92:93]
	s_mov_b32 m0, s85
	s_nop 0
	global_load_lds_dwordx4 v140, s[92:93]
	s_mov_b32 m0, s15
	s_nop 0
	global_load_lds_dwordx4 v137, s[64:65]
	s_mov_b32 m0, s18
	s_nop 0
	global_load_lds_dwordx4 v139, s[64:65]
	s_waitcnt vmcnt(8)
	s_waitcnt lgkmcnt(0)
	s_setprio 1
	s_barrier
	s_waitcnt lgkmcnt(0)
	v_mfma_f32_16x16x32_bf16 v[58:61], v[144:147], v[176:179], v[58:61]
	v_mfma_f32_16x16x32_bf16 v[50:53], v[152:155], v[176:179], v[50:53]
	v_mfma_f32_16x16x32_bf16 v[38:41], v[144:147], v[184:187], v[38:41]
	v_mfma_f32_16x16x32_bf16 v[34:37], v[152:155], v[184:187], v[34:37]
	v_mfma_f32_16x16x32_bf16 v[22:25], v[144:147], v[194:197], v[22:25]
	v_mfma_f32_16x16x32_bf16 v[18:21], v[152:155], v[194:197], v[18:21]
	v_mfma_f32_16x16x32_bf16 v[6:9], v[144:147], v[202:205], v[6:9]
	v_mfma_f32_16x16x32_bf16 v[2:5], v[152:155], v[202:205], v[2:5]
	v_mfma_f32_16x16x32_bf16 v[58:61], v[148:151], v[180:183], v[58:61]
	v_mfma_f32_16x16x32_bf16 v[50:53], v[156:159], v[180:183], v[50:53]
	v_mfma_f32_16x16x32_bf16 v[38:41], v[148:151], v[188:191], v[38:41]
	v_mfma_f32_16x16x32_bf16 v[34:37], v[156:159], v[188:191], v[34:37]
	v_mfma_f32_16x16x32_bf16 v[22:25], v[148:151], v[198:201], v[22:25]
	v_mfma_f32_16x16x32_bf16 v[18:21], v[156:159], v[198:201], v[18:21]
	v_mfma_f32_16x16x32_bf16 v[6:9], v[148:151], v[206:209], v[6:9]
	v_mfma_f32_16x16x32_bf16 v[2:5], v[156:159], v[206:209], v[2:5]
	v_mfma_f32_16x16x32_bf16 v[74:77], v[160:163], v[176:179], v[74:77]
	v_mfma_f32_16x16x32_bf16 v[66:69], v[168:171], v[176:179], v[66:69]
	v_mfma_f32_16x16x32_bf16 v[46:49], v[160:163], v[184:187], v[46:49]
	v_mfma_f32_16x16x32_bf16 v[42:45], v[168:171], v[184:187], v[42:45]
	v_mfma_f32_16x16x32_bf16 v[30:33], v[160:163], v[194:197], v[30:33]
	v_mfma_f32_16x16x32_bf16 v[26:29], v[168:171], v[194:197], v[26:29]
	v_mfma_f32_16x16x32_bf16 v[14:17], v[160:163], v[202:205], v[14:17]
	v_mfma_f32_16x16x32_bf16 v[10:13], v[168:171], v[202:205], v[10:13]
	v_mfma_f32_16x16x32_bf16 v[74:77], v[164:167], v[180:183], v[74:77]
	v_mfma_f32_16x16x32_bf16 v[66:69], v[172:175], v[180:183], v[66:69]
	v_mfma_f32_16x16x32_bf16 v[46:49], v[164:167], v[188:191], v[46:49]
	v_mfma_f32_16x16x32_bf16 v[42:45], v[172:175], v[188:191], v[42:45]
	v_mfma_f32_16x16x32_bf16 v[30:33], v[164:167], v[198:201], v[30:33]
	v_mfma_f32_16x16x32_bf16 v[26:29], v[172:175], v[198:201], v[26:29]
	v_mfma_f32_16x16x32_bf16 v[14:17], v[164:167], v[206:209], v[14:17]
	v_mfma_f32_16x16x32_bf16 v[10:13], v[172:175], v[206:209], v[10:13]
	s_barrier
	s_setprio 0
	ds_read_b128 v[144:147], v134
	ds_read_b128 v[148:151], v134 offset:1024
	ds_read_b128 v[152:155], v134 offset:2048
	ds_read_b128 v[156:159], v134 offset:3072
	ds_read_b128 v[160:163], v135
	ds_read_b128 v[164:167], v135 offset:1024
	ds_read_b128 v[168:171], v135 offset:2048
	ds_read_b128 v[172:175], v135 offset:3072
	s_add_u32 s64, s64, 0x4000
	s_addc_u32 s65, s65, 0
	s_mov_b32 m0, s20
	ds_read_b128 v[176:179], v143 offset:32768
	ds_read_b128 v[180:183], v143 offset:33792
	ds_read_b128 v[184:187], v143 offset:34816
	ds_read_b128 v[188:191], v143 offset:35840
	ds_read_b128 v[194:197], v143 offset:36864
	ds_read_b128 v[198:201], v143 offset:37888
	ds_read_b128 v[202:205], v143 offset:38912
	ds_read_b128 v[206:209], v143 offset:39936
	s_nop 0
	global_load_lds_dwordx4 v137, s[64:65]
	s_mov_b32 m0, s21
	s_nop 0
	global_load_lds_dwordx4 v139, s[64:65]
	s_waitcnt vmcnt(8)
	s_waitcnt lgkmcnt(0)
	s_setprio 1
	s_barrier
	s_waitcnt lgkmcnt(0)
	v_mfma_f32_16x16x32_bf16 v[118:121], v[144:147], v[176:179], v[118:121]
	v_mfma_f32_16x16x32_bf16 v[114:117], v[152:155], v[176:179], v[114:117]
	v_mfma_f32_16x16x32_bf16 v[102:105], v[144:147], v[184:187], v[102:105]
	v_mfma_f32_16x16x32_bf16 v[98:101], v[152:155], v[184:187], v[98:101]
	v_mfma_f32_16x16x32_bf16 v[86:89], v[144:147], v[194:197], v[86:89]
	v_mfma_f32_16x16x32_bf16 v[82:85], v[152:155], v[194:197], v[82:85]
	v_mfma_f32_16x16x32_bf16 v[62:65], v[144:147], v[202:205], v[62:65]
	v_mfma_f32_16x16x32_bf16 v[54:57], v[152:155], v[202:205], v[54:57]
	v_mfma_f32_16x16x32_bf16 v[118:121], v[148:151], v[180:183], v[118:121]
	v_mfma_f32_16x16x32_bf16 v[114:117], v[156:159], v[180:183], v[114:117]
	v_mfma_f32_16x16x32_bf16 v[102:105], v[148:151], v[188:191], v[102:105]
	v_mfma_f32_16x16x32_bf16 v[98:101], v[156:159], v[188:191], v[98:101]
	v_mfma_f32_16x16x32_bf16 v[86:89], v[148:151], v[198:201], v[86:89]
	v_mfma_f32_16x16x32_bf16 v[82:85], v[156:159], v[198:201], v[82:85]
	v_mfma_f32_16x16x32_bf16 v[62:65], v[148:151], v[206:209], v[62:65]
	v_mfma_f32_16x16x32_bf16 v[54:57], v[156:159], v[206:209], v[54:57]
	v_mfma_f32_16x16x32_bf16 v[126:129], v[160:163], v[176:179], v[126:129]
	v_mfma_f32_16x16x32_bf16 v[122:125], v[168:171], v[176:179], v[122:125]
	v_mfma_f32_16x16x32_bf16 v[110:113], v[160:163], v[184:187], v[110:113]
	v_mfma_f32_16x16x32_bf16 v[106:109], v[168:171], v[184:187], v[106:109]
	v_mfma_f32_16x16x32_bf16 v[94:97], v[160:163], v[194:197], v[94:97]
	v_mfma_f32_16x16x32_bf16 v[90:93], v[168:171], v[194:197], v[90:93]
	v_mfma_f32_16x16x32_bf16 v[78:81], v[160:163], v[202:205], v[78:81]
	v_mfma_f32_16x16x32_bf16 v[70:73], v[168:171], v[202:205], v[70:73]
	v_mfma_f32_16x16x32_bf16 v[126:129], v[164:167], v[180:183], v[126:129]
	v_mfma_f32_16x16x32_bf16 v[122:125], v[172:175], v[180:183], v[122:125]
	v_mfma_f32_16x16x32_bf16 v[110:113], v[164:167], v[188:191], v[110:113]
	v_mfma_f32_16x16x32_bf16 v[106:109], v[172:175], v[188:191], v[106:109]
	v_mfma_f32_16x16x32_bf16 v[94:97], v[164:167], v[198:201], v[94:97]
	v_mfma_f32_16x16x32_bf16 v[90:93], v[172:175], v[198:201], v[90:93]
	v_mfma_f32_16x16x32_bf16 v[78:81], v[164:167], v[206:209], v[78:81]
	v_mfma_f32_16x16x32_bf16 v[70:73], v[172:175], v[206:209], v[70:73]
	s_barrier
	s_setprio 0
	s_mov_b32 m0, s66
	ds_read_b128 v[176:179], v143 offset:49152
	ds_read_b128 v[180:183], v143 offset:50176
	ds_read_b128 v[184:187], v143 offset:51200
	ds_read_b128 v[188:191], v143 offset:52224
	ds_read_b128 v[194:197], v143 offset:53248
	ds_read_b128 v[198:201], v143 offset:54272
	ds_read_b128 v[202:205], v143 offset:55296
	ds_read_b128 v[206:209], v143 offset:56320
	s_add_u32 s60, s60, 0xc000
	global_load_lds_dwordx4 v138, s[62:63]
	s_mov_b32 m0, s67
	s_addc_u32 s61, s61, 0
	global_load_lds_dwordx4 v140, s[62:63]
	s_mov_b32 m0, s86
	s_nop 0
	global_load_lds_dwordx4 v138, s[60:61]
	s_mov_b32 m0, s87
	s_nop 0
	global_load_lds_dwordx4 v140, s[60:61]
	s_mov_b32 m0, s69
	s_nop 0
	global_load_lds_dwordx4 v137, s[58:59]
	s_mov_b32 m0, s70
	s_nop 0
	global_load_lds_dwordx4 v139, s[58:59]
	s_waitcnt vmcnt(8)
	s_waitcnt lgkmcnt(0)
	s_setprio 1
	s_barrier
	s_waitcnt lgkmcnt(0)
	v_mfma_f32_16x16x32_bf16 v[58:61], v[144:147], v[176:179], v[58:61]
	v_mfma_f32_16x16x32_bf16 v[50:53], v[152:155], v[176:179], v[50:53]
	v_mfma_f32_16x16x32_bf16 v[38:41], v[144:147], v[184:187], v[38:41]
	v_mfma_f32_16x16x32_bf16 v[34:37], v[152:155], v[184:187], v[34:37]
	v_mfma_f32_16x16x32_bf16 v[22:25], v[144:147], v[194:197], v[22:25]
	v_mfma_f32_16x16x32_bf16 v[18:21], v[152:155], v[194:197], v[18:21]
	v_mfma_f32_16x16x32_bf16 v[6:9], v[144:147], v[202:205], v[6:9]
	v_mfma_f32_16x16x32_bf16 v[2:5], v[152:155], v[202:205], v[2:5]
	v_mfma_f32_16x16x32_bf16 v[58:61], v[148:151], v[180:183], v[58:61]
	v_mfma_f32_16x16x32_bf16 v[50:53], v[156:159], v[180:183], v[50:53]
	v_mfma_f32_16x16x32_bf16 v[38:41], v[148:151], v[188:191], v[38:41]
	v_mfma_f32_16x16x32_bf16 v[34:37], v[156:159], v[188:191], v[34:37]
	v_mfma_f32_16x16x32_bf16 v[22:25], v[148:151], v[198:201], v[22:25]
	v_mfma_f32_16x16x32_bf16 v[18:21], v[156:159], v[198:201], v[18:21]
	v_mfma_f32_16x16x32_bf16 v[6:9], v[148:151], v[206:209], v[6:9]
	v_mfma_f32_16x16x32_bf16 v[2:5], v[156:159], v[206:209], v[2:5]
	v_mfma_f32_16x16x32_bf16 v[74:77], v[160:163], v[176:179], v[74:77]
	v_mfma_f32_16x16x32_bf16 v[66:69], v[168:171], v[176:179], v[66:69]
	v_mfma_f32_16x16x32_bf16 v[46:49], v[160:163], v[184:187], v[46:49]
	v_mfma_f32_16x16x32_bf16 v[42:45], v[168:171], v[184:187], v[42:45]
	v_mfma_f32_16x16x32_bf16 v[30:33], v[160:163], v[194:197], v[30:33]
	v_mfma_f32_16x16x32_bf16 v[26:29], v[168:171], v[194:197], v[26:29]
	v_mfma_f32_16x16x32_bf16 v[14:17], v[160:163], v[202:205], v[14:17]
	v_mfma_f32_16x16x32_bf16 v[10:13], v[168:171], v[202:205], v[10:13]
	v_mfma_f32_16x16x32_bf16 v[74:77], v[164:167], v[180:183], v[74:77]
	v_mfma_f32_16x16x32_bf16 v[66:69], v[172:175], v[180:183], v[66:69]
	v_mfma_f32_16x16x32_bf16 v[46:49], v[164:167], v[188:191], v[46:49]
	v_mfma_f32_16x16x32_bf16 v[42:45], v[172:175], v[188:191], v[42:45]
	v_mfma_f32_16x16x32_bf16 v[30:33], v[164:167], v[198:201], v[30:33]
	v_mfma_f32_16x16x32_bf16 v[26:29], v[172:175], v[198:201], v[26:29]
	v_mfma_f32_16x16x32_bf16 v[14:17], v[164:167], v[206:209], v[14:17]
	v_mfma_f32_16x16x32_bf16 v[10:13], v[172:175], v[206:209], v[10:13]
	s_barrier
	s_setprio 0
	s_add_i32 s58, s91, 2
	s_add_u32 s89, s89, 0x10000
	s_addc_u32 s90, s90, 0
	s_add_u32 s56, s56, 0x10000
	s_addc_u32 s57, s57, 0
	s_cmp_lt_i32 s91, s25
	s_cbranch_scc0 .LBB0_282
	s_mov_b32 s91, s58
	s_branch .LBB0_278

.LBB0_306:
	s_add_i32 s68, s50, 2
	s_add_u32 s48, s46, 0x100
	s_addc_u32 s49, s47, 0
	s_add_i32 s69, 0, 0x10000
	s_cmp_eq_u32 s60, s50
	s_cselect_b32 s51, s41, s49
	s_cselect_b32 s50, s40, s48
	v_add_u32_e32 v131, s69, v133
	s_cselect_b32 s53, s43, s67
	s_cselect_b32 s52, s42, s45
	s_add_i32 s70, 0, 0x14000
	ds_read_b128 v[138:141], v131
	ds_read_b128 v[142:145], v131 offset:1024
	ds_read_b128 v[146:149], v131 offset:2048
	ds_read_b128 v[150:153], v131 offset:3072
	v_add_u32_e32 v131, s70, v133
	ds_read_b128 v[154:157], v131
	ds_read_b128 v[158:161], v131 offset:1024
	ds_read_b128 v[162:165], v131 offset:2048
	ds_read_b128 v[166:169], v131 offset:3072
	s_add_u32 s46, s46, s61
	s_addc_u32 s47, s47, s62
	s_add_i32 m0, s15, 0xc000
	ds_read_b128 v[170:173], v136
	ds_read_b128 v[174:177], v136 offset:1024
	ds_read_b128 v[178:181], v136 offset:2048
	ds_read_b128 v[182:185], v136 offset:3072
	ds_read_b128 v[186:189], v136 offset:4096
	ds_read_b128 v[194:197], v136 offset:5120
	ds_read_b128 v[198:201], v136 offset:6144
	ds_read_b128 v[202:205], v136 offset:7168
	s_nop 0
	global_load_lds_dwordx4 v0, s[46:47]
	s_add_i32 m0, s15, 0xe000
	s_nop 0
	global_load_lds_dwordx4 v130, s[46:47]
	s_waitcnt vmcnt(8)
	s_waitcnt lgkmcnt(0)
	s_setprio 1
	s_barrier
	s_waitcnt lgkmcnt(0)
	v_mfma_f32_16x16x32_bf16 v[126:129], v[138:141], v[170:173], v[126:129]
	v_mfma_f32_16x16x32_bf16 v[118:121], v[146:149], v[170:173], v[118:121]
	v_mfma_f32_16x16x32_bf16 v[110:113], v[138:141], v[178:181], v[110:113]
	v_mfma_f32_16x16x32_bf16 v[102:105], v[146:149], v[178:181], v[102:105]
	v_mfma_f32_16x16x32_bf16 v[94:97], v[138:141], v[186:189], v[94:97]
	v_mfma_f32_16x16x32_bf16 v[86:89], v[146:149], v[186:189], v[86:89]
	v_mfma_f32_16x16x32_bf16 v[78:81], v[138:141], v[198:201], v[78:81]
	v_mfma_f32_16x16x32_bf16 v[70:73], v[146:149], v[198:201], v[70:73]
	v_mfma_f32_16x16x32_bf16 v[126:129], v[142:145], v[174:177], v[126:129]
	v_mfma_f32_16x16x32_bf16 v[118:121], v[150:153], v[174:177], v[118:121]
	v_mfma_f32_16x16x32_bf16 v[110:113], v[142:145], v[182:185], v[110:113]
	v_mfma_f32_16x16x32_bf16 v[102:105], v[150:153], v[182:185], v[102:105]
	v_mfma_f32_16x16x32_bf16 v[94:97], v[142:145], v[194:197], v[94:97]
	v_mfma_f32_16x16x32_bf16 v[86:89], v[150:153], v[194:197], v[86:89]
	v_mfma_f32_16x16x32_bf16 v[78:81], v[142:145], v[202:205], v[78:81]
	v_mfma_f32_16x16x32_bf16 v[70:73], v[150:153], v[202:205], v[70:73]
	v_mfma_f32_16x16x32_bf16 v[54:57], v[154:157], v[170:173], v[54:57]
	v_mfma_f32_16x16x32_bf16 v[46:49], v[162:165], v[170:173], v[46:49]
	v_mfma_f32_16x16x32_bf16 v[38:41], v[154:157], v[178:181], v[38:41]
	v_mfma_f32_16x16x32_bf16 v[30:33], v[162:165], v[178:181], v[30:33]
	v_mfma_f32_16x16x32_bf16 v[22:25], v[154:157], v[186:189], v[22:25]
	v_mfma_f32_16x16x32_bf16 v[14:17], v[162:165], v[186:189], v[14:17]
	v_mfma_f32_16x16x32_bf16 v[6:9], v[154:157], v[198:201], v[6:9]
	v_mfma_f32_16x16x32_bf16 v[2:5], v[162:165], v[198:201], v[2:5]
	v_mfma_f32_16x16x32_bf16 v[54:57], v[158:161], v[174:177], v[54:57]
	v_mfma_f32_16x16x32_bf16 v[46:49], v[166:169], v[174:177], v[46:49]
	v_mfma_f32_16x16x32_bf16 v[38:41], v[158:161], v[182:185], v[38:41]
	v_mfma_f32_16x16x32_bf16 v[30:33], v[166:169], v[182:185], v[30:33]
	v_mfma_f32_16x16x32_bf16 v[22:25], v[158:161], v[194:197], v[22:25]
	v_mfma_f32_16x16x32_bf16 v[14:17], v[166:169], v[194:197], v[14:17]
	v_mfma_f32_16x16x32_bf16 v[6:9], v[158:161], v[202:205], v[6:9]
	v_mfma_f32_16x16x32_bf16 v[2:5], v[166:169], v[202:205], v[2:5]
	s_barrier
	s_setprio 0
	s_add_i32 s46, s69, s14
	s_mov_b32 m0, s46
	ds_read_b128 v[170:173], v136 offset:16384
	ds_read_b128 v[174:177], v136 offset:17408
	ds_read_b128 v[178:181], v136 offset:18432
	ds_read_b128 v[182:185], v136 offset:19456
	ds_read_b128 v[186:189], v136 offset:20480
	ds_read_b128 v[194:197], v136 offset:21504
	ds_read_b128 v[198:201], v136 offset:22528
	ds_read_b128 v[202:205], v136 offset:23552
	s_nop 0
	global_load_lds_dwordx4 v135, s[52:53]
	s_add_i32 m0, s46, 0x2000
	s_add_u32 s46, s52, 0x4000
	s_addc_u32 s47, s53, 0
	s_add_i32 s69, s70, s14
	s_nop 0
	global_load_lds_dwordx4 v134, s[52:53]
	s_mov_b32 m0, s69
	s_nop 0
	global_load_lds_dwordx4 v135, s[46:47]
	s_add_i32 m0, s69, 0x2000
	s_nop 0
	global_load_lds_dwordx4 v134, s[46:47]
	s_mov_b32 m0, s15
	s_nop 0
	global_load_lds_dwordx4 v0, s[50:51]
	s_mov_b32 m0, s18
	s_nop 0
	global_load_lds_dwordx4 v130, s[50:51]
	s_waitcnt vmcnt(8)
	s_waitcnt lgkmcnt(0)
	s_setprio 1
	s_barrier
	s_waitcnt lgkmcnt(0)
	v_mfma_f32_16x16x32_bf16 v[122:125], v[138:141], v[170:173], v[122:125]
	v_mfma_f32_16x16x32_bf16 v[114:117], v[146:149], v[170:173], v[114:117]
	v_mfma_f32_16x16x32_bf16 v[106:109], v[138:141], v[178:181], v[106:109]
	v_mfma_f32_16x16x32_bf16 v[98:101], v[146:149], v[178:181], v[98:101]
	v_mfma_f32_16x16x32_bf16 v[90:93], v[138:141], v[186:189], v[90:93]
	v_mfma_f32_16x16x32_bf16 v[82:85], v[146:149], v[186:189], v[82:85]
	v_mfma_f32_16x16x32_bf16 v[74:77], v[138:141], v[198:201], v[74:77]
	v_mfma_f32_16x16x32_bf16 v[66:69], v[146:149], v[198:201], v[66:69]
	v_mfma_f32_16x16x32_bf16 v[122:125], v[142:145], v[174:177], v[122:125]
	v_mfma_f32_16x16x32_bf16 v[114:117], v[150:153], v[174:177], v[114:117]
	v_mfma_f32_16x16x32_bf16 v[106:109], v[142:145], v[182:185], v[106:109]
	v_mfma_f32_16x16x32_bf16 v[98:101], v[150:153], v[182:185], v[98:101]
	v_mfma_f32_16x16x32_bf16 v[90:93], v[142:145], v[194:197], v[90:93]
	v_mfma_f32_16x16x32_bf16 v[82:85], v[150:153], v[194:197], v[82:85]
	v_mfma_f32_16x16x32_bf16 v[74:77], v[142:145], v[202:205], v[74:77]
	v_mfma_f32_16x16x32_bf16 v[66:69], v[150:153], v[202:205], v[66:69]
	v_mfma_f32_16x16x32_bf16 v[50:53], v[154:157], v[170:173], v[50:53]
	v_mfma_f32_16x16x32_bf16 v[42:45], v[162:165], v[170:173], v[42:45]
	v_mfma_f32_16x16x32_bf16 v[34:37], v[154:157], v[178:181], v[34:37]
	v_mfma_f32_16x16x32_bf16 v[26:29], v[162:165], v[178:181], v[26:29]
	v_mfma_f32_16x16x32_bf16 v[18:21], v[154:157], v[186:189], v[18:21]
	v_mfma_f32_16x16x32_bf16 v[10:13], v[162:165], v[186:189], v[10:13]
	v_mfma_f32_16x16x32_bf16 v[58:61], v[154:157], v[198:201], v[58:61]
	v_mfma_f32_16x16x32_bf16 v[62:65], v[162:165], v[198:201], v[62:65]
	v_mfma_f32_16x16x32_bf16 v[50:53], v[158:161], v[174:177], v[50:53]
	v_mfma_f32_16x16x32_bf16 v[42:45], v[166:169], v[174:177], v[42:45]
	v_mfma_f32_16x16x32_bf16 v[34:37], v[158:161], v[182:185], v[34:37]
	v_mfma_f32_16x16x32_bf16 v[26:29], v[166:169], v[182:185], v[26:29]
	v_mfma_f32_16x16x32_bf16 v[18:21], v[158:161], v[194:197], v[18:21]
	v_mfma_f32_16x16x32_bf16 v[10:13], v[166:169], v[194:197], v[10:13]
	v_mfma_f32_16x16x32_bf16 v[58:61], v[158:161], v[202:205], v[58:61]
	v_mfma_f32_16x16x32_bf16 v[62:65], v[166:169], v[202:205], v[62:65]
	s_barrier
	s_setprio 0
	s_add_i32 s69, 0, 0x18000
	v_add_u32_e32 v131, s69, v133
	s_add_i32 s70, 0, 0x1c000
	ds_read_b128 v[138:141], v131
	ds_read_b128 v[142:145], v131 offset:1024
	ds_read_b128 v[146:149], v131 offset:2048
	ds_read_b128 v[150:153], v131 offset:3072
	v_add_u32_e32 v131, s70, v133
	ds_read_b128 v[154:157], v131
	ds_read_b128 v[158:161], v131 offset:1024
	ds_read_b128 v[162:165], v131 offset:2048
	ds_read_b128 v[166:169], v131 offset:3072
	s_add_u32 s46, s50, s26
	s_addc_u32 s47, s51, s27
	s_mov_b32 m0, s20
	ds_read_b128 v[170:173], v136 offset:32768
	ds_read_b128 v[174:177], v136 offset:33792
	ds_read_b128 v[178:181], v136 offset:34816
	ds_read_b128 v[182:185], v136 offset:35840
	ds_read_b128 v[186:189], v136 offset:36864
	ds_read_b128 v[194:197], v136 offset:37888
	ds_read_b128 v[198:201], v136 offset:38912
	ds_read_b128 v[202:205], v136 offset:39936
	s_nop 0
	global_load_lds_dwordx4 v0, s[46:47]
	s_mov_b32 m0, s21
	s_nop 0
	global_load_lds_dwordx4 v130, s[46:47]
	s_waitcnt vmcnt(8)
	s_waitcnt lgkmcnt(0)
	s_setprio 1
	s_barrier
	s_waitcnt lgkmcnt(0)
	v_mfma_f32_16x16x32_bf16 v[126:129], v[138:141], v[170:173], v[126:129]
	v_mfma_f32_16x16x32_bf16 v[118:121], v[146:149], v[170:173], v[118:121]
	v_mfma_f32_16x16x32_bf16 v[110:113], v[138:141], v[178:181], v[110:113]
	v_mfma_f32_16x16x32_bf16 v[102:105], v[146:149], v[178:181], v[102:105]
	v_mfma_f32_16x16x32_bf16 v[94:97], v[138:141], v[186:189], v[94:97]
	v_mfma_f32_16x16x32_bf16 v[86:89], v[146:149], v[186:189], v[86:89]
	v_mfma_f32_16x16x32_bf16 v[78:81], v[138:141], v[198:201], v[78:81]
	v_mfma_f32_16x16x32_bf16 v[70:73], v[146:149], v[198:201], v[70:73]
	v_mfma_f32_16x16x32_bf16 v[126:129], v[142:145], v[174:177], v[126:129]
	v_mfma_f32_16x16x32_bf16 v[118:121], v[150:153], v[174:177], v[118:121]
	v_mfma_f32_16x16x32_bf16 v[110:113], v[142:145], v[182:185], v[110:113]
	v_mfma_f32_16x16x32_bf16 v[102:105], v[150:153], v[182:185], v[102:105]
	v_mfma_f32_16x16x32_bf16 v[94:97], v[142:145], v[194:197], v[94:97]
	v_mfma_f32_16x16x32_bf16 v[86:89], v[150:153], v[194:197], v[86:89]
	v_mfma_f32_16x16x32_bf16 v[78:81], v[142:145], v[202:205], v[78:81]
	v_mfma_f32_16x16x32_bf16 v[70:73], v[150:153], v[202:205], v[70:73]
	v_mfma_f32_16x16x32_bf16 v[54:57], v[154:157], v[170:173], v[54:57]
	v_mfma_f32_16x16x32_bf16 v[46:49], v[162:165], v[170:173], v[46:49]
	v_mfma_f32_16x16x32_bf16 v[38:41], v[154:157], v[178:181], v[38:41]
	v_mfma_f32_16x16x32_bf16 v[30:33], v[162:165], v[178:181], v[30:33]
	v_mfma_f32_16x16x32_bf16 v[22:25], v[154:157], v[186:189], v[22:25]
	v_mfma_f32_16x16x32_bf16 v[14:17], v[162:165], v[186:189], v[14:17]
	v_mfma_f32_16x16x32_bf16 v[6:9], v[154:157], v[198:201], v[6:9]
	v_mfma_f32_16x16x32_bf16 v[2:5], v[162:165], v[198:201], v[2:5]
	v_mfma_f32_16x16x32_bf16 v[54:57], v[158:161], v[174:177], v[54:57]
	v_mfma_f32_16x16x32_bf16 v[46:49], v[166:169], v[174:177], v[46:49]
	v_mfma_f32_16x16x32_bf16 v[38:41], v[158:161], v[182:185], v[38:41]
	v_mfma_f32_16x16x32_bf16 v[30:33], v[166:169], v[182:185], v[30:33]
	v_mfma_f32_16x16x32_bf16 v[22:25], v[158:161], v[194:197], v[22:25]
	v_mfma_f32_16x16x32_bf16 v[14:17], v[166:169], v[194:197], v[14:17]
	v_mfma_f32_16x16x32_bf16 v[6:9], v[158:161], v[202:205], v[6:9]
	v_mfma_f32_16x16x32_bf16 v[2:5], v[166:169], v[202:205], v[2:5]
	s_barrier
	s_setprio 0
	s_add_u32 s46, s52, 0x8000
	s_addc_u32 s47, s53, 0
	s_add_i32 s69, s69, s14
	s_mov_b32 m0, s69
	ds_read_b128 v[170:173], v136 offset:49152
	ds_read_b128 v[174:177], v136 offset:50176
	ds_read_b128 v[178:181], v136 offset:51200
	ds_read_b128 v[182:185], v136 offset:52224
	ds_read_b128 v[186:189], v136 offset:53248
	ds_read_b128 v[194:197], v136 offset:54272
	ds_read_b128 v[198:201], v136 offset:55296
	ds_read_b128 v[202:205], v136 offset:56320
	v_mov_b32_e32 v131, v1
	global_load_lds_dwordx4 v135, s[46:47]
	s_add_i32 m0, s69, 0x2000
	s_nop 0
	global_load_lds_dwordx4 v134, s[46:47]
	s_add_u32 s46, s52, 0xc000
	s_addc_u32 s47, s53, 0
	s_add_i32 s52, s70, s14
	s_mov_b32 m0, s52
	s_nop 0
	global_load_lds_dwordx4 v135, s[46:47]
	s_add_i32 m0, s52, 0x2000
	s_nop 0
	global_load_lds_dwordx4 v134, s[46:47]
	s_mov_b32 m0, s58
	v_lshl_add_u64 v[190:191], s[50:51], 0, v[0:1]
	v_lshl_add_u64 v[190:191], v[190:191], 0, s[16:17]
	global_load_lds_dwordx4 v[190:191], off
	s_mov_b32 m0, s59
	v_lshl_add_u64 v[190:191], s[50:51], 0, v[130:131]
	v_lshl_add_u64 v[190:191], v[190:191], 0, s[16:17]
	global_load_lds_dwordx4 v[190:191], off
	s_waitcnt vmcnt(8)
	s_waitcnt lgkmcnt(0)
	s_setprio 1
	s_barrier
	s_waitcnt lgkmcnt(0)
	v_mfma_f32_16x16x32_bf16 v[122:125], v[138:141], v[170:173], v[122:125]
	v_mfma_f32_16x16x32_bf16 v[114:117], v[146:149], v[170:173], v[114:117]
	v_mfma_f32_16x16x32_bf16 v[106:109], v[138:141], v[178:181], v[106:109]
	v_mfma_f32_16x16x32_bf16 v[98:101], v[146:149], v[178:181], v[98:101]
	v_mfma_f32_16x16x32_bf16 v[90:93], v[138:141], v[186:189], v[90:93]
	v_mfma_f32_16x16x32_bf16 v[82:85], v[146:149], v[186:189], v[82:85]
	v_mfma_f32_16x16x32_bf16 v[74:77], v[138:141], v[198:201], v[74:77]
	v_mfma_f32_16x16x32_bf16 v[66:69], v[146:149], v[198:201], v[66:69]
	v_mfma_f32_16x16x32_bf16 v[122:125], v[142:145], v[174:177], v[122:125]
	v_mfma_f32_16x16x32_bf16 v[114:117], v[150:153], v[174:177], v[114:117]
	v_mfma_f32_16x16x32_bf16 v[106:109], v[142:145], v[182:185], v[106:109]
	v_mfma_f32_16x16x32_bf16 v[98:101], v[150:153], v[182:185], v[98:101]
	v_mfma_f32_16x16x32_bf16 v[90:93], v[142:145], v[194:197], v[90:93]
	v_mfma_f32_16x16x32_bf16 v[82:85], v[150:153], v[194:197], v[82:85]
	v_mfma_f32_16x16x32_bf16 v[74:77], v[142:145], v[202:205], v[74:77]
	v_mfma_f32_16x16x32_bf16 v[66:69], v[150:153], v[202:205], v[66:69]
	v_mfma_f32_16x16x32_bf16 v[50:53], v[154:157], v[170:173], v[50:53]
	v_mfma_f32_16x16x32_bf16 v[42:45], v[162:165], v[170:173], v[42:45]
	v_mfma_f32_16x16x32_bf16 v[34:37], v[154:157], v[178:181], v[34:37]
	v_mfma_f32_16x16x32_bf16 v[26:29], v[162:165], v[178:181], v[26:29]
	v_mfma_f32_16x16x32_bf16 v[18:21], v[154:157], v[186:189], v[18:21]
	v_mfma_f32_16x16x32_bf16 v[10:13], v[162:165], v[186:189], v[10:13]
	v_mfma_f32_16x16x32_bf16 v[58:61], v[154:157], v[198:201], v[58:61]
	v_mfma_f32_16x16x32_bf16 v[62:65], v[162:165], v[198:201], v[62:65]
	v_mfma_f32_16x16x32_bf16 v[50:53], v[158:161], v[174:177], v[50:53]
	v_mfma_f32_16x16x32_bf16 v[42:45], v[166:169], v[174:177], v[42:45]
	v_mfma_f32_16x16x32_bf16 v[34:37], v[158:161], v[182:185], v[34:37]
	v_mfma_f32_16x16x32_bf16 v[26:29], v[166:169], v[182:185], v[26:29]
	v_mfma_f32_16x16x32_bf16 v[18:21], v[158:161], v[194:197], v[18:21]
	v_mfma_f32_16x16x32_bf16 v[10:13], v[166:169], v[194:197], v[10:13]
	v_mfma_f32_16x16x32_bf16 v[58:61], v[158:161], v[202:205], v[58:61]
	v_mfma_f32_16x16x32_bf16 v[62:65], v[166:169], v[202:205], v[62:65]
	s_barrier
	s_setprio 0
	s_add_u32 s45, s45, 0x10000
	s_addc_u32 s67, s67, 0
	s_cmp_ge_i32 s68, s55
	s_mov_b64 s[46:47], s[48:49]
	s_mov_b32 s50, s68
	s_cbranch_scc0 .LBB0_306

.LBB0_379:
	s_add_u32 s34, s26, 0x10000
	s_addc_u32 s35, s27, 0
	s_and_b64 s[30:31], s[46:47], exec
	s_cselect_b32 s53, s43, s35
	s_cselect_b32 s52, s42, s34
	s_add_u32 s65, s28, 0x10000
	s_addc_u32 s66, s29, 0
	s_add_u32 s30, s52, 0x8000
	s_addc_u32 s31, s53, 0
	s_add_i32 s67, 0, 0x10000
	s_and_b64 s[34:35], s[46:47], exec
	s_cselect_b32 s35, s45, s66
	s_cselect_b32 s34, s44, s65
	s_add_i32 s70, 0, 0x14000
	v_add_u32_e32 v114, s67, v236
	v_add_u32_e32 v115, s70, v236
	ds_read_b128 v[2:5], v114
	s_waitcnt lgkmcnt(0)
	ds_read_b128 v[6:9], v114 offset:1024
	ds_read_b128 v[10:13], v114 offset:2048
	ds_read_b128 v[14:17], v114 offset:3072
	ds_read_b128 v[18:21], v115
	ds_read_b128 v[22:25], v115 offset:1024
	ds_read_b128 v[26:29], v115 offset:2048
	ds_read_b128 v[30:33], v115 offset:3072
	s_add_u32 s68, s26, 0xc000
	s_addc_u32 s69, s27, 0
	s_add_i32 s65, s20, 0xc000
	s_mov_b32 m0, s65
	s_add_i32 s66, s20, 0xe000
	ds_read_b128 v[34:37], v237
	ds_read_b128 v[38:41], v237 offset:1024
	ds_read_b128 v[42:45], v237 offset:2048
	ds_read_b128 v[46:49], v237 offset:3072
	ds_read_b128 v[50:53], v237 offset:4096
	ds_read_b128 v[54:57], v237 offset:5120
	ds_read_b128 v[58:61], v237 offset:6144
	ds_read_b128 v[62:65], v237 offset:7168
	s_nop 0
	global_load_lds_dwordx4 v235, s[68:69]
	s_mov_b32 m0, s66
	s_nop 0
	global_load_lds_dwordx4 v226, s[68:69]
	s_waitcnt vmcnt(8)
	s_waitcnt lgkmcnt(0)
	s_setprio 1
	s_barrier
	s_waitcnt lgkmcnt(0)
	v_mfma_f32_16x16x32_bf16 v[90:93], v[2:5], v[58:61], 0
	v_mfma_f32_16x16x32_bf16 v[66:69], v[2:5], v[34:37], 0
	v_mfma_f32_16x16x32_bf16 v[70:73], v[10:13], v[34:37], 0
	v_mfma_f32_16x16x32_bf16 v[74:77], v[2:5], v[42:45], 0
	v_mfma_f32_16x16x32_bf16 v[78:81], v[10:13], v[42:45], 0
	v_mfma_f32_16x16x32_bf16 v[82:85], v[2:5], v[50:53], 0
	v_mfma_f32_16x16x32_bf16 v[86:89], v[10:13], v[50:53], 0
	v_mfma_f32_16x16x32_bf16 v[98:101], v[6:9], v[62:65], v[90:93]
	v_mfma_f32_16x16x32_bf16 v[90:93], v[10:13], v[58:61], 0
	v_mfma_f32_16x16x32_bf16 v[66:69], v[6:9], v[38:41], v[66:69]
	v_mfma_f32_16x16x32_bf16 v[70:73], v[14:17], v[38:41], v[70:73]
	v_mfma_f32_16x16x32_bf16 v[74:77], v[6:9], v[46:49], v[74:77]
	v_mfma_f32_16x16x32_bf16 v[78:81], v[14:17], v[46:49], v[78:81]
	v_mfma_f32_16x16x32_bf16 v[82:85], v[6:9], v[54:57], v[82:85]
	v_mfma_f32_16x16x32_bf16 v[86:89], v[14:17], v[54:57], v[86:89]
	v_mfma_f32_16x16x32_bf16 v[102:105], v[14:17], v[62:65], v[90:93]
	v_mfma_f32_16x16x32_bf16 v[90:93], v[18:21], v[34:37], 0
	v_mfma_f32_16x16x32_bf16 v[34:37], v[26:29], v[34:37], 0
	v_mfma_f32_16x16x32_bf16 v[118:121], v[22:25], v[38:41], v[90:93]
	v_mfma_f32_16x16x32_bf16 v[34:37], v[30:33], v[38:41], v[34:37]
	v_mfma_f32_16x16x32_bf16 v[38:41], v[18:21], v[42:45], 0
	v_mfma_f32_16x16x32_bf16 v[42:45], v[26:29], v[42:45], 0
	v_mfma_f32_16x16x32_bf16 v[38:41], v[22:25], v[46:49], v[38:41]
	v_mfma_f32_16x16x32_bf16 v[42:45], v[30:33], v[46:49], v[42:45]
	v_mfma_f32_16x16x32_bf16 v[46:49], v[18:21], v[50:53], 0
	v_mfma_f32_16x16x32_bf16 v[50:53], v[26:29], v[50:53], 0
	v_mfma_f32_16x16x32_bf16 v[46:49], v[22:25], v[54:57], v[46:49]
	v_mfma_f32_16x16x32_bf16 v[50:53], v[30:33], v[54:57], v[50:53]
	v_mfma_f32_16x16x32_bf16 v[54:57], v[18:21], v[58:61], 0
	v_mfma_f32_16x16x32_bf16 v[58:61], v[26:29], v[58:61], 0
	v_mfma_f32_16x16x32_bf16 v[54:57], v[22:25], v[62:65], v[54:57]
	v_mfma_f32_16x16x32_bf16 v[58:61], v[30:33], v[62:65], v[58:61]
	s_barrier
	s_setprio 0
	s_add_i32 s67, s67, s18
	s_add_i32 s68, s67, 0x2000
	s_mov_b32 m0, s67
	s_add_u32 s72, s34, 0x4000
	ds_read_b128 v[62:65], v237 offset:16384
	ds_read_b128 v[90:93], v237 offset:17408
	ds_read_b128 v[94:97], v237 offset:18432
	ds_read_b128 v[106:109], v237 offset:19456
	ds_read_b128 v[110:113], v237 offset:20480
	ds_read_b128 v[122:125], v237 offset:21504
	ds_read_b128 v[126:129], v237 offset:22528
	ds_read_b128 v[130:133], v237 offset:23552
	s_addc_u32 s73, s35, 0
	global_load_lds_dwordx4 v227, s[34:35]
	s_mov_b32 m0, s68
	s_add_i32 s69, s70, s18
	s_add_i32 s70, s69, 0x2000
	global_load_lds_dwordx4 v0, s[34:35]
	s_mov_b32 m0, s69
	s_nop 0
	global_load_lds_dwordx4 v227, s[72:73]
	s_mov_b32 m0, s70
	s_nop 0
	global_load_lds_dwordx4 v0, s[72:73]
	s_mov_b32 m0, s20
	s_nop 0
	global_load_lds_dwordx4 v235, s[52:53]
	s_mov_b32 m0, s25
	s_nop 0
	global_load_lds_dwordx4 v226, s[52:53]
	s_waitcnt vmcnt(8)
	s_waitcnt lgkmcnt(0)
	s_setprio 1
	s_barrier
	s_waitcnt lgkmcnt(0)
	v_mfma_f32_16x16x32_bf16 v[134:137], v[2:5], v[62:65], 0
	v_mfma_f32_16x16x32_bf16 v[142:145], v[2:5], v[94:97], 0
	v_mfma_f32_16x16x32_bf16 v[150:153], v[2:5], v[110:113], 0
	v_mfma_f32_16x16x32_bf16 v[2:5], v[2:5], v[126:129], 0
	v_mfma_f32_16x16x32_bf16 v[134:137], v[6:9], v[90:93], v[134:137]
	v_mfma_f32_16x16x32_bf16 v[142:145], v[6:9], v[106:109], v[142:145]
	v_mfma_f32_16x16x32_bf16 v[150:153], v[6:9], v[122:125], v[150:153]
	v_mfma_f32_16x16x32_bf16 v[2:5], v[6:9], v[130:133], v[2:5]
	v_mfma_f32_16x16x32_bf16 v[6:9], v[10:13], v[126:129], 0
	v_mfma_f32_16x16x32_bf16 v[138:141], v[10:13], v[62:65], 0
	v_mfma_f32_16x16x32_bf16 v[146:149], v[10:13], v[94:97], 0
	v_mfma_f32_16x16x32_bf16 v[154:157], v[10:13], v[110:113], 0
	v_mfma_f32_16x16x32_bf16 v[6:9], v[14:17], v[130:133], v[6:9]
	v_mfma_f32_16x16x32_bf16 v[138:141], v[14:17], v[90:93], v[138:141]
	v_mfma_f32_16x16x32_bf16 v[146:149], v[14:17], v[106:109], v[146:149]
	v_mfma_f32_16x16x32_bf16 v[154:157], v[14:17], v[122:125], v[154:157]
	v_mfma_f32_16x16x32_bf16 v[10:13], v[18:21], v[62:65], 0
	v_mfma_f32_16x16x32_bf16 v[158:161], v[22:25], v[90:93], v[10:13]
	v_mfma_f32_16x16x32_bf16 v[10:13], v[26:29], v[62:65], 0
	v_mfma_f32_16x16x32_bf16 v[162:165], v[30:33], v[90:93], v[10:13]
	v_mfma_f32_16x16x32_bf16 v[10:13], v[18:21], v[94:97], 0
	v_mfma_f32_16x16x32_bf16 v[174:177], v[22:25], v[106:109], v[10:13]
	v_mfma_f32_16x16x32_bf16 v[10:13], v[26:29], v[94:97], 0
	v_mfma_f32_16x16x32_bf16 v[178:181], v[30:33], v[106:109], v[10:13]
	v_mfma_f32_16x16x32_bf16 v[10:13], v[18:21], v[110:113], 0
	v_mfma_f32_16x16x32_bf16 v[182:185], v[22:25], v[122:125], v[10:13]
	v_mfma_f32_16x16x32_bf16 v[10:13], v[26:29], v[110:113], 0
	v_mfma_f32_16x16x32_bf16 v[122:125], v[30:33], v[122:125], v[10:13]
	v_mfma_f32_16x16x32_bf16 v[10:13], v[18:21], v[126:129], 0
	v_mfma_f32_16x16x32_bf16 v[186:189], v[22:25], v[130:133], v[10:13]
	v_mfma_f32_16x16x32_bf16 v[10:13], v[26:29], v[126:129], 0
	v_mfma_f32_16x16x32_bf16 v[130:133], v[30:33], v[130:133], v[10:13]
	s_barrier
	s_setprio 0
	s_add_i32 s71, 0, 0x18000
	s_add_i32 s74, 0, 0x1c000
	v_add_u32_e32 v116, s71, v236
	v_add_u32_e32 v117, s74, v236
	s_nop 0
	ds_read_b128 v[10:13], v116
	ds_read_b128 v[14:17], v116 offset:1024
	ds_read_b128 v[18:21], v116 offset:2048
	ds_read_b128 v[22:25], v116 offset:3072
	ds_read_b128 v[194:197], v117
	ds_read_b128 v[198:201], v117 offset:1024
	ds_read_b128 v[202:205], v117 offset:2048
	ds_read_b128 v[206:209], v117 offset:3072
	s_add_u32 s52, s52, 0x4000
	s_addc_u32 s53, s53, 0
	s_mov_b32 m0, s54
	ds_read_b128 v[26:29], v237 offset:32768
	ds_read_b128 v[30:33], v237 offset:33792
	ds_read_b128 v[62:65], v237 offset:34816
	ds_read_b128 v[210:213], v237 offset:35840
	ds_read_b128 v[214:217], v237 offset:36864
	ds_read_b128 v[218:221], v237 offset:37888
	ds_read_b128 v[222:225], v237 offset:38912
	ds_read_b128 v[238:241], v237 offset:39936
	s_nop 0
	global_load_lds_dwordx4 v235, s[52:53]
	s_mov_b32 m0, s55
	s_nop 0
	global_load_lds_dwordx4 v226, s[52:53]
	s_waitcnt vmcnt(8)
	s_waitcnt lgkmcnt(0)
	s_setprio 1
	s_barrier
	s_waitcnt lgkmcnt(0)
	v_mfma_f32_16x16x32_bf16 v[66:69], v[10:13], v[26:29], v[66:69]
	v_mfma_f32_16x16x32_bf16 v[166:169], v[14:17], v[30:33], v[66:69]
	v_mfma_f32_16x16x32_bf16 v[66:69], v[18:21], v[26:29], v[70:73]
	v_mfma_f32_16x16x32_bf16 v[170:173], v[22:25], v[30:33], v[66:69]
	v_mfma_f32_16x16x32_bf16 v[66:69], v[10:13], v[62:65], v[74:77]
	v_mfma_f32_16x16x32_bf16 v[110:113], v[14:17], v[210:213], v[66:69]
	v_mfma_f32_16x16x32_bf16 v[66:69], v[18:21], v[62:65], v[78:81]
	v_mfma_f32_16x16x32_bf16 v[106:109], v[22:25], v[210:213], v[66:69]
	v_mfma_f32_16x16x32_bf16 v[66:69], v[10:13], v[214:217], v[82:85]
	v_mfma_f32_16x16x32_bf16 v[94:97], v[14:17], v[218:221], v[66:69]
	v_mfma_f32_16x16x32_bf16 v[66:69], v[18:21], v[214:217], v[86:89]
	v_mfma_f32_16x16x32_bf16 v[90:93], v[22:25], v[218:221], v[66:69]
	v_mfma_f32_16x16x32_bf16 v[66:69], v[10:13], v[222:225], v[98:101]
	v_mfma_f32_16x16x32_bf16 v[78:81], v[14:17], v[238:241], v[66:69]
	v_mfma_f32_16x16x32_bf16 v[66:69], v[18:21], v[222:225], v[102:105]
	v_mfma_f32_16x16x32_bf16 v[70:73], v[22:25], v[238:241], v[66:69]
	v_mfma_f32_16x16x32_bf16 v[66:69], v[194:197], v[26:29], v[118:121]
	v_mfma_f32_16x16x32_bf16 v[26:29], v[202:205], v[26:29], v[34:37]
	v_mfma_f32_16x16x32_bf16 v[118:121], v[206:209], v[30:33], v[26:29]
	v_mfma_f32_16x16x32_bf16 v[26:29], v[194:197], v[62:65], v[38:41]
	v_mfma_f32_16x16x32_bf16 v[102:105], v[198:201], v[210:213], v[26:29]
	v_mfma_f32_16x16x32_bf16 v[26:29], v[202:205], v[62:65], v[42:45]
	v_mfma_f32_16x16x32_bf16 v[98:101], v[206:209], v[210:213], v[26:29]
	v_mfma_f32_16x16x32_bf16 v[26:29], v[194:197], v[214:217], v[46:49]
	v_mfma_f32_16x16x32_bf16 v[86:89], v[198:201], v[218:221], v[26:29]
	v_mfma_f32_16x16x32_bf16 v[26:29], v[202:205], v[214:217], v[50:53]
	v_mfma_f32_16x16x32_bf16 v[82:85], v[206:209], v[218:221], v[26:29]
	v_mfma_f32_16x16x32_bf16 v[26:29], v[194:197], v[222:225], v[54:57]
	v_mfma_f32_16x16x32_bf16 v[62:65], v[198:201], v[238:241], v[26:29]
	v_mfma_f32_16x16x32_bf16 v[26:29], v[202:205], v[222:225], v[58:61]
	v_mfma_f32_16x16x32_bf16 v[126:129], v[198:201], v[30:33], v[66:69]
	v_mfma_f32_16x16x32_bf16 v[54:57], v[206:209], v[238:241], v[26:29]
	s_barrier
	s_setprio 0
	s_add_u32 s72, s34, 0x8000
	s_addc_u32 s73, s35, 0
	s_add_i32 s52, s71, s18
	s_add_i32 s53, s52, 0x2000
	s_mov_b32 m0, s52
	s_add_u32 s34, s34, 0xc000
	ds_read_b128 v[34:37], v237 offset:49152
	ds_read_b128 v[38:41], v237 offset:50176
	ds_read_b128 v[210:213], v237 offset:51200
	ds_read_b128 v[214:217], v237 offset:52224
	ds_read_b128 v[218:221], v237 offset:53248
	ds_read_b128 v[222:225], v237 offset:54272
	ds_read_b128 v[238:241], v237 offset:55296
	ds_read_b128 v[242:245], v237 offset:56320
	s_addc_u32 s35, s35, 0
	global_load_lds_dwordx4 v227, s[72:73]
	s_mov_b32 m0, s53
	s_add_i32 s71, s74, s18
	s_nop 0
	global_load_lds_dwordx4 v0, s[72:73]
	s_mov_b32 m0, s71
	s_add_i32 s72, s71, 0x2000
	s_nop 0
	global_load_lds_dwordx4 v227, s[34:35]
	s_mov_b32 m0, s72
	s_nop 0
	global_load_lds_dwordx4 v0, s[34:35]
	s_mov_b32 m0, s58
	s_nop 0
	global_load_lds_dwordx4 v235, s[30:31]
	s_mov_b32 m0, s59
	s_nop 0
	global_load_lds_dwordx4 v226, s[30:31]
	s_waitcnt vmcnt(8)
	s_waitcnt lgkmcnt(0)
	s_setprio 1
	s_barrier
	s_waitcnt lgkmcnt(0)
	v_mfma_f32_16x16x32_bf16 v[26:29], v[10:13], v[34:37], v[134:137]
	v_mfma_f32_16x16x32_bf16 v[74:77], v[14:17], v[38:41], v[26:29]
	v_mfma_f32_16x16x32_bf16 v[26:29], v[18:21], v[34:37], v[138:141]
	v_mfma_f32_16x16x32_bf16 v[66:69], v[22:25], v[38:41], v[26:29]
	v_mfma_f32_16x16x32_bf16 v[26:29], v[10:13], v[210:213], v[142:145]
	v_mfma_f32_16x16x32_bf16 v[46:49], v[14:17], v[214:217], v[26:29]
	v_mfma_f32_16x16x32_bf16 v[26:29], v[18:21], v[210:213], v[146:149]
	v_mfma_f32_16x16x32_bf16 v[42:45], v[22:25], v[214:217], v[26:29]
	v_mfma_f32_16x16x32_bf16 v[26:29], v[10:13], v[218:221], v[150:153]
	v_mfma_f32_16x16x32_bf16 v[2:5], v[10:13], v[238:241], v[2:5]
	v_mfma_f32_16x16x32_bf16 v[30:33], v[14:17], v[222:225], v[26:29]
	v_mfma_f32_16x16x32_bf16 v[26:29], v[18:21], v[218:221], v[154:157]
	v_mfma_f32_16x16x32_bf16 v[14:17], v[14:17], v[242:245], v[2:5]
	v_mfma_f32_16x16x32_bf16 v[2:5], v[18:21], v[238:241], v[6:9]
	v_mfma_f32_16x16x32_bf16 v[26:29], v[22:25], v[222:225], v[26:29]
	v_mfma_f32_16x16x32_bf16 v[10:13], v[22:25], v[242:245], v[2:5]
	v_mfma_f32_16x16x32_bf16 v[2:5], v[194:197], v[34:37], v[158:161]
	v_mfma_f32_16x16x32_bf16 v[58:61], v[198:201], v[38:41], v[2:5]
	v_mfma_f32_16x16x32_bf16 v[2:5], v[202:205], v[34:37], v[162:165]
	v_mfma_f32_16x16x32_bf16 v[50:53], v[206:209], v[38:41], v[2:5]
	v_mfma_f32_16x16x32_bf16 v[2:5], v[194:197], v[210:213], v[174:177]
	v_mfma_f32_16x16x32_bf16 v[38:41], v[198:201], v[214:217], v[2:5]
	v_mfma_f32_16x16x32_bf16 v[2:5], v[202:205], v[210:213], v[178:181]
	v_mfma_f32_16x16x32_bf16 v[34:37], v[206:209], v[214:217], v[2:5]
	v_mfma_f32_16x16x32_bf16 v[2:5], v[194:197], v[218:221], v[182:185]
	v_mfma_f32_16x16x32_bf16 v[22:25], v[198:201], v[222:225], v[2:5]
	v_mfma_f32_16x16x32_bf16 v[2:5], v[202:205], v[218:221], v[122:125]
	v_mfma_f32_16x16x32_bf16 v[18:21], v[206:209], v[222:225], v[2:5]
	v_mfma_f32_16x16x32_bf16 v[2:5], v[194:197], v[238:241], v[186:189]
	v_mfma_f32_16x16x32_bf16 v[6:9], v[198:201], v[242:245], v[2:5]
	v_mfma_f32_16x16x32_bf16 v[2:5], v[202:205], v[238:241], v[130:133]
	v_mfma_f32_16x16x32_bf16 v[2:5], v[206:209], v[242:245], v[2:5]
	s_barrier
	s_setprio 0
	s_andn2_b64 vcc, exec, s[48:49]
	s_cbranch_vccnz .LBB0_382
	s_add_u32 s73, s28, 0x20000
	s_addc_u32 s74, s29, 0
	s_add_u32 s26, s26, 0x1c000
	s_addc_u32 s27, s27, 0
	s_mov_b32 s75, 4
.LBB0_381:
	ds_read_b128 v[122:125], v114
	ds_read_b128 v[130:133], v114 offset:1024
	ds_read_b128 v[134:137], v114 offset:2048
	ds_read_b128 v[138:141], v114 offset:3072
	ds_read_b128 v[142:145], v115
	ds_read_b128 v[146:149], v115 offset:1024
	ds_read_b128 v[150:153], v115 offset:2048
	ds_read_b128 v[154:157], v115 offset:3072
	s_add_u32 s28, s26, 0x4000
	s_addc_u32 s29, s27, 0
	s_cmp_eq_u32 s56, s75
	s_cselect_b32 s34, s42, s28
	s_cselect_b32 s35, s43, s29
	s_cselect_b32 s30, s44, s73
	s_cselect_b32 s31, s45, s74
	s_add_u32 s28, s34, 0x8000
	s_addc_u32 s29, s35, 0
	s_mov_b32 m0, s65
	ds_read_b128 v[158:161], v237
	ds_read_b128 v[162:165], v237 offset:1024
	ds_read_b128 v[174:177], v237 offset:2048
	ds_read_b128 v[178:181], v237 offset:3072
	ds_read_b128 v[182:185], v237 offset:4096
	ds_read_b128 v[186:189], v237 offset:5120
	ds_read_b128 v[194:197], v237 offset:6144
	ds_read_b128 v[198:201], v237 offset:7168
	s_nop 0
	global_load_lds_dwordx4 v235, s[26:27]
	s_mov_b32 m0, s66
	s_nop 0
	global_load_lds_dwordx4 v226, s[26:27]
	s_waitcnt vmcnt(8)
	s_waitcnt lgkmcnt(0)
	s_setprio 1
	s_barrier
	s_waitcnt lgkmcnt(0)
	v_mfma_f32_16x16x32_bf16 v[166:169], v[122:125], v[158:161], v[166:169]
	v_mfma_f32_16x16x32_bf16 v[170:173], v[134:137], v[158:161], v[170:173]
	v_mfma_f32_16x16x32_bf16 v[110:113], v[122:125], v[174:177], v[110:113]
	v_mfma_f32_16x16x32_bf16 v[106:109], v[134:137], v[174:177], v[106:109]
	v_mfma_f32_16x16x32_bf16 v[94:97], v[122:125], v[182:185], v[94:97]
	v_mfma_f32_16x16x32_bf16 v[90:93], v[134:137], v[182:185], v[90:93]
	v_mfma_f32_16x16x32_bf16 v[78:81], v[122:125], v[194:197], v[78:81]
	v_mfma_f32_16x16x32_bf16 v[70:73], v[134:137], v[194:197], v[70:73]
	v_mfma_f32_16x16x32_bf16 v[166:169], v[130:133], v[162:165], v[166:169]
	v_mfma_f32_16x16x32_bf16 v[170:173], v[138:141], v[162:165], v[170:173]
	v_mfma_f32_16x16x32_bf16 v[110:113], v[130:133], v[178:181], v[110:113]
	v_mfma_f32_16x16x32_bf16 v[106:109], v[138:141], v[178:181], v[106:109]
	v_mfma_f32_16x16x32_bf16 v[94:97], v[130:133], v[186:189], v[94:97]
	v_mfma_f32_16x16x32_bf16 v[90:93], v[138:141], v[186:189], v[90:93]
	v_mfma_f32_16x16x32_bf16 v[78:81], v[130:133], v[198:201], v[78:81]
	v_mfma_f32_16x16x32_bf16 v[70:73], v[138:141], v[198:201], v[70:73]
	v_mfma_f32_16x16x32_bf16 v[126:129], v[142:145], v[158:161], v[126:129]
	v_mfma_f32_16x16x32_bf16 v[118:121], v[150:153], v[158:161], v[118:121]
	v_mfma_f32_16x16x32_bf16 v[102:105], v[142:145], v[174:177], v[102:105]
	v_mfma_f32_16x16x32_bf16 v[98:101], v[150:153], v[174:177], v[98:101]
	v_mfma_f32_16x16x32_bf16 v[86:89], v[142:145], v[182:185], v[86:89]
	v_mfma_f32_16x16x32_bf16 v[82:85], v[150:153], v[182:185], v[82:85]
	v_mfma_f32_16x16x32_bf16 v[62:65], v[142:145], v[194:197], v[62:65]
	v_mfma_f32_16x16x32_bf16 v[54:57], v[150:153], v[194:197], v[54:57]
	v_mfma_f32_16x16x32_bf16 v[126:129], v[146:149], v[162:165], v[126:129]
	v_mfma_f32_16x16x32_bf16 v[118:121], v[154:157], v[162:165], v[118:121]
	v_mfma_f32_16x16x32_bf16 v[102:105], v[146:149], v[178:181], v[102:105]
	v_mfma_f32_16x16x32_bf16 v[98:101], v[154:157], v[178:181], v[98:101]
	v_mfma_f32_16x16x32_bf16 v[86:89], v[146:149], v[186:189], v[86:89]
	v_mfma_f32_16x16x32_bf16 v[82:85], v[154:157], v[186:189], v[82:85]
	v_mfma_f32_16x16x32_bf16 v[62:65], v[146:149], v[198:201], v[62:65]
	v_mfma_f32_16x16x32_bf16 v[54:57], v[154:157], v[198:201], v[54:57]
	s_barrier
	s_setprio 0
	s_mov_b32 m0, s67
	ds_read_b128 v[158:161], v237 offset:16384
	ds_read_b128 v[162:165], v237 offset:17408
	ds_read_b128 v[174:177], v237 offset:18432
	ds_read_b128 v[178:181], v237 offset:19456
	ds_read_b128 v[182:185], v237 offset:20480
	ds_read_b128 v[186:189], v237 offset:21504
	ds_read_b128 v[194:197], v237 offset:22528
	ds_read_b128 v[198:201], v237 offset:23552
	s_add_u32 s76, s30, 0x4000
	global_load_lds_dwordx4 v227, s[30:31]
	s_mov_b32 m0, s68
	s_addc_u32 s77, s31, 0
	global_load_lds_dwordx4 v0, s[30:31]
	s_mov_b32 m0, s69
	s_nop 0
	global_load_lds_dwordx4 v227, s[76:77]
	s_mov_b32 m0, s70
	s_nop 0
	global_load_lds_dwordx4 v0, s[76:77]
	s_mov_b32 m0, s20
	s_nop 0
	global_load_lds_dwordx4 v235, s[34:35]
	s_mov_b32 m0, s25
	s_nop 0
	global_load_lds_dwordx4 v226, s[34:35]
	s_waitcnt vmcnt(8)
	s_waitcnt lgkmcnt(0)
	s_setprio 1
	s_barrier
	s_waitcnt lgkmcnt(0)
	v_mfma_f32_16x16x32_bf16 v[74:77], v[122:125], v[158:161], v[74:77]
	v_mfma_f32_16x16x32_bf16 v[66:69], v[134:137], v[158:161], v[66:69]
	v_mfma_f32_16x16x32_bf16 v[46:49], v[122:125], v[174:177], v[46:49]
	v_mfma_f32_16x16x32_bf16 v[42:45], v[134:137], v[174:177], v[42:45]
	v_mfma_f32_16x16x32_bf16 v[30:33], v[122:125], v[182:185], v[30:33]
	v_mfma_f32_16x16x32_bf16 v[26:29], v[134:137], v[182:185], v[26:29]
	v_mfma_f32_16x16x32_bf16 v[14:17], v[122:125], v[194:197], v[14:17]
	v_mfma_f32_16x16x32_bf16 v[10:13], v[134:137], v[194:197], v[10:13]
	v_mfma_f32_16x16x32_bf16 v[74:77], v[130:133], v[162:165], v[74:77]
	v_mfma_f32_16x16x32_bf16 v[66:69], v[138:141], v[162:165], v[66:69]
	v_mfma_f32_16x16x32_bf16 v[46:49], v[130:133], v[178:181], v[46:49]
	v_mfma_f32_16x16x32_bf16 v[42:45], v[138:141], v[178:181], v[42:45]
	v_mfma_f32_16x16x32_bf16 v[30:33], v[130:133], v[186:189], v[30:33]
	v_mfma_f32_16x16x32_bf16 v[26:29], v[138:141], v[186:189], v[26:29]
	v_mfma_f32_16x16x32_bf16 v[14:17], v[130:133], v[198:201], v[14:17]
	v_mfma_f32_16x16x32_bf16 v[10:13], v[138:141], v[198:201], v[10:13]
	v_mfma_f32_16x16x32_bf16 v[58:61], v[142:145], v[158:161], v[58:61]
	v_mfma_f32_16x16x32_bf16 v[50:53], v[150:153], v[158:161], v[50:53]
	v_mfma_f32_16x16x32_bf16 v[38:41], v[142:145], v[174:177], v[38:41]
	v_mfma_f32_16x16x32_bf16 v[34:37], v[150:153], v[174:177], v[34:37]
	v_mfma_f32_16x16x32_bf16 v[22:25], v[142:145], v[182:185], v[22:25]
	v_mfma_f32_16x16x32_bf16 v[18:21], v[150:153], v[182:185], v[18:21]
	v_mfma_f32_16x16x32_bf16 v[6:9], v[142:145], v[194:197], v[6:9]
	v_mfma_f32_16x16x32_bf16 v[2:5], v[150:153], v[194:197], v[2:5]
	v_mfma_f32_16x16x32_bf16 v[58:61], v[146:149], v[162:165], v[58:61]
	v_mfma_f32_16x16x32_bf16 v[50:53], v[154:157], v[162:165], v[50:53]
	v_mfma_f32_16x16x32_bf16 v[38:41], v[146:149], v[178:181], v[38:41]
	v_mfma_f32_16x16x32_bf16 v[34:37], v[154:157], v[178:181], v[34:37]
	v_mfma_f32_16x16x32_bf16 v[22:25], v[146:149], v[186:189], v[22:25]
	v_mfma_f32_16x16x32_bf16 v[18:21], v[154:157], v[186:189], v[18:21]
	v_mfma_f32_16x16x32_bf16 v[6:9], v[146:149], v[198:201], v[6:9]
	v_mfma_f32_16x16x32_bf16 v[2:5], v[154:157], v[198:201], v[2:5]
	s_barrier
	s_setprio 0
	ds_read_b128 v[122:125], v116
	ds_read_b128 v[130:133], v116 offset:1024
	ds_read_b128 v[134:137], v116 offset:2048
	ds_read_b128 v[138:141], v116 offset:3072
	ds_read_b128 v[142:145], v117
	ds_read_b128 v[146:149], v117 offset:1024
	ds_read_b128 v[150:153], v117 offset:2048
	ds_read_b128 v[154:157], v117 offset:3072
	s_add_u32 s34, s34, 0x4000
	s_addc_u32 s35, s35, 0
	s_mov_b32 m0, s54
	ds_read_b128 v[158:161], v237 offset:32768
	ds_read_b128 v[162:165], v237 offset:33792
	ds_read_b128 v[174:177], v237 offset:34816
	ds_read_b128 v[178:181], v237 offset:35840
	ds_read_b128 v[182:185], v237 offset:36864
	ds_read_b128 v[186:189], v237 offset:37888
	ds_read_b128 v[194:197], v237 offset:38912
	ds_read_b128 v[198:201], v237 offset:39936
	s_nop 0
	global_load_lds_dwordx4 v235, s[34:35]
	s_mov_b32 m0, s55
	s_nop 0
	global_load_lds_dwordx4 v226, s[34:35]
	s_waitcnt vmcnt(8)
	s_waitcnt lgkmcnt(0)
	s_setprio 1
	s_barrier
	s_waitcnt lgkmcnt(0)
	v_mfma_f32_16x16x32_bf16 v[166:169], v[122:125], v[158:161], v[166:169]
	v_mfma_f32_16x16x32_bf16 v[170:173], v[134:137], v[158:161], v[170:173]
	v_mfma_f32_16x16x32_bf16 v[110:113], v[122:125], v[174:177], v[110:113]
	v_mfma_f32_16x16x32_bf16 v[106:109], v[134:137], v[174:177], v[106:109]
	v_mfma_f32_16x16x32_bf16 v[94:97], v[122:125], v[182:185], v[94:97]
	v_mfma_f32_16x16x32_bf16 v[90:93], v[134:137], v[182:185], v[90:93]
	v_mfma_f32_16x16x32_bf16 v[78:81], v[122:125], v[194:197], v[78:81]
	v_mfma_f32_16x16x32_bf16 v[70:73], v[134:137], v[194:197], v[70:73]
	v_mfma_f32_16x16x32_bf16 v[166:169], v[130:133], v[162:165], v[166:169]
	v_mfma_f32_16x16x32_bf16 v[170:173], v[138:141], v[162:165], v[170:173]
	v_mfma_f32_16x16x32_bf16 v[110:113], v[130:133], v[178:181], v[110:113]
	v_mfma_f32_16x16x32_bf16 v[106:109], v[138:141], v[178:181], v[106:109]
	v_mfma_f32_16x16x32_bf16 v[94:97], v[130:133], v[186:189], v[94:97]
	v_mfma_f32_16x16x32_bf16 v[90:93], v[138:141], v[186:189], v[90:93]
	v_mfma_f32_16x16x32_bf16 v[78:81], v[130:133], v[198:201], v[78:81]
	v_mfma_f32_16x16x32_bf16 v[70:73], v[138:141], v[198:201], v[70:73]
	v_mfma_f32_16x16x32_bf16 v[126:129], v[142:145], v[158:161], v[126:129]
	v_mfma_f32_16x16x32_bf16 v[118:121], v[150:153], v[158:161], v[118:121]
	v_mfma_f32_16x16x32_bf16 v[102:105], v[142:145], v[174:177], v[102:105]
	v_mfma_f32_16x16x32_bf16 v[98:101], v[150:153], v[174:177], v[98:101]
	v_mfma_f32_16x16x32_bf16 v[86:89], v[142:145], v[182:185], v[86:89]
	v_mfma_f32_16x16x32_bf16 v[82:85], v[150:153], v[182:185], v[82:85]
	v_mfma_f32_16x16x32_bf16 v[62:65], v[142:145], v[194:197], v[62:65]
	v_mfma_f32_16x16x32_bf16 v[54:57], v[150:153], v[194:197], v[54:57]
	v_mfma_f32_16x16x32_bf16 v[126:129], v[146:149], v[162:165], v[126:129]
	v_mfma_f32_16x16x32_bf16 v[118:121], v[154:157], v[162:165], v[118:121]
	v_mfma_f32_16x16x32_bf16 v[102:105], v[146:149], v[178:181], v[102:105]
	v_mfma_f32_16x16x32_bf16 v[98:101], v[154:157], v[178:181], v[98:101]
	v_mfma_f32_16x16x32_bf16 v[86:89], v[146:149], v[186:189], v[86:89]
	v_mfma_f32_16x16x32_bf16 v[82:85], v[154:157], v[186:189], v[82:85]
	v_mfma_f32_16x16x32_bf16 v[62:65], v[146:149], v[198:201], v[62:65]
	v_mfma_f32_16x16x32_bf16 v[54:57], v[154:157], v[198:201], v[54:57]
	s_barrier
	s_setprio 0
	s_add_u32 s34, s30, 0x8000
	s_mov_b32 m0, s52
	s_addc_u32 s35, s31, 0
	ds_read_b128 v[158:161], v237 offset:49152
	ds_read_b128 v[162:165], v237 offset:50176
	ds_read_b128 v[174:177], v237 offset:51200
	ds_read_b128 v[178:181], v237 offset:52224
	ds_read_b128 v[182:185], v237 offset:53248
	ds_read_b128 v[186:189], v237 offset:54272
	ds_read_b128 v[194:197], v237 offset:55296
	ds_read_b128 v[198:201], v237 offset:56320
	s_add_u32 s30, s30, 0xc000
	global_load_lds_dwordx4 v227, s[34:35]
	s_mov_b32 m0, s53
	s_addc_u32 s31, s31, 0
	global_load_lds_dwordx4 v0, s[34:35]
	s_mov_b32 m0, s71
	s_nop 0
	global_load_lds_dwordx4 v227, s[30:31]
	s_mov_b32 m0, s72
	s_nop 0
	global_load_lds_dwordx4 v0, s[30:31]
	s_mov_b32 m0, s58
	s_nop 0
	global_load_lds_dwordx4 v235, s[28:29]
	s_mov_b32 m0, s59
	s_nop 0
	global_load_lds_dwordx4 v226, s[28:29]
	s_waitcnt vmcnt(8)
	s_waitcnt lgkmcnt(0)
	s_setprio 1
	s_barrier
	s_waitcnt lgkmcnt(0)
	v_mfma_f32_16x16x32_bf16 v[74:77], v[122:125], v[158:161], v[74:77]
	v_mfma_f32_16x16x32_bf16 v[66:69], v[134:137], v[158:161], v[66:69]
	v_mfma_f32_16x16x32_bf16 v[46:49], v[122:125], v[174:177], v[46:49]
	v_mfma_f32_16x16x32_bf16 v[42:45], v[134:137], v[174:177], v[42:45]
	v_mfma_f32_16x16x32_bf16 v[30:33], v[122:125], v[182:185], v[30:33]
	v_mfma_f32_16x16x32_bf16 v[26:29], v[134:137], v[182:185], v[26:29]
	v_mfma_f32_16x16x32_bf16 v[14:17], v[122:125], v[194:197], v[14:17]
	v_mfma_f32_16x16x32_bf16 v[10:13], v[134:137], v[194:197], v[10:13]
	v_mfma_f32_16x16x32_bf16 v[74:77], v[130:133], v[162:165], v[74:77]
	v_mfma_f32_16x16x32_bf16 v[66:69], v[138:141], v[162:165], v[66:69]
	v_mfma_f32_16x16x32_bf16 v[46:49], v[130:133], v[178:181], v[46:49]
	v_mfma_f32_16x16x32_bf16 v[42:45], v[138:141], v[178:181], v[42:45]
	v_mfma_f32_16x16x32_bf16 v[30:33], v[130:133], v[186:189], v[30:33]
	v_mfma_f32_16x16x32_bf16 v[26:29], v[138:141], v[186:189], v[26:29]
	v_mfma_f32_16x16x32_bf16 v[14:17], v[130:133], v[198:201], v[14:17]
	v_mfma_f32_16x16x32_bf16 v[10:13], v[138:141], v[198:201], v[10:13]
	v_mfma_f32_16x16x32_bf16 v[58:61], v[142:145], v[158:161], v[58:61]
	v_mfma_f32_16x16x32_bf16 v[50:53], v[150:153], v[158:161], v[50:53]
	v_mfma_f32_16x16x32_bf16 v[38:41], v[142:145], v[174:177], v[38:41]
	v_mfma_f32_16x16x32_bf16 v[34:37], v[150:153], v[174:177], v[34:37]
	v_mfma_f32_16x16x32_bf16 v[22:25], v[142:145], v[182:185], v[22:25]
	v_mfma_f32_16x16x32_bf16 v[18:21], v[150:153], v[182:185], v[18:21]
	v_mfma_f32_16x16x32_bf16 v[6:9], v[142:145], v[194:197], v[6:9]
	v_mfma_f32_16x16x32_bf16 v[2:5], v[150:153], v[194:197], v[2:5]
	v_mfma_f32_16x16x32_bf16 v[58:61], v[146:149], v[162:165], v[58:61]
	v_mfma_f32_16x16x32_bf16 v[50:53], v[154:157], v[162:165], v[50:53]
	v_mfma_f32_16x16x32_bf16 v[38:41], v[146:149], v[178:181], v[38:41]
	v_mfma_f32_16x16x32_bf16 v[34:37], v[154:157], v[178:181], v[34:37]
	v_mfma_f32_16x16x32_bf16 v[22:25], v[146:149], v[186:189], v[22:25]
	v_mfma_f32_16x16x32_bf16 v[18:21], v[154:157], v[186:189], v[18:21]
	v_mfma_f32_16x16x32_bf16 v[6:9], v[146:149], v[198:201], v[6:9]
	v_mfma_f32_16x16x32_bf16 v[2:5], v[154:157], v[198:201], v[2:5]
	s_barrier
	s_setprio 0
	s_add_i32 s28, s75, 2
	s_add_u32 s73, s73, 0x10000
	s_addc_u32 s74, s74, 0
	s_add_u32 s26, s26, 0x10000
	s_addc_u32 s27, s27, 0
	s_cmp_lt_i32 s75, s56
	s_mov_b32 s75, s28
	s_cbranch_scc1 .LBB0_381

.LBB0_454:
	s_or_b64 exec, exec, s[34:35]
	s_add_i32 s11, s11, 2
	s_add_u32 s18, s28, 0x4000
	s_addc_u32 s20, s29, 0
	s_and_b64 s[14:15], s[30:31], exec
	s_cselect_b32 s64, s18, s46
	s_cselect_b32 s65, s20, s47
	s_cselect_b32 s35, s2, s63
	s_cselect_b32 s34, s1, s62
	s_add_u32 s30, s64, 0x8000
	s_addc_u32 s31, s65, 0
	s_add_u32 s38, s34, 0x8000
	s_addc_u32 s39, s35, 0
	s_add_i32 s14, 0, 0x10000
	v_add_u32_e32 v149, s14, v146
	s_add_i32 s18, 0, 0x14000
	ds_read_b128 v[132:135], v149
	ds_read_b128 v[136:139], v149 offset:1024
	ds_read_b128 v[150:153], v149 offset:2048
	ds_read_b128 v[154:157], v149 offset:3072
	v_add_u32_e32 v149, s18, v146
	ds_read_b128 v[158:161], v149
	ds_read_b128 v[162:165], v149 offset:1024
	ds_read_b128 v[166:169], v149 offset:2048
	ds_read_b128 v[170:173], v149 offset:3072
	s_add_i32 m0, s71, 0xc000
	ds_read_b128 v[174:177], v148
	ds_read_b128 v[178:181], v148 offset:1024
	ds_read_b128 v[182:185], v148 offset:2048
	ds_read_b128 v[186:189], v148 offset:3072
	ds_read_b128 v[194:197], v148 offset:4096
	ds_read_b128 v[198:201], v148 offset:5120
	ds_read_b128 v[202:205], v148 offset:6144
	ds_read_b128 v[206:209], v148 offset:7168
	s_nop 0
	global_load_lds_dwordx4 v142, s[28:29]
	s_add_i32 m0, s71, 0xe000
	s_nop 0
	global_load_lds_dwordx4 v144, s[28:29]
	s_waitcnt vmcnt(8)
	s_waitcnt lgkmcnt(0)
	s_setprio 1
	s_barrier
	s_waitcnt lgkmcnt(0)
	v_mfma_f32_16x16x32_bf16 v[66:69], v[132:135], v[174:177], v[66:69]
	v_mfma_f32_16x16x32_bf16 v[70:73], v[150:153], v[174:177], v[70:73]
	v_mfma_f32_16x16x32_bf16 v[58:61], v[132:135], v[182:185], v[58:61]
	v_mfma_f32_16x16x32_bf16 v[62:65], v[150:153], v[182:185], v[62:65]
	v_mfma_f32_16x16x32_bf16 v[50:53], v[132:135], v[194:197], v[50:53]
	v_mfma_f32_16x16x32_bf16 v[54:57], v[150:153], v[194:197], v[54:57]
	v_mfma_f32_16x16x32_bf16 v[42:45], v[132:135], v[202:205], v[42:45]
	v_mfma_f32_16x16x32_bf16 v[46:49], v[150:153], v[202:205], v[46:49]
	v_mfma_f32_16x16x32_bf16 v[66:69], v[136:139], v[178:181], v[66:69]
	v_mfma_f32_16x16x32_bf16 v[70:73], v[154:157], v[178:181], v[70:73]
	v_mfma_f32_16x16x32_bf16 v[58:61], v[136:139], v[186:189], v[58:61]
	v_mfma_f32_16x16x32_bf16 v[62:65], v[154:157], v[186:189], v[62:65]
	v_mfma_f32_16x16x32_bf16 v[50:53], v[136:139], v[198:201], v[50:53]
	v_mfma_f32_16x16x32_bf16 v[54:57], v[154:157], v[198:201], v[54:57]
	v_mfma_f32_16x16x32_bf16 v[42:45], v[136:139], v[206:209], v[42:45]
	v_mfma_f32_16x16x32_bf16 v[46:49], v[154:157], v[206:209], v[46:49]
	v_mfma_f32_16x16x32_bf16 v[126:129], v[158:161], v[174:177], v[126:129]
	v_mfma_f32_16x16x32_bf16 v[122:125], v[166:169], v[174:177], v[122:125]
	v_mfma_f32_16x16x32_bf16 v[118:121], v[158:161], v[182:185], v[118:121]
	v_mfma_f32_16x16x32_bf16 v[114:117], v[166:169], v[182:185], v[114:117]
	v_mfma_f32_16x16x32_bf16 v[110:113], v[158:161], v[194:197], v[110:113]
	v_mfma_f32_16x16x32_bf16 v[106:109], v[166:169], v[194:197], v[106:109]
	v_mfma_f32_16x16x32_bf16 v[94:97], v[158:161], v[202:205], v[94:97]
	v_mfma_f32_16x16x32_bf16 v[90:93], v[166:169], v[202:205], v[90:93]
	v_mfma_f32_16x16x32_bf16 v[126:129], v[162:165], v[178:181], v[126:129]
	v_mfma_f32_16x16x32_bf16 v[122:125], v[170:173], v[178:181], v[122:125]
	v_mfma_f32_16x16x32_bf16 v[118:121], v[162:165], v[186:189], v[118:121]
	v_mfma_f32_16x16x32_bf16 v[114:117], v[170:173], v[186:189], v[114:117]
	v_mfma_f32_16x16x32_bf16 v[110:113], v[162:165], v[198:201], v[110:113]
	v_mfma_f32_16x16x32_bf16 v[106:109], v[170:173], v[198:201], v[106:109]
	v_mfma_f32_16x16x32_bf16 v[94:97], v[162:165], v[206:209], v[94:97]
	v_mfma_f32_16x16x32_bf16 v[90:93], v[170:173], v[206:209], v[90:93]
	s_barrier
	s_setprio 0
	s_add_i32 s14, s14, s70
	s_mov_b32 m0, s14
	ds_read_b128 v[174:177], v148 offset:16384
	ds_read_b128 v[178:181], v148 offset:17408
	ds_read_b128 v[182:185], v148 offset:18432
	ds_read_b128 v[186:189], v148 offset:19456
	ds_read_b128 v[194:197], v148 offset:20480
	ds_read_b128 v[198:201], v148 offset:21504
	ds_read_b128 v[202:205], v148 offset:22528
	ds_read_b128 v[206:209], v148 offset:23552
	s_nop 0
	global_load_lds_dwordx4 v143, s[34:35]
	s_add_i32 m0, s14, 0x2000
	s_add_u32 s14, s34, 0x4000
	s_addc_u32 s15, s35, 0
	s_add_i32 s18, s18, s70
	s_nop 0
	global_load_lds_dwordx4 v145, s[34:35]
	s_mov_b32 m0, s18
	s_nop 0
	global_load_lds_dwordx4 v143, s[14:15]
	s_add_i32 m0, s18, 0x2000
	s_nop 0
	global_load_lds_dwordx4 v145, s[14:15]
	s_mov_b32 m0, s71
	s_nop 0
	global_load_lds_dwordx4 v142, s[64:65]
	s_mov_b32 m0, s72
	s_nop 0
	global_load_lds_dwordx4 v144, s[64:65]
	s_waitcnt vmcnt(8)
	s_waitcnt lgkmcnt(0)
	s_setprio 1
	s_barrier
	s_waitcnt lgkmcnt(0)
	v_mfma_f32_16x16x32_bf16 v[26:29], v[132:135], v[174:177], v[26:29]
	v_mfma_f32_16x16x32_bf16 v[30:33], v[150:153], v[174:177], v[30:33]
	v_mfma_f32_16x16x32_bf16 v[18:21], v[132:135], v[182:185], v[18:21]
	v_mfma_f32_16x16x32_bf16 v[22:25], v[150:153], v[182:185], v[22:25]
	v_mfma_f32_16x16x32_bf16 v[10:13], v[132:135], v[194:197], v[10:13]
	v_mfma_f32_16x16x32_bf16 v[14:17], v[150:153], v[194:197], v[14:17]
	v_mfma_f32_16x16x32_bf16 v[2:5], v[132:135], v[202:205], v[2:5]
	v_mfma_f32_16x16x32_bf16 v[6:9], v[150:153], v[202:205], v[6:9]
	v_mfma_f32_16x16x32_bf16 v[26:29], v[136:139], v[178:181], v[26:29]
	v_mfma_f32_16x16x32_bf16 v[30:33], v[154:157], v[178:181], v[30:33]
	v_mfma_f32_16x16x32_bf16 v[18:21], v[136:139], v[186:189], v[18:21]
	v_mfma_f32_16x16x32_bf16 v[22:25], v[154:157], v[186:189], v[22:25]
	v_mfma_f32_16x16x32_bf16 v[10:13], v[136:139], v[198:201], v[10:13]
	v_mfma_f32_16x16x32_bf16 v[14:17], v[154:157], v[198:201], v[14:17]
	v_mfma_f32_16x16x32_bf16 v[2:5], v[136:139], v[206:209], v[2:5]
	v_mfma_f32_16x16x32_bf16 v[6:9], v[154:157], v[206:209], v[6:9]
	v_mfma_f32_16x16x32_bf16 v[102:105], v[158:161], v[174:177], v[102:105]
	v_mfma_f32_16x16x32_bf16 v[98:101], v[166:169], v[174:177], v[98:101]
	v_mfma_f32_16x16x32_bf16 v[82:85], v[158:161], v[182:185], v[82:85]
	v_mfma_f32_16x16x32_bf16 v[86:89], v[166:169], v[182:185], v[86:89]
	v_mfma_f32_16x16x32_bf16 v[78:81], v[158:161], v[194:197], v[78:81]
	v_mfma_f32_16x16x32_bf16 v[74:77], v[166:169], v[194:197], v[74:77]
	v_mfma_f32_16x16x32_bf16 v[34:37], v[158:161], v[202:205], v[34:37]
	v_mfma_f32_16x16x32_bf16 v[38:41], v[166:169], v[202:205], v[38:41]
	v_mfma_f32_16x16x32_bf16 v[102:105], v[162:165], v[178:181], v[102:105]
	v_mfma_f32_16x16x32_bf16 v[98:101], v[170:173], v[178:181], v[98:101]
	v_mfma_f32_16x16x32_bf16 v[82:85], v[162:165], v[186:189], v[82:85]
	v_mfma_f32_16x16x32_bf16 v[86:89], v[170:173], v[186:189], v[86:89]
	v_mfma_f32_16x16x32_bf16 v[78:81], v[162:165], v[198:201], v[78:81]
	v_mfma_f32_16x16x32_bf16 v[74:77], v[170:173], v[198:201], v[74:77]
	v_mfma_f32_16x16x32_bf16 v[34:37], v[162:165], v[206:209], v[34:37]
	v_mfma_f32_16x16x32_bf16 v[38:41], v[170:173], v[206:209], v[38:41]
	s_barrier
	s_setprio 0
	s_add_i32 s18, 0, 0x18000
	v_add_u32_e32 v149, s18, v146
	s_add_i32 s20, 0, 0x1c000
	ds_read_b128 v[132:135], v149
	ds_read_b128 v[136:139], v149 offset:1024
	ds_read_b128 v[150:153], v149 offset:2048
	ds_read_b128 v[154:157], v149 offset:3072
	v_add_u32_e32 v149, s20, v146
	ds_read_b128 v[158:161], v149
	ds_read_b128 v[162:165], v149 offset:1024
	ds_read_b128 v[166:169], v149 offset:2048
	ds_read_b128 v[170:173], v149 offset:3072
	s_add_u32 s14, s64, 0x4000
	s_addc_u32 s15, s65, 0
	s_mov_b32 m0, s73
	ds_read_b128 v[174:177], v148 offset:32768
	ds_read_b128 v[178:181], v148 offset:33792
	ds_read_b128 v[182:185], v148 offset:34816
	ds_read_b128 v[186:189], v148 offset:35840
	ds_read_b128 v[194:197], v148 offset:36864
	ds_read_b128 v[198:201], v148 offset:37888
	ds_read_b128 v[202:205], v148 offset:38912
	ds_read_b128 v[206:209], v148 offset:39936
	s_nop 0
	global_load_lds_dwordx4 v142, s[14:15]
	s_mov_b32 m0, s74
	s_nop 0
	global_load_lds_dwordx4 v144, s[14:15]
	s_waitcnt vmcnt(8)
	s_waitcnt lgkmcnt(0)
	s_setprio 1
	s_barrier
	s_waitcnt lgkmcnt(0)
	v_mfma_f32_16x16x32_bf16 v[66:69], v[132:135], v[174:177], v[66:69]
	v_mfma_f32_16x16x32_bf16 v[70:73], v[150:153], v[174:177], v[70:73]
	v_mfma_f32_16x16x32_bf16 v[58:61], v[132:135], v[182:185], v[58:61]
	v_mfma_f32_16x16x32_bf16 v[62:65], v[150:153], v[182:185], v[62:65]
	v_mfma_f32_16x16x32_bf16 v[50:53], v[132:135], v[194:197], v[50:53]
	v_mfma_f32_16x16x32_bf16 v[54:57], v[150:153], v[194:197], v[54:57]
	v_mfma_f32_16x16x32_bf16 v[42:45], v[132:135], v[202:205], v[42:45]
	v_mfma_f32_16x16x32_bf16 v[46:49], v[150:153], v[202:205], v[46:49]
	v_mfma_f32_16x16x32_bf16 v[66:69], v[136:139], v[178:181], v[66:69]
	v_mfma_f32_16x16x32_bf16 v[70:73], v[154:157], v[178:181], v[70:73]
	v_mfma_f32_16x16x32_bf16 v[58:61], v[136:139], v[186:189], v[58:61]
	v_mfma_f32_16x16x32_bf16 v[62:65], v[154:157], v[186:189], v[62:65]
	v_mfma_f32_16x16x32_bf16 v[50:53], v[136:139], v[198:201], v[50:53]
	v_mfma_f32_16x16x32_bf16 v[54:57], v[154:157], v[198:201], v[54:57]
	v_mfma_f32_16x16x32_bf16 v[42:45], v[136:139], v[206:209], v[42:45]
	v_mfma_f32_16x16x32_bf16 v[46:49], v[154:157], v[206:209], v[46:49]
	v_mfma_f32_16x16x32_bf16 v[126:129], v[158:161], v[174:177], v[126:129]
	v_mfma_f32_16x16x32_bf16 v[122:125], v[166:169], v[174:177], v[122:125]
	v_mfma_f32_16x16x32_bf16 v[118:121], v[158:161], v[182:185], v[118:121]
	v_mfma_f32_16x16x32_bf16 v[114:117], v[166:169], v[182:185], v[114:117]
	v_mfma_f32_16x16x32_bf16 v[110:113], v[158:161], v[194:197], v[110:113]
	v_mfma_f32_16x16x32_bf16 v[106:109], v[166:169], v[194:197], v[106:109]
	v_mfma_f32_16x16x32_bf16 v[94:97], v[158:161], v[202:205], v[94:97]
	v_mfma_f32_16x16x32_bf16 v[90:93], v[166:169], v[202:205], v[90:93]
	v_mfma_f32_16x16x32_bf16 v[126:129], v[162:165], v[178:181], v[126:129]
	v_mfma_f32_16x16x32_bf16 v[122:125], v[170:173], v[178:181], v[122:125]
	v_mfma_f32_16x16x32_bf16 v[118:121], v[162:165], v[186:189], v[118:121]
	v_mfma_f32_16x16x32_bf16 v[114:117], v[170:173], v[186:189], v[114:117]
	v_mfma_f32_16x16x32_bf16 v[110:113], v[162:165], v[198:201], v[110:113]
	v_mfma_f32_16x16x32_bf16 v[106:109], v[170:173], v[198:201], v[106:109]
	v_mfma_f32_16x16x32_bf16 v[94:97], v[162:165], v[206:209], v[94:97]
	v_mfma_f32_16x16x32_bf16 v[90:93], v[170:173], v[206:209], v[90:93]
	s_barrier
	s_setprio 0
	s_add_i32 s14, s18, s70
	s_mov_b32 m0, s14
	ds_read_b128 v[174:177], v148 offset:49152
	ds_read_b128 v[178:181], v148 offset:50176
	ds_read_b128 v[182:185], v148 offset:51200
	ds_read_b128 v[186:189], v148 offset:52224
	ds_read_b128 v[194:197], v148 offset:53248
	ds_read_b128 v[198:201], v148 offset:54272
	ds_read_b128 v[202:205], v148 offset:55296
	ds_read_b128 v[206:209], v148 offset:56320
	s_nop 0
	global_load_lds_dwordx4 v143, s[38:39]
	s_add_i32 m0, s14, 0x2000
	s_add_u32 s14, s34, 0xc000
	s_addc_u32 s15, s35, 0
	s_add_i32 s18, s20, s70
	s_nop 0
	global_load_lds_dwordx4 v145, s[38:39]
	s_mov_b32 m0, s18
	s_nop 0
	global_load_lds_dwordx4 v143, s[14:15]
	s_add_i32 m0, s18, 0x2000
	s_nop 0
	global_load_lds_dwordx4 v145, s[14:15]
	s_mov_b32 m0, s81
	s_nop 0
	global_load_lds_dwordx4 v142, s[30:31]
	s_mov_b32 m0, s82
	s_nop 0
	global_load_lds_dwordx4 v144, s[30:31]
	s_waitcnt vmcnt(8)
	s_waitcnt lgkmcnt(0)
	s_setprio 1
	s_barrier
	s_waitcnt lgkmcnt(0)
	v_mfma_f32_16x16x32_bf16 v[26:29], v[132:135], v[174:177], v[26:29]
	v_mfma_f32_16x16x32_bf16 v[30:33], v[150:153], v[174:177], v[30:33]
	v_mfma_f32_16x16x32_bf16 v[18:21], v[132:135], v[182:185], v[18:21]
	v_mfma_f32_16x16x32_bf16 v[22:25], v[150:153], v[182:185], v[22:25]
	v_mfma_f32_16x16x32_bf16 v[10:13], v[132:135], v[194:197], v[10:13]
	v_mfma_f32_16x16x32_bf16 v[14:17], v[150:153], v[194:197], v[14:17]
	v_mfma_f32_16x16x32_bf16 v[2:5], v[132:135], v[202:205], v[2:5]
	v_mfma_f32_16x16x32_bf16 v[6:9], v[150:153], v[202:205], v[6:9]
	v_mfma_f32_16x16x32_bf16 v[26:29], v[136:139], v[178:181], v[26:29]
	v_mfma_f32_16x16x32_bf16 v[30:33], v[154:157], v[178:181], v[30:33]
	v_mfma_f32_16x16x32_bf16 v[18:21], v[136:139], v[186:189], v[18:21]
	v_mfma_f32_16x16x32_bf16 v[22:25], v[154:157], v[186:189], v[22:25]
	v_mfma_f32_16x16x32_bf16 v[10:13], v[136:139], v[198:201], v[10:13]
	v_mfma_f32_16x16x32_bf16 v[14:17], v[154:157], v[198:201], v[14:17]
	v_mfma_f32_16x16x32_bf16 v[2:5], v[136:139], v[206:209], v[2:5]
	v_mfma_f32_16x16x32_bf16 v[6:9], v[154:157], v[206:209], v[6:9]
	v_mfma_f32_16x16x32_bf16 v[102:105], v[158:161], v[174:177], v[102:105]
	v_mfma_f32_16x16x32_bf16 v[98:101], v[166:169], v[174:177], v[98:101]
	v_mfma_f32_16x16x32_bf16 v[82:85], v[158:161], v[182:185], v[82:85]
	v_mfma_f32_16x16x32_bf16 v[86:89], v[166:169], v[182:185], v[86:89]
	v_mfma_f32_16x16x32_bf16 v[78:81], v[158:161], v[194:197], v[78:81]
	v_mfma_f32_16x16x32_bf16 v[74:77], v[166:169], v[194:197], v[74:77]
	v_mfma_f32_16x16x32_bf16 v[34:37], v[158:161], v[202:205], v[34:37]
	v_mfma_f32_16x16x32_bf16 v[38:41], v[166:169], v[202:205], v[38:41]
	v_mfma_f32_16x16x32_bf16 v[102:105], v[162:165], v[178:181], v[102:105]
	v_mfma_f32_16x16x32_bf16 v[98:101], v[170:173], v[178:181], v[98:101]
	v_mfma_f32_16x16x32_bf16 v[82:85], v[162:165], v[186:189], v[82:85]
	v_mfma_f32_16x16x32_bf16 v[86:89], v[170:173], v[186:189], v[86:89]
	v_mfma_f32_16x16x32_bf16 v[78:81], v[162:165], v[198:201], v[78:81]
	v_mfma_f32_16x16x32_bf16 v[74:77], v[170:173], v[198:201], v[74:77]
	v_mfma_f32_16x16x32_bf16 v[34:37], v[162:165], v[206:209], v[34:37]
	v_mfma_f32_16x16x32_bf16 v[38:41], v[170:173], v[206:209], v[38:41]
	s_barrier
	s_setprio 0
	s_add_u32 s1, s1, 0x10000
	s_addc_u32 s2, s2, 0
	s_add_u32 s28, s28, 0x10000
	s_addc_u32 s29, s29, 0
	s_cmp_ge_i32 s11, s78
	s_cbranch_scc1 .LBB0_457

.LBB0_498:
	s_add_i32 s83, s52, 2
	s_add_u32 s50, s48, 0x100
	s_addc_u32 s51, s49, 0
	s_add_i32 s84, 0, 0x10000
	s_cmp_eq_u32 s71, s52
	s_cselect_b32 s53, s43, s51
	s_cselect_b32 s52, s42, s50
	v_add_u32_e32 v131, s84, v137
	s_cselect_b32 s55, s47, s82
	s_cselect_b32 s54, s46, s81
	s_add_i32 s85, 0, 0x14000
	ds_read_b128 v[142:145], v131
	ds_read_b128 v[146:149], v131 offset:1024
	ds_read_b128 v[150:153], v131 offset:2048
	ds_read_b128 v[154:157], v131 offset:3072
	v_add_u32_e32 v131, s85, v137
	ds_read_b128 v[158:161], v131
	ds_read_b128 v[162:165], v131 offset:1024
	ds_read_b128 v[166:169], v131 offset:2048
	ds_read_b128 v[170:173], v131 offset:3072
	s_add_u32 s48, s48, s74
	s_addc_u32 s49, s49, s75
	s_add_i32 m0, s62, 0xc000
	ds_read_b128 v[174:177], v138
	ds_read_b128 v[178:181], v138 offset:1024
	ds_read_b128 v[182:185], v138 offset:2048
	ds_read_b128 v[186:189], v138 offset:3072
	ds_read_b128 v[194:197], v138 offset:4096
	ds_read_b128 v[198:201], v138 offset:5120
	ds_read_b128 v[202:205], v138 offset:6144
	ds_read_b128 v[206:209], v138 offset:7168
	s_nop 0
	global_load_lds_dwordx4 v130, s[48:49]
	s_add_i32 m0, s62, 0xe000
	s_nop 0
	global_load_lds_dwordx4 v132, s[48:49]
	s_waitcnt vmcnt(8)
	s_waitcnt lgkmcnt(0)
	s_setprio 1
	s_barrier
	s_waitcnt lgkmcnt(0)
	v_mfma_f32_16x16x32_bf16 v[118:121], v[142:145], v[174:177], v[118:121]
	v_mfma_f32_16x16x32_bf16 v[114:117], v[150:153], v[174:177], v[114:117]
	v_mfma_f32_16x16x32_bf16 v[102:105], v[142:145], v[182:185], v[102:105]
	v_mfma_f32_16x16x32_bf16 v[98:101], v[150:153], v[182:185], v[98:101]
	v_mfma_f32_16x16x32_bf16 v[86:89], v[142:145], v[194:197], v[86:89]
	v_mfma_f32_16x16x32_bf16 v[82:85], v[150:153], v[194:197], v[82:85]
	v_mfma_f32_16x16x32_bf16 v[70:73], v[142:145], v[202:205], v[70:73]
	v_mfma_f32_16x16x32_bf16 v[66:69], v[150:153], v[202:205], v[66:69]
	v_mfma_f32_16x16x32_bf16 v[118:121], v[146:149], v[178:181], v[118:121]
	v_mfma_f32_16x16x32_bf16 v[114:117], v[154:157], v[178:181], v[114:117]
	v_mfma_f32_16x16x32_bf16 v[102:105], v[146:149], v[186:189], v[102:105]
	v_mfma_f32_16x16x32_bf16 v[98:101], v[154:157], v[186:189], v[98:101]
	v_mfma_f32_16x16x32_bf16 v[86:89], v[146:149], v[198:201], v[86:89]
	v_mfma_f32_16x16x32_bf16 v[82:85], v[154:157], v[198:201], v[82:85]
	v_mfma_f32_16x16x32_bf16 v[70:73], v[146:149], v[206:209], v[70:73]
	v_mfma_f32_16x16x32_bf16 v[66:69], v[154:157], v[206:209], v[66:69]
	v_mfma_f32_16x16x32_bf16 v[46:49], v[158:161], v[174:177], v[46:49]
	v_mfma_f32_16x16x32_bf16 v[42:45], v[166:169], v[174:177], v[42:45]
	v_mfma_f32_16x16x32_bf16 v[30:33], v[158:161], v[182:185], v[30:33]
	v_mfma_f32_16x16x32_bf16 v[26:29], v[166:169], v[182:185], v[26:29]
	v_mfma_f32_16x16x32_bf16 v[14:17], v[158:161], v[194:197], v[14:17]
	v_mfma_f32_16x16x32_bf16 v[10:13], v[166:169], v[194:197], v[10:13]
	v_mfma_f32_16x16x32_bf16 v[6:9], v[158:161], v[202:205], v[6:9]
	v_mfma_f32_16x16x32_bf16 v[2:5], v[166:169], v[202:205], v[2:5]
	v_mfma_f32_16x16x32_bf16 v[46:49], v[162:165], v[178:181], v[46:49]
	v_mfma_f32_16x16x32_bf16 v[42:45], v[170:173], v[178:181], v[42:45]
	v_mfma_f32_16x16x32_bf16 v[30:33], v[162:165], v[186:189], v[30:33]
	v_mfma_f32_16x16x32_bf16 v[26:29], v[170:173], v[186:189], v[26:29]
	v_mfma_f32_16x16x32_bf16 v[14:17], v[162:165], v[198:201], v[14:17]
	v_mfma_f32_16x16x32_bf16 v[10:13], v[170:173], v[198:201], v[10:13]
	v_mfma_f32_16x16x32_bf16 v[6:9], v[162:165], v[206:209], v[6:9]
	v_mfma_f32_16x16x32_bf16 v[2:5], v[170:173], v[206:209], v[2:5]
	s_barrier
	s_setprio 0
	s_add_i32 s48, s84, s61
	s_mov_b32 m0, s48
	ds_read_b128 v[174:177], v138 offset:16384
	ds_read_b128 v[178:181], v138 offset:17408
	ds_read_b128 v[182:185], v138 offset:18432
	ds_read_b128 v[186:189], v138 offset:19456
	ds_read_b128 v[194:197], v138 offset:20480
	ds_read_b128 v[198:201], v138 offset:21504
	ds_read_b128 v[202:205], v138 offset:22528
	ds_read_b128 v[206:209], v138 offset:23552
	s_nop 0
	global_load_lds_dwordx4 v0, s[54:55]
	s_add_i32 m0, s48, 0x2000
	s_add_u32 s48, s54, s28
	s_addc_u32 s49, s55, s29
	s_add_i32 s84, s85, s61
	s_nop 0
	global_load_lds_dwordx4 v134, s[54:55]
	s_mov_b32 m0, s84
	s_nop 0
	global_load_lds_dwordx4 v0, s[48:49]
	s_add_i32 m0, s84, 0x2000
	s_nop 0
	global_load_lds_dwordx4 v134, s[48:49]
	s_mov_b32 m0, s62
	s_nop 0
	global_load_lds_dwordx4 v130, s[52:53]
	s_mov_b32 m0, s63
	s_nop 0
	global_load_lds_dwordx4 v132, s[52:53]
	s_waitcnt vmcnt(8)
	s_waitcnt lgkmcnt(0)
	s_setprio 1
	s_barrier
	s_waitcnt lgkmcnt(0)
	v_mfma_f32_16x16x32_bf16 v[126:129], v[142:145], v[174:177], v[126:129]
	v_mfma_f32_16x16x32_bf16 v[122:125], v[150:153], v[174:177], v[122:125]
	v_mfma_f32_16x16x32_bf16 v[110:113], v[142:145], v[182:185], v[110:113]
	v_mfma_f32_16x16x32_bf16 v[106:109], v[150:153], v[182:185], v[106:109]
	v_mfma_f32_16x16x32_bf16 v[94:97], v[142:145], v[194:197], v[94:97]
	v_mfma_f32_16x16x32_bf16 v[90:93], v[150:153], v[194:197], v[90:93]
	v_mfma_f32_16x16x32_bf16 v[78:81], v[142:145], v[202:205], v[78:81]
	v_mfma_f32_16x16x32_bf16 v[74:77], v[150:153], v[202:205], v[74:77]
	v_mfma_f32_16x16x32_bf16 v[126:129], v[146:149], v[178:181], v[126:129]
	v_mfma_f32_16x16x32_bf16 v[122:125], v[154:157], v[178:181], v[122:125]
	v_mfma_f32_16x16x32_bf16 v[110:113], v[146:149], v[186:189], v[110:113]
	v_mfma_f32_16x16x32_bf16 v[106:109], v[154:157], v[186:189], v[106:109]
	v_mfma_f32_16x16x32_bf16 v[94:97], v[146:149], v[198:201], v[94:97]
	v_mfma_f32_16x16x32_bf16 v[90:93], v[154:157], v[198:201], v[90:93]
	v_mfma_f32_16x16x32_bf16 v[78:81], v[146:149], v[206:209], v[78:81]
	v_mfma_f32_16x16x32_bf16 v[74:77], v[154:157], v[206:209], v[74:77]
	v_mfma_f32_16x16x32_bf16 v[54:57], v[158:161], v[174:177], v[54:57]
	v_mfma_f32_16x16x32_bf16 v[50:53], v[166:169], v[174:177], v[50:53]
	v_mfma_f32_16x16x32_bf16 v[38:41], v[158:161], v[182:185], v[38:41]
	v_mfma_f32_16x16x32_bf16 v[34:37], v[166:169], v[182:185], v[34:37]
	v_mfma_f32_16x16x32_bf16 v[22:25], v[158:161], v[194:197], v[22:25]
	v_mfma_f32_16x16x32_bf16 v[18:21], v[166:169], v[194:197], v[18:21]
	v_mfma_f32_16x16x32_bf16 v[58:61], v[158:161], v[202:205], v[58:61]
	v_mfma_f32_16x16x32_bf16 v[62:65], v[166:169], v[202:205], v[62:65]
	v_mfma_f32_16x16x32_bf16 v[54:57], v[162:165], v[178:181], v[54:57]
	v_mfma_f32_16x16x32_bf16 v[50:53], v[170:173], v[178:181], v[50:53]
	v_mfma_f32_16x16x32_bf16 v[38:41], v[162:165], v[186:189], v[38:41]
	v_mfma_f32_16x16x32_bf16 v[34:37], v[170:173], v[186:189], v[34:37]
	v_mfma_f32_16x16x32_bf16 v[22:25], v[162:165], v[198:201], v[22:25]
	v_mfma_f32_16x16x32_bf16 v[18:21], v[170:173], v[198:201], v[18:21]
	v_mfma_f32_16x16x32_bf16 v[58:61], v[162:165], v[206:209], v[58:61]
	v_mfma_f32_16x16x32_bf16 v[62:65], v[170:173], v[206:209], v[62:65]
	s_barrier
	s_setprio 0
	s_add_i32 s86, 0, 0x18000
	v_add_u32_e32 v131, s86, v137
	s_add_i32 s87, 0, 0x1c000
	ds_read_b128 v[142:145], v131
	ds_read_b128 v[146:149], v131 offset:1024
	ds_read_b128 v[150:153], v131 offset:2048
	ds_read_b128 v[154:157], v131 offset:3072
	v_add_u32_e32 v131, s87, v137
	ds_read_b128 v[158:161], v131
	ds_read_b128 v[162:165], v131 offset:1024
	ds_read_b128 v[166:169], v131 offset:2048
	ds_read_b128 v[170:173], v131 offset:3072
	s_add_u32 s84, s52, s28
	s_addc_u32 s85, s53, s29
	s_mov_b32 m0, s64
	ds_read_b128 v[174:177], v138 offset:32768
	ds_read_b128 v[178:181], v138 offset:33792
	ds_read_b128 v[182:185], v138 offset:34816
	ds_read_b128 v[186:189], v138 offset:35840
	ds_read_b128 v[194:197], v138 offset:36864
	ds_read_b128 v[198:201], v138 offset:37888
	ds_read_b128 v[202:205], v138 offset:38912
	ds_read_b128 v[206:209], v138 offset:39936
	s_nop 0
	global_load_lds_dwordx4 v130, s[84:85]
	s_mov_b32 m0, s65
	s_nop 0
	global_load_lds_dwordx4 v132, s[84:85]
	s_waitcnt vmcnt(8)
	s_waitcnt lgkmcnt(0)
	s_setprio 1
	s_barrier
	s_waitcnt lgkmcnt(0)
	v_mfma_f32_16x16x32_bf16 v[118:121], v[142:145], v[174:177], v[118:121]
	v_mfma_f32_16x16x32_bf16 v[114:117], v[150:153], v[174:177], v[114:117]
	v_mfma_f32_16x16x32_bf16 v[102:105], v[142:145], v[182:185], v[102:105]
	v_mfma_f32_16x16x32_bf16 v[98:101], v[150:153], v[182:185], v[98:101]
	v_mfma_f32_16x16x32_bf16 v[86:89], v[142:145], v[194:197], v[86:89]
	v_mfma_f32_16x16x32_bf16 v[82:85], v[150:153], v[194:197], v[82:85]
	v_mfma_f32_16x16x32_bf16 v[70:73], v[142:145], v[202:205], v[70:73]
	v_mfma_f32_16x16x32_bf16 v[66:69], v[150:153], v[202:205], v[66:69]
	v_mfma_f32_16x16x32_bf16 v[118:121], v[146:149], v[178:181], v[118:121]
	v_mfma_f32_16x16x32_bf16 v[114:117], v[154:157], v[178:181], v[114:117]
	v_mfma_f32_16x16x32_bf16 v[102:105], v[146:149], v[186:189], v[102:105]
	v_mfma_f32_16x16x32_bf16 v[98:101], v[154:157], v[186:189], v[98:101]
	v_mfma_f32_16x16x32_bf16 v[86:89], v[146:149], v[198:201], v[86:89]
	v_mfma_f32_16x16x32_bf16 v[82:85], v[154:157], v[198:201], v[82:85]
	v_mfma_f32_16x16x32_bf16 v[70:73], v[146:149], v[206:209], v[70:73]
	v_mfma_f32_16x16x32_bf16 v[66:69], v[154:157], v[206:209], v[66:69]
	v_mfma_f32_16x16x32_bf16 v[46:49], v[158:161], v[174:177], v[46:49]
	v_mfma_f32_16x16x32_bf16 v[42:45], v[166:169], v[174:177], v[42:45]
	v_mfma_f32_16x16x32_bf16 v[30:33], v[158:161], v[182:185], v[30:33]
	v_mfma_f32_16x16x32_bf16 v[26:29], v[166:169], v[182:185], v[26:29]
	v_mfma_f32_16x16x32_bf16 v[14:17], v[158:161], v[194:197], v[14:17]
	v_mfma_f32_16x16x32_bf16 v[10:13], v[166:169], v[194:197], v[10:13]
	v_mfma_f32_16x16x32_bf16 v[6:9], v[158:161], v[202:205], v[6:9]
	v_mfma_f32_16x16x32_bf16 v[2:5], v[166:169], v[202:205], v[2:5]
	v_mfma_f32_16x16x32_bf16 v[46:49], v[162:165], v[178:181], v[46:49]
	v_mfma_f32_16x16x32_bf16 v[42:45], v[170:173], v[178:181], v[42:45]
	v_mfma_f32_16x16x32_bf16 v[30:33], v[162:165], v[186:189], v[30:33]
	v_mfma_f32_16x16x32_bf16 v[26:29], v[170:173], v[186:189], v[26:29]
	v_mfma_f32_16x16x32_bf16 v[14:17], v[162:165], v[198:201], v[14:17]
	v_mfma_f32_16x16x32_bf16 v[10:13], v[170:173], v[198:201], v[10:13]
	v_mfma_f32_16x16x32_bf16 v[6:9], v[162:165], v[206:209], v[6:9]
	v_mfma_f32_16x16x32_bf16 v[2:5], v[170:173], v[206:209], v[2:5]
	s_barrier
	s_setprio 0
	ds_read_b128 v[174:177], v138 offset:49152
	ds_read_b128 v[178:181], v138 offset:50176
	ds_read_b128 v[182:185], v138 offset:51200
	ds_read_b128 v[186:189], v138 offset:52224
	ds_read_b128 v[194:197], v138 offset:53248
	ds_read_b128 v[198:201], v138 offset:54272
	ds_read_b128 v[202:205], v138 offset:55296
	ds_read_b128 v[206:209], v138 offset:56320
	s_add_i32 s84, s86, s61
	v_lshl_add_u64 v[190:191], s[54:55], 0, v[0:1]
	v_lshl_add_u64 v[190:191], v[190:191], 0, s[16:17]
	s_mov_b32 m0, s84
	v_mov_b32_e32 v135, v1
	global_load_lds_dwordx4 v[190:191], off
	s_add_i32 m0, s84, 0x2000
	v_lshl_add_u64 v[190:191], s[54:55], 0, v[134:135]
	v_lshl_add_u64 v[190:191], v[190:191], 0, s[16:17]
	global_load_lds_dwordx4 v[190:191], off
	s_add_i32 s54, s87, s61
	v_lshl_add_u64 v[190:191], s[48:49], 0, v[0:1]
	v_lshl_add_u64 v[190:191], v[190:191], 0, s[16:17]
	s_mov_b32 m0, s54
	v_mov_b32_e32 v131, v1
	global_load_lds_dwordx4 v[190:191], off
	s_add_i32 m0, s54, 0x2000
	v_lshl_add_u64 v[190:191], s[48:49], 0, v[134:135]
	v_lshl_add_u64 v[190:191], v[190:191], 0, s[16:17]
	global_load_lds_dwordx4 v[190:191], off
	s_mov_b32 m0, s66
	v_lshl_add_u64 v[190:191], s[52:53], 0, v[130:131]
	v_lshl_add_u64 v[190:191], v[190:191], 0, s[16:17]
	v_mov_b32_e32 v133, v1
	global_load_lds_dwordx4 v[190:191], off
	s_mov_b32 m0, s67
	v_lshl_add_u64 v[190:191], s[52:53], 0, v[132:133]
	v_lshl_add_u64 v[190:191], v[190:191], 0, s[16:17]
	global_load_lds_dwordx4 v[190:191], off
	s_waitcnt vmcnt(8)
	s_waitcnt lgkmcnt(0)
	s_setprio 1
	s_barrier
	s_waitcnt lgkmcnt(0)
	v_mfma_f32_16x16x32_bf16 v[126:129], v[142:145], v[174:177], v[126:129]
	v_mfma_f32_16x16x32_bf16 v[122:125], v[150:153], v[174:177], v[122:125]
	v_mfma_f32_16x16x32_bf16 v[110:113], v[142:145], v[182:185], v[110:113]
	v_mfma_f32_16x16x32_bf16 v[106:109], v[150:153], v[182:185], v[106:109]
	v_mfma_f32_16x16x32_bf16 v[94:97], v[142:145], v[194:197], v[94:97]
	v_mfma_f32_16x16x32_bf16 v[90:93], v[150:153], v[194:197], v[90:93]
	v_mfma_f32_16x16x32_bf16 v[78:81], v[142:145], v[202:205], v[78:81]
	v_mfma_f32_16x16x32_bf16 v[74:77], v[150:153], v[202:205], v[74:77]
	v_mfma_f32_16x16x32_bf16 v[126:129], v[146:149], v[178:181], v[126:129]
	v_mfma_f32_16x16x32_bf16 v[122:125], v[154:157], v[178:181], v[122:125]
	v_mfma_f32_16x16x32_bf16 v[110:113], v[146:149], v[186:189], v[110:113]
	v_mfma_f32_16x16x32_bf16 v[106:109], v[154:157], v[186:189], v[106:109]
	v_mfma_f32_16x16x32_bf16 v[94:97], v[146:149], v[198:201], v[94:97]
	v_mfma_f32_16x16x32_bf16 v[90:93], v[154:157], v[198:201], v[90:93]
	v_mfma_f32_16x16x32_bf16 v[78:81], v[146:149], v[206:209], v[78:81]
	v_mfma_f32_16x16x32_bf16 v[74:77], v[154:157], v[206:209], v[74:77]
	v_mfma_f32_16x16x32_bf16 v[54:57], v[158:161], v[174:177], v[54:57]
	v_mfma_f32_16x16x32_bf16 v[50:53], v[166:169], v[174:177], v[50:53]
	v_mfma_f32_16x16x32_bf16 v[38:41], v[158:161], v[182:185], v[38:41]
	v_mfma_f32_16x16x32_bf16 v[34:37], v[166:169], v[182:185], v[34:37]
	v_mfma_f32_16x16x32_bf16 v[22:25], v[158:161], v[194:197], v[22:25]
	v_mfma_f32_16x16x32_bf16 v[18:21], v[166:169], v[194:197], v[18:21]
	v_mfma_f32_16x16x32_bf16 v[58:61], v[158:161], v[202:205], v[58:61]
	v_mfma_f32_16x16x32_bf16 v[62:65], v[166:169], v[202:205], v[62:65]
	v_mfma_f32_16x16x32_bf16 v[54:57], v[162:165], v[178:181], v[54:57]
	v_mfma_f32_16x16x32_bf16 v[50:53], v[170:173], v[178:181], v[50:53]
	v_mfma_f32_16x16x32_bf16 v[38:41], v[162:165], v[186:189], v[38:41]
	v_mfma_f32_16x16x32_bf16 v[34:37], v[170:173], v[186:189], v[34:37]
	v_mfma_f32_16x16x32_bf16 v[22:25], v[162:165], v[198:201], v[22:25]
	v_mfma_f32_16x16x32_bf16 v[18:21], v[170:173], v[198:201], v[18:21]
	v_mfma_f32_16x16x32_bf16 v[58:61], v[162:165], v[206:209], v[58:61]
	v_mfma_f32_16x16x32_bf16 v[62:65], v[170:173], v[206:209], v[62:65]
	s_barrier
	s_setprio 0
	s_add_u32 s81, s81, 0x100
	s_addc_u32 s82, s82, 0
	s_cmp_ge_i32 s83, s68
	s_mov_b64 s[48:49], s[50:51]
	s_mov_b32 s52, s83
	s_cbranch_scc0 .LBB0_498

.LBB0_531:
	s_add_i32 s81, s52, 2
	s_add_u32 s50, s48, 0x100
	s_addc_u32 s51, s49, 0
	s_add_i32 s82, 0, 0x10000
	s_cmp_eq_u32 s71, s52
	s_cselect_b32 s53, s43, s51
	s_cselect_b32 s52, s42, s50
	v_add_u32_e32 v131, s82, v137
	s_cselect_b32 s55, s45, s80
	s_cselect_b32 s54, s44, s47
	s_add_i32 s83, 0, 0x14000
	ds_read_b128 v[142:145], v131
	ds_read_b128 v[146:149], v131 offset:1024
	ds_read_b128 v[150:153], v131 offset:2048
	ds_read_b128 v[154:157], v131 offset:3072
	v_add_u32_e32 v131, s83, v137
	ds_read_b128 v[158:161], v131
	ds_read_b128 v[162:165], v131 offset:1024
	ds_read_b128 v[166:169], v131 offset:2048
	ds_read_b128 v[170:173], v131 offset:3072
	s_add_u32 s48, s48, s74
	s_addc_u32 s49, s49, s75
	s_add_i32 m0, s62, 0xc000
	ds_read_b128 v[174:177], v138
	ds_read_b128 v[178:181], v138 offset:1024
	ds_read_b128 v[182:185], v138 offset:2048
	ds_read_b128 v[186:189], v138 offset:3072
	ds_read_b128 v[194:197], v138 offset:4096
	ds_read_b128 v[198:201], v138 offset:5120
	ds_read_b128 v[202:205], v138 offset:6144
	ds_read_b128 v[206:209], v138 offset:7168
	s_nop 0
	global_load_lds_dwordx4 v130, s[48:49]
	s_add_i32 m0, s62, 0xe000
	s_nop 0
	global_load_lds_dwordx4 v132, s[48:49]
	s_waitcnt vmcnt(8)
	s_waitcnt lgkmcnt(0)
	s_setprio 1
	s_barrier
	s_waitcnt lgkmcnt(0)
	v_mfma_f32_16x16x32_bf16 v[118:121], v[142:145], v[174:177], v[118:121]
	v_mfma_f32_16x16x32_bf16 v[114:117], v[150:153], v[174:177], v[114:117]
	v_mfma_f32_16x16x32_bf16 v[102:105], v[142:145], v[182:185], v[102:105]
	v_mfma_f32_16x16x32_bf16 v[98:101], v[150:153], v[182:185], v[98:101]
	v_mfma_f32_16x16x32_bf16 v[86:89], v[142:145], v[194:197], v[86:89]
	v_mfma_f32_16x16x32_bf16 v[82:85], v[150:153], v[194:197], v[82:85]
	v_mfma_f32_16x16x32_bf16 v[70:73], v[142:145], v[202:205], v[70:73]
	v_mfma_f32_16x16x32_bf16 v[66:69], v[150:153], v[202:205], v[66:69]
	v_mfma_f32_16x16x32_bf16 v[118:121], v[146:149], v[178:181], v[118:121]
	v_mfma_f32_16x16x32_bf16 v[114:117], v[154:157], v[178:181], v[114:117]
	v_mfma_f32_16x16x32_bf16 v[102:105], v[146:149], v[186:189], v[102:105]
	v_mfma_f32_16x16x32_bf16 v[98:101], v[154:157], v[186:189], v[98:101]
	v_mfma_f32_16x16x32_bf16 v[86:89], v[146:149], v[198:201], v[86:89]
	v_mfma_f32_16x16x32_bf16 v[82:85], v[154:157], v[198:201], v[82:85]
	v_mfma_f32_16x16x32_bf16 v[70:73], v[146:149], v[206:209], v[70:73]
	v_mfma_f32_16x16x32_bf16 v[66:69], v[154:157], v[206:209], v[66:69]
	v_mfma_f32_16x16x32_bf16 v[46:49], v[158:161], v[174:177], v[46:49]
	v_mfma_f32_16x16x32_bf16 v[42:45], v[166:169], v[174:177], v[42:45]
	v_mfma_f32_16x16x32_bf16 v[30:33], v[158:161], v[182:185], v[30:33]
	v_mfma_f32_16x16x32_bf16 v[26:29], v[166:169], v[182:185], v[26:29]
	v_mfma_f32_16x16x32_bf16 v[14:17], v[158:161], v[194:197], v[14:17]
	v_mfma_f32_16x16x32_bf16 v[10:13], v[166:169], v[194:197], v[10:13]
	v_mfma_f32_16x16x32_bf16 v[6:9], v[158:161], v[202:205], v[6:9]
	v_mfma_f32_16x16x32_bf16 v[2:5], v[166:169], v[202:205], v[2:5]
	v_mfma_f32_16x16x32_bf16 v[46:49], v[162:165], v[178:181], v[46:49]
	v_mfma_f32_16x16x32_bf16 v[42:45], v[170:173], v[178:181], v[42:45]
	v_mfma_f32_16x16x32_bf16 v[30:33], v[162:165], v[186:189], v[30:33]
	v_mfma_f32_16x16x32_bf16 v[26:29], v[170:173], v[186:189], v[26:29]
	v_mfma_f32_16x16x32_bf16 v[14:17], v[162:165], v[198:201], v[14:17]
	v_mfma_f32_16x16x32_bf16 v[10:13], v[170:173], v[198:201], v[10:13]
	v_mfma_f32_16x16x32_bf16 v[6:9], v[162:165], v[206:209], v[6:9]
	v_mfma_f32_16x16x32_bf16 v[2:5], v[170:173], v[206:209], v[2:5]
	s_barrier
	s_setprio 0
	s_add_i32 s48, s82, s61
	s_mov_b32 m0, s48
	ds_read_b128 v[174:177], v138 offset:16384
	ds_read_b128 v[178:181], v138 offset:17408
	ds_read_b128 v[182:185], v138 offset:18432
	ds_read_b128 v[186:189], v138 offset:19456
	ds_read_b128 v[194:197], v138 offset:20480
	ds_read_b128 v[198:201], v138 offset:21504
	ds_read_b128 v[202:205], v138 offset:22528
	ds_read_b128 v[206:209], v138 offset:23552
	s_nop 0
	global_load_lds_dwordx4 v0, s[54:55]
	s_add_i32 m0, s48, 0x2000
	s_add_u32 s48, s54, s26
	s_addc_u32 s49, s55, s27
	s_add_i32 s82, s83, s61
	s_nop 0
	global_load_lds_dwordx4 v134, s[54:55]
	s_mov_b32 m0, s82
	s_nop 0
	global_load_lds_dwordx4 v0, s[48:49]
	s_add_i32 m0, s82, 0x2000
	s_nop 0
	global_load_lds_dwordx4 v134, s[48:49]
	s_mov_b32 m0, s62
	s_nop 0
	global_load_lds_dwordx4 v130, s[52:53]
	s_mov_b32 m0, s63
	s_nop 0
	global_load_lds_dwordx4 v132, s[52:53]
	s_waitcnt vmcnt(8)
	s_waitcnt lgkmcnt(0)
	s_setprio 1
	s_barrier
	s_waitcnt lgkmcnt(0)
	v_mfma_f32_16x16x32_bf16 v[126:129], v[142:145], v[174:177], v[126:129]
	v_mfma_f32_16x16x32_bf16 v[122:125], v[150:153], v[174:177], v[122:125]
	v_mfma_f32_16x16x32_bf16 v[110:113], v[142:145], v[182:185], v[110:113]
	v_mfma_f32_16x16x32_bf16 v[106:109], v[150:153], v[182:185], v[106:109]
	v_mfma_f32_16x16x32_bf16 v[94:97], v[142:145], v[194:197], v[94:97]
	v_mfma_f32_16x16x32_bf16 v[90:93], v[150:153], v[194:197], v[90:93]
	v_mfma_f32_16x16x32_bf16 v[78:81], v[142:145], v[202:205], v[78:81]
	v_mfma_f32_16x16x32_bf16 v[74:77], v[150:153], v[202:205], v[74:77]
	v_mfma_f32_16x16x32_bf16 v[126:129], v[146:149], v[178:181], v[126:129]
	v_mfma_f32_16x16x32_bf16 v[122:125], v[154:157], v[178:181], v[122:125]
	v_mfma_f32_16x16x32_bf16 v[110:113], v[146:149], v[186:189], v[110:113]
	v_mfma_f32_16x16x32_bf16 v[106:109], v[154:157], v[186:189], v[106:109]
	v_mfma_f32_16x16x32_bf16 v[94:97], v[146:149], v[198:201], v[94:97]
	v_mfma_f32_16x16x32_bf16 v[90:93], v[154:157], v[198:201], v[90:93]
	v_mfma_f32_16x16x32_bf16 v[78:81], v[146:149], v[206:209], v[78:81]
	v_mfma_f32_16x16x32_bf16 v[74:77], v[154:157], v[206:209], v[74:77]
	v_mfma_f32_16x16x32_bf16 v[54:57], v[158:161], v[174:177], v[54:57]
	v_mfma_f32_16x16x32_bf16 v[50:53], v[166:169], v[174:177], v[50:53]
	v_mfma_f32_16x16x32_bf16 v[38:41], v[158:161], v[182:185], v[38:41]
	v_mfma_f32_16x16x32_bf16 v[34:37], v[166:169], v[182:185], v[34:37]
	v_mfma_f32_16x16x32_bf16 v[22:25], v[158:161], v[194:197], v[22:25]
	v_mfma_f32_16x16x32_bf16 v[18:21], v[166:169], v[194:197], v[18:21]
	v_mfma_f32_16x16x32_bf16 v[58:61], v[158:161], v[202:205], v[58:61]
	v_mfma_f32_16x16x32_bf16 v[62:65], v[166:169], v[202:205], v[62:65]
	v_mfma_f32_16x16x32_bf16 v[54:57], v[162:165], v[178:181], v[54:57]
	v_mfma_f32_16x16x32_bf16 v[50:53], v[170:173], v[178:181], v[50:53]
	v_mfma_f32_16x16x32_bf16 v[38:41], v[162:165], v[186:189], v[38:41]
	v_mfma_f32_16x16x32_bf16 v[34:37], v[170:173], v[186:189], v[34:37]
	v_mfma_f32_16x16x32_bf16 v[22:25], v[162:165], v[198:201], v[22:25]
	v_mfma_f32_16x16x32_bf16 v[18:21], v[170:173], v[198:201], v[18:21]
	v_mfma_f32_16x16x32_bf16 v[58:61], v[162:165], v[206:209], v[58:61]
	v_mfma_f32_16x16x32_bf16 v[62:65], v[170:173], v[206:209], v[62:65]
	s_barrier
	s_setprio 0
	s_add_i32 s84, 0, 0x18000
	v_add_u32_e32 v131, s84, v137
	s_add_i32 s85, 0, 0x1c000
	ds_read_b128 v[142:145], v131
	ds_read_b128 v[146:149], v131 offset:1024
	ds_read_b128 v[150:153], v131 offset:2048
	ds_read_b128 v[154:157], v131 offset:3072
	v_add_u32_e32 v131, s85, v137
	ds_read_b128 v[158:161], v131
	ds_read_b128 v[162:165], v131 offset:1024
	ds_read_b128 v[166:169], v131 offset:2048
	ds_read_b128 v[170:173], v131 offset:3072
	s_add_u32 s82, s52, s26
	s_addc_u32 s83, s53, s27
	s_mov_b32 m0, s64
	ds_read_b128 v[174:177], v138 offset:32768
	ds_read_b128 v[178:181], v138 offset:33792
	ds_read_b128 v[182:185], v138 offset:34816
	ds_read_b128 v[186:189], v138 offset:35840
	ds_read_b128 v[194:197], v138 offset:36864
	ds_read_b128 v[198:201], v138 offset:37888
	ds_read_b128 v[202:205], v138 offset:38912
	ds_read_b128 v[206:209], v138 offset:39936
	s_nop 0
	global_load_lds_dwordx4 v130, s[82:83]
	s_mov_b32 m0, s65
	s_nop 0
	global_load_lds_dwordx4 v132, s[82:83]
	s_waitcnt vmcnt(8)
	s_waitcnt lgkmcnt(0)
	s_setprio 1
	s_barrier
	s_waitcnt lgkmcnt(0)
	v_mfma_f32_16x16x32_bf16 v[118:121], v[142:145], v[174:177], v[118:121]
	v_mfma_f32_16x16x32_bf16 v[114:117], v[150:153], v[174:177], v[114:117]
	v_mfma_f32_16x16x32_bf16 v[102:105], v[142:145], v[182:185], v[102:105]
	v_mfma_f32_16x16x32_bf16 v[98:101], v[150:153], v[182:185], v[98:101]
	v_mfma_f32_16x16x32_bf16 v[86:89], v[142:145], v[194:197], v[86:89]
	v_mfma_f32_16x16x32_bf16 v[82:85], v[150:153], v[194:197], v[82:85]
	v_mfma_f32_16x16x32_bf16 v[70:73], v[142:145], v[202:205], v[70:73]
	v_mfma_f32_16x16x32_bf16 v[66:69], v[150:153], v[202:205], v[66:69]
	v_mfma_f32_16x16x32_bf16 v[118:121], v[146:149], v[178:181], v[118:121]
	v_mfma_f32_16x16x32_bf16 v[114:117], v[154:157], v[178:181], v[114:117]
	v_mfma_f32_16x16x32_bf16 v[102:105], v[146:149], v[186:189], v[102:105]
	v_mfma_f32_16x16x32_bf16 v[98:101], v[154:157], v[186:189], v[98:101]
	v_mfma_f32_16x16x32_bf16 v[86:89], v[146:149], v[198:201], v[86:89]
	v_mfma_f32_16x16x32_bf16 v[82:85], v[154:157], v[198:201], v[82:85]
	v_mfma_f32_16x16x32_bf16 v[70:73], v[146:149], v[206:209], v[70:73]
	v_mfma_f32_16x16x32_bf16 v[66:69], v[154:157], v[206:209], v[66:69]
	v_mfma_f32_16x16x32_bf16 v[46:49], v[158:161], v[174:177], v[46:49]
	v_mfma_f32_16x16x32_bf16 v[42:45], v[166:169], v[174:177], v[42:45]
	v_mfma_f32_16x16x32_bf16 v[30:33], v[158:161], v[182:185], v[30:33]
	v_mfma_f32_16x16x32_bf16 v[26:29], v[166:169], v[182:185], v[26:29]
	v_mfma_f32_16x16x32_bf16 v[14:17], v[158:161], v[194:197], v[14:17]
	v_mfma_f32_16x16x32_bf16 v[10:13], v[166:169], v[194:197], v[10:13]
	v_mfma_f32_16x16x32_bf16 v[6:9], v[158:161], v[202:205], v[6:9]
	v_mfma_f32_16x16x32_bf16 v[2:5], v[166:169], v[202:205], v[2:5]
	v_mfma_f32_16x16x32_bf16 v[46:49], v[162:165], v[178:181], v[46:49]
	v_mfma_f32_16x16x32_bf16 v[42:45], v[170:173], v[178:181], v[42:45]
	v_mfma_f32_16x16x32_bf16 v[30:33], v[162:165], v[186:189], v[30:33]
	v_mfma_f32_16x16x32_bf16 v[26:29], v[170:173], v[186:189], v[26:29]
	v_mfma_f32_16x16x32_bf16 v[14:17], v[162:165], v[198:201], v[14:17]
	v_mfma_f32_16x16x32_bf16 v[10:13], v[170:173], v[198:201], v[10:13]
	v_mfma_f32_16x16x32_bf16 v[6:9], v[162:165], v[206:209], v[6:9]
	v_mfma_f32_16x16x32_bf16 v[2:5], v[170:173], v[206:209], v[2:5]
	s_barrier
	s_setprio 0
	ds_read_b128 v[174:177], v138 offset:49152
	ds_read_b128 v[178:181], v138 offset:50176
	ds_read_b128 v[182:185], v138 offset:51200
	ds_read_b128 v[186:189], v138 offset:52224
	ds_read_b128 v[194:197], v138 offset:53248
	ds_read_b128 v[198:201], v138 offset:54272
	ds_read_b128 v[202:205], v138 offset:55296
	ds_read_b128 v[206:209], v138 offset:56320
	s_add_i32 s82, s84, s61
	v_lshl_add_u64 v[190:191], s[54:55], 0, v[0:1]
	v_lshl_add_u64 v[190:191], v[190:191], 0, s[16:17]
	s_mov_b32 m0, s82
	v_mov_b32_e32 v135, v1
	global_load_lds_dwordx4 v[190:191], off
	s_add_i32 m0, s82, 0x2000
	v_lshl_add_u64 v[190:191], s[54:55], 0, v[134:135]
	v_lshl_add_u64 v[190:191], v[190:191], 0, s[16:17]
	global_load_lds_dwordx4 v[190:191], off
	s_add_i32 s54, s85, s61
	v_lshl_add_u64 v[190:191], s[48:49], 0, v[0:1]
	v_lshl_add_u64 v[190:191], v[190:191], 0, s[16:17]
	s_mov_b32 m0, s54
	v_mov_b32_e32 v131, v1
	global_load_lds_dwordx4 v[190:191], off
	s_add_i32 m0, s54, 0x2000
	v_lshl_add_u64 v[190:191], s[48:49], 0, v[134:135]
	v_lshl_add_u64 v[190:191], v[190:191], 0, s[16:17]
	global_load_lds_dwordx4 v[190:191], off
	s_mov_b32 m0, s66
	v_lshl_add_u64 v[190:191], s[52:53], 0, v[130:131]
	v_lshl_add_u64 v[190:191], v[190:191], 0, s[16:17]
	v_mov_b32_e32 v133, v1
	global_load_lds_dwordx4 v[190:191], off
	s_mov_b32 m0, s67
	v_lshl_add_u64 v[190:191], s[52:53], 0, v[132:133]
	v_lshl_add_u64 v[190:191], v[190:191], 0, s[16:17]
	global_load_lds_dwordx4 v[190:191], off
	s_waitcnt vmcnt(8)
	s_waitcnt lgkmcnt(0)
	s_setprio 1
	s_barrier
	s_waitcnt lgkmcnt(0)
	v_mfma_f32_16x16x32_bf16 v[126:129], v[142:145], v[174:177], v[126:129]
	v_mfma_f32_16x16x32_bf16 v[122:125], v[150:153], v[174:177], v[122:125]
	v_mfma_f32_16x16x32_bf16 v[110:113], v[142:145], v[182:185], v[110:113]
	v_mfma_f32_16x16x32_bf16 v[106:109], v[150:153], v[182:185], v[106:109]
	v_mfma_f32_16x16x32_bf16 v[94:97], v[142:145], v[194:197], v[94:97]
	v_mfma_f32_16x16x32_bf16 v[90:93], v[150:153], v[194:197], v[90:93]
	v_mfma_f32_16x16x32_bf16 v[78:81], v[142:145], v[202:205], v[78:81]
	v_mfma_f32_16x16x32_bf16 v[74:77], v[150:153], v[202:205], v[74:77]
	v_mfma_f32_16x16x32_bf16 v[126:129], v[146:149], v[178:181], v[126:129]
	v_mfma_f32_16x16x32_bf16 v[122:125], v[154:157], v[178:181], v[122:125]
	v_mfma_f32_16x16x32_bf16 v[110:113], v[146:149], v[186:189], v[110:113]
	v_mfma_f32_16x16x32_bf16 v[106:109], v[154:157], v[186:189], v[106:109]
	v_mfma_f32_16x16x32_bf16 v[94:97], v[146:149], v[198:201], v[94:97]
	v_mfma_f32_16x16x32_bf16 v[90:93], v[154:157], v[198:201], v[90:93]
	v_mfma_f32_16x16x32_bf16 v[78:81], v[146:149], v[206:209], v[78:81]
	v_mfma_f32_16x16x32_bf16 v[74:77], v[154:157], v[206:209], v[74:77]
	v_mfma_f32_16x16x32_bf16 v[54:57], v[158:161], v[174:177], v[54:57]
	v_mfma_f32_16x16x32_bf16 v[50:53], v[166:169], v[174:177], v[50:53]
	v_mfma_f32_16x16x32_bf16 v[38:41], v[158:161], v[182:185], v[38:41]
	v_mfma_f32_16x16x32_bf16 v[34:37], v[166:169], v[182:185], v[34:37]
	v_mfma_f32_16x16x32_bf16 v[22:25], v[158:161], v[194:197], v[22:25]
	v_mfma_f32_16x16x32_bf16 v[18:21], v[166:169], v[194:197], v[18:21]
	v_mfma_f32_16x16x32_bf16 v[58:61], v[158:161], v[202:205], v[58:61]
	v_mfma_f32_16x16x32_bf16 v[62:65], v[166:169], v[202:205], v[62:65]
	v_mfma_f32_16x16x32_bf16 v[54:57], v[162:165], v[178:181], v[54:57]
	v_mfma_f32_16x16x32_bf16 v[50:53], v[170:173], v[178:181], v[50:53]
	v_mfma_f32_16x16x32_bf16 v[38:41], v[162:165], v[186:189], v[38:41]
	v_mfma_f32_16x16x32_bf16 v[34:37], v[170:173], v[186:189], v[34:37]
	v_mfma_f32_16x16x32_bf16 v[22:25], v[162:165], v[198:201], v[22:25]
	v_mfma_f32_16x16x32_bf16 v[18:21], v[170:173], v[198:201], v[18:21]
	v_mfma_f32_16x16x32_bf16 v[58:61], v[162:165], v[206:209], v[58:61]
	v_mfma_f32_16x16x32_bf16 v[62:65], v[170:173], v[206:209], v[62:65]
	s_barrier
	s_setprio 0
	s_add_u32 s47, s47, 0x100
	s_addc_u32 s80, s80, 0
	s_cmp_ge_i32 s81, s68
	s_mov_b64 s[48:49], s[50:51]
	s_mov_b32 s52, s81
	s_cbranch_scc0 .LBB0_531

.LBB0_707:
	s_add_i32 s74, s52, 2
	s_add_u32 s50, s48, 0x100
	s_addc_u32 s51, s49, 0
	s_add_i32 s75, 0, 0x10000
	s_cmp_eq_u32 s64, s52
	s_cselect_b32 s53, s41, s51
	s_cselect_b32 s52, s40, s50
	v_add_u32_e32 v139, s75, v148
	s_cselect_b32 s55, s47, s73
	s_cselect_b32 s54, s46, s72
	s_add_i32 s76, 0, 0x14000
	ds_read_b128 v[130:133], v139
	ds_read_b128 v[134:137], v139 offset:1024
	ds_read_b128 v[140:143], v139 offset:2048
	ds_read_b128 v[150:153], v139 offset:3072
	v_add_u32_e32 v139, s76, v148
	ds_read_b128 v[154:157], v139
	ds_read_b128 v[158:161], v139 offset:1024
	ds_read_b128 v[162:165], v139 offset:2048
	ds_read_b128 v[166:169], v139 offset:3072
	s_add_u32 s48, s48, s66
	s_addc_u32 s49, s49, s67
	s_add_i32 m0, s15, 0xc000
	ds_read_b128 v[170:173], v149
	ds_read_b128 v[174:177], v149 offset:1024
	ds_read_b128 v[178:181], v149 offset:2048
	ds_read_b128 v[182:185], v149 offset:3072
	ds_read_b128 v[186:189], v149 offset:4096
	ds_read_b128 v[194:197], v149 offset:5120
	ds_read_b128 v[198:201], v149 offset:6144
	ds_read_b128 v[202:205], v149 offset:7168
	s_nop 0
	global_load_lds_dwordx4 v0, s[48:49]
	s_add_i32 m0, s15, 0xe000
	s_nop 0
	global_load_lds_dwordx4 v138, s[48:49]
	s_waitcnt vmcnt(8)
	s_waitcnt lgkmcnt(0)
	s_setprio 1
	s_barrier
	s_waitcnt lgkmcnt(0)
	v_mfma_f32_16x16x32_bf16 v[122:125], v[130:133], v[170:173], v[122:125]
	v_mfma_f32_16x16x32_bf16 v[126:129], v[140:143], v[170:173], v[126:129]
	v_mfma_f32_16x16x32_bf16 v[118:121], v[130:133], v[178:181], v[118:121]
	v_mfma_f32_16x16x32_bf16 v[114:117], v[140:143], v[178:181], v[114:117]
	v_mfma_f32_16x16x32_bf16 v[102:105], v[130:133], v[186:189], v[102:105]
	v_mfma_f32_16x16x32_bf16 v[98:101], v[140:143], v[186:189], v[98:101]
	v_mfma_f32_16x16x32_bf16 v[86:89], v[130:133], v[198:201], v[86:89]
	v_mfma_f32_16x16x32_bf16 v[82:85], v[140:143], v[198:201], v[82:85]
	v_mfma_f32_16x16x32_bf16 v[122:125], v[134:137], v[174:177], v[122:125]
	v_mfma_f32_16x16x32_bf16 v[126:129], v[150:153], v[174:177], v[126:129]
	v_mfma_f32_16x16x32_bf16 v[118:121], v[134:137], v[182:185], v[118:121]
	v_mfma_f32_16x16x32_bf16 v[114:117], v[150:153], v[182:185], v[114:117]
	v_mfma_f32_16x16x32_bf16 v[102:105], v[134:137], v[194:197], v[102:105]
	v_mfma_f32_16x16x32_bf16 v[98:101], v[150:153], v[194:197], v[98:101]
	v_mfma_f32_16x16x32_bf16 v[86:89], v[134:137], v[202:205], v[86:89]
	v_mfma_f32_16x16x32_bf16 v[82:85], v[150:153], v[202:205], v[82:85]
	v_mfma_f32_16x16x32_bf16 v[58:61], v[154:157], v[170:173], v[58:61]
	v_mfma_f32_16x16x32_bf16 v[62:65], v[162:165], v[170:173], v[62:65]
	v_mfma_f32_16x16x32_bf16 v[54:57], v[154:157], v[178:181], v[54:57]
	v_mfma_f32_16x16x32_bf16 v[50:53], v[162:165], v[178:181], v[50:53]
	v_mfma_f32_16x16x32_bf16 v[38:41], v[154:157], v[186:189], v[38:41]
	v_mfma_f32_16x16x32_bf16 v[34:37], v[162:165], v[186:189], v[34:37]
	v_mfma_f32_16x16x32_bf16 v[14:17], v[154:157], v[198:201], v[14:17]
	v_mfma_f32_16x16x32_bf16 v[10:13], v[162:165], v[198:201], v[10:13]
	v_mfma_f32_16x16x32_bf16 v[58:61], v[158:161], v[174:177], v[58:61]
	v_mfma_f32_16x16x32_bf16 v[62:65], v[166:169], v[174:177], v[62:65]
	v_mfma_f32_16x16x32_bf16 v[54:57], v[158:161], v[182:185], v[54:57]
	v_mfma_f32_16x16x32_bf16 v[50:53], v[166:169], v[182:185], v[50:53]
	v_mfma_f32_16x16x32_bf16 v[38:41], v[158:161], v[194:197], v[38:41]
	v_mfma_f32_16x16x32_bf16 v[34:37], v[166:169], v[194:197], v[34:37]
	v_mfma_f32_16x16x32_bf16 v[14:17], v[158:161], v[202:205], v[14:17]
	v_mfma_f32_16x16x32_bf16 v[10:13], v[166:169], v[202:205], v[10:13]
	s_barrier
	s_setprio 0
	s_add_i32 s48, s75, s14
	s_mov_b32 m0, s48
	ds_read_b128 v[170:173], v149 offset:16384
	ds_read_b128 v[174:177], v149 offset:17408
	ds_read_b128 v[178:181], v149 offset:18432
	ds_read_b128 v[182:185], v149 offset:19456
	ds_read_b128 v[186:189], v149 offset:20480
	ds_read_b128 v[194:197], v149 offset:21504
	ds_read_b128 v[198:201], v149 offset:22528
	ds_read_b128 v[202:205], v149 offset:23552
	s_nop 0
	global_load_lds_dwordx4 v147, s[54:55]
	s_add_i32 m0, s48, 0x2000
	s_add_u32 s48, s54, 0x4000
	s_addc_u32 s49, s55, 0
	s_add_i32 s75, s76, s14
	s_nop 0
	global_load_lds_dwordx4 v146, s[54:55]
	s_mov_b32 m0, s75
	s_nop 0
	global_load_lds_dwordx4 v147, s[48:49]
	s_add_i32 m0, s75, 0x2000
	s_nop 0
	global_load_lds_dwordx4 v146, s[48:49]
	s_mov_b32 m0, s15
	s_nop 0
	global_load_lds_dwordx4 v0, s[52:53]
	s_mov_b32 m0, s18
	s_nop 0
	global_load_lds_dwordx4 v138, s[52:53]
	s_waitcnt vmcnt(8)
	s_waitcnt lgkmcnt(0)
	s_setprio 1
	s_barrier
	s_waitcnt lgkmcnt(0)
	v_mfma_f32_16x16x32_bf16 v[110:113], v[130:133], v[170:173], v[110:113]
	v_mfma_f32_16x16x32_bf16 v[106:109], v[140:143], v[170:173], v[106:109]
	v_mfma_f32_16x16x32_bf16 v[94:97], v[130:133], v[178:181], v[94:97]
	v_mfma_f32_16x16x32_bf16 v[90:93], v[140:143], v[178:181], v[90:93]
	v_mfma_f32_16x16x32_bf16 v[78:81], v[130:133], v[186:189], v[78:81]
	v_mfma_f32_16x16x32_bf16 v[74:77], v[140:143], v[186:189], v[74:77]
	v_mfma_f32_16x16x32_bf16 v[70:73], v[130:133], v[198:201], v[70:73]
	v_mfma_f32_16x16x32_bf16 v[66:69], v[140:143], v[198:201], v[66:69]
	v_mfma_f32_16x16x32_bf16 v[110:113], v[134:137], v[174:177], v[110:113]
	v_mfma_f32_16x16x32_bf16 v[106:109], v[150:153], v[174:177], v[106:109]
	v_mfma_f32_16x16x32_bf16 v[94:97], v[134:137], v[182:185], v[94:97]
	v_mfma_f32_16x16x32_bf16 v[90:93], v[150:153], v[182:185], v[90:93]
	v_mfma_f32_16x16x32_bf16 v[78:81], v[134:137], v[194:197], v[78:81]
	v_mfma_f32_16x16x32_bf16 v[74:77], v[150:153], v[194:197], v[74:77]
	v_mfma_f32_16x16x32_bf16 v[70:73], v[134:137], v[202:205], v[70:73]
	v_mfma_f32_16x16x32_bf16 v[66:69], v[150:153], v[202:205], v[66:69]
	v_mfma_f32_16x16x32_bf16 v[46:49], v[154:157], v[170:173], v[46:49]
	v_mfma_f32_16x16x32_bf16 v[42:45], v[162:165], v[170:173], v[42:45]
	v_mfma_f32_16x16x32_bf16 v[26:29], v[154:157], v[178:181], v[26:29]
	v_mfma_f32_16x16x32_bf16 v[22:25], v[162:165], v[178:181], v[22:25]
	v_mfma_f32_16x16x32_bf16 v[6:9], v[154:157], v[186:189], v[6:9]
	v_mfma_f32_16x16x32_bf16 v[2:5], v[162:165], v[186:189], v[2:5]
	v_mfma_f32_16x16x32_bf16 v[18:21], v[154:157], v[198:201], v[18:21]
	v_mfma_f32_16x16x32_bf16 v[30:33], v[162:165], v[198:201], v[30:33]
	v_mfma_f32_16x16x32_bf16 v[46:49], v[158:161], v[174:177], v[46:49]
	v_mfma_f32_16x16x32_bf16 v[42:45], v[166:169], v[174:177], v[42:45]
	v_mfma_f32_16x16x32_bf16 v[26:29], v[158:161], v[182:185], v[26:29]
	v_mfma_f32_16x16x32_bf16 v[22:25], v[166:169], v[182:185], v[22:25]
	v_mfma_f32_16x16x32_bf16 v[6:9], v[158:161], v[194:197], v[6:9]
	v_mfma_f32_16x16x32_bf16 v[2:5], v[166:169], v[194:197], v[2:5]
	v_mfma_f32_16x16x32_bf16 v[18:21], v[158:161], v[202:205], v[18:21]
	v_mfma_f32_16x16x32_bf16 v[30:33], v[166:169], v[202:205], v[30:33]
	s_barrier
	s_setprio 0
	s_add_i32 s75, 0, 0x18000
	v_add_u32_e32 v139, s75, v148
	s_add_i32 s76, 0, 0x1c000
	ds_read_b128 v[130:133], v139
	ds_read_b128 v[134:137], v139 offset:1024
	ds_read_b128 v[140:143], v139 offset:2048
	ds_read_b128 v[150:153], v139 offset:3072
	v_add_u32_e32 v139, s76, v148
	ds_read_b128 v[154:157], v139
	ds_read_b128 v[158:161], v139 offset:1024
	ds_read_b128 v[162:165], v139 offset:2048
	ds_read_b128 v[166:169], v139 offset:3072
	s_add_u32 s48, s52, s26
	s_addc_u32 s49, s53, s27
	s_mov_b32 m0, s20
	ds_read_b128 v[170:173], v149 offset:32768
	ds_read_b128 v[174:177], v149 offset:33792
	ds_read_b128 v[178:181], v149 offset:34816
	ds_read_b128 v[182:185], v149 offset:35840
	ds_read_b128 v[186:189], v149 offset:36864
	ds_read_b128 v[194:197], v149 offset:37888
	ds_read_b128 v[198:201], v149 offset:38912
	ds_read_b128 v[202:205], v149 offset:39936
	s_nop 0
	global_load_lds_dwordx4 v0, s[48:49]
	s_mov_b32 m0, s21
	s_nop 0
	global_load_lds_dwordx4 v138, s[48:49]
	s_waitcnt vmcnt(8)
	s_waitcnt lgkmcnt(0)
	s_setprio 1
	s_barrier
	s_waitcnt lgkmcnt(0)
	v_mfma_f32_16x16x32_bf16 v[122:125], v[130:133], v[170:173], v[122:125]
	v_mfma_f32_16x16x32_bf16 v[126:129], v[140:143], v[170:173], v[126:129]
	v_mfma_f32_16x16x32_bf16 v[118:121], v[130:133], v[178:181], v[118:121]
	v_mfma_f32_16x16x32_bf16 v[114:117], v[140:143], v[178:181], v[114:117]
	v_mfma_f32_16x16x32_bf16 v[102:105], v[130:133], v[186:189], v[102:105]
	v_mfma_f32_16x16x32_bf16 v[98:101], v[140:143], v[186:189], v[98:101]
	v_mfma_f32_16x16x32_bf16 v[86:89], v[130:133], v[198:201], v[86:89]
	v_mfma_f32_16x16x32_bf16 v[82:85], v[140:143], v[198:201], v[82:85]
	v_mfma_f32_16x16x32_bf16 v[122:125], v[134:137], v[174:177], v[122:125]
	v_mfma_f32_16x16x32_bf16 v[126:129], v[150:153], v[174:177], v[126:129]
	v_mfma_f32_16x16x32_bf16 v[118:121], v[134:137], v[182:185], v[118:121]
	v_mfma_f32_16x16x32_bf16 v[114:117], v[150:153], v[182:185], v[114:117]
	v_mfma_f32_16x16x32_bf16 v[102:105], v[134:137], v[194:197], v[102:105]
	v_mfma_f32_16x16x32_bf16 v[98:101], v[150:153], v[194:197], v[98:101]
	v_mfma_f32_16x16x32_bf16 v[86:89], v[134:137], v[202:205], v[86:89]
	v_mfma_f32_16x16x32_bf16 v[82:85], v[150:153], v[202:205], v[82:85]
	v_mfma_f32_16x16x32_bf16 v[58:61], v[154:157], v[170:173], v[58:61]
	v_mfma_f32_16x16x32_bf16 v[62:65], v[162:165], v[170:173], v[62:65]
	v_mfma_f32_16x16x32_bf16 v[54:57], v[154:157], v[178:181], v[54:57]
	v_mfma_f32_16x16x32_bf16 v[50:53], v[162:165], v[178:181], v[50:53]
	v_mfma_f32_16x16x32_bf16 v[38:41], v[154:157], v[186:189], v[38:41]
	v_mfma_f32_16x16x32_bf16 v[34:37], v[162:165], v[186:189], v[34:37]
	v_mfma_f32_16x16x32_bf16 v[14:17], v[154:157], v[198:201], v[14:17]
	v_mfma_f32_16x16x32_bf16 v[10:13], v[162:165], v[198:201], v[10:13]
	v_mfma_f32_16x16x32_bf16 v[58:61], v[158:161], v[174:177], v[58:61]
	v_mfma_f32_16x16x32_bf16 v[62:65], v[166:169], v[174:177], v[62:65]
	v_mfma_f32_16x16x32_bf16 v[54:57], v[158:161], v[182:185], v[54:57]
	v_mfma_f32_16x16x32_bf16 v[50:53], v[166:169], v[182:185], v[50:53]
	v_mfma_f32_16x16x32_bf16 v[38:41], v[158:161], v[194:197], v[38:41]
	v_mfma_f32_16x16x32_bf16 v[34:37], v[166:169], v[194:197], v[34:37]
	v_mfma_f32_16x16x32_bf16 v[14:17], v[158:161], v[202:205], v[14:17]
	v_mfma_f32_16x16x32_bf16 v[10:13], v[166:169], v[202:205], v[10:13]
	s_barrier
	s_setprio 0
	s_add_u32 s48, s54, 0x8000
	s_addc_u32 s49, s55, 0
	s_add_i32 s75, s75, s14
	s_mov_b32 m0, s75
	ds_read_b128 v[170:173], v149 offset:49152
	ds_read_b128 v[174:177], v149 offset:50176
	ds_read_b128 v[178:181], v149 offset:51200
	ds_read_b128 v[182:185], v149 offset:52224
	ds_read_b128 v[186:189], v149 offset:53248
	ds_read_b128 v[194:197], v149 offset:54272
	ds_read_b128 v[198:201], v149 offset:55296
	ds_read_b128 v[202:205], v149 offset:56320
	v_mov_b32_e32 v139, v1
	global_load_lds_dwordx4 v147, s[48:49]
	s_add_i32 m0, s75, 0x2000
	s_nop 0
	global_load_lds_dwordx4 v146, s[48:49]
	s_add_u32 s48, s54, 0xc000
	s_addc_u32 s49, s55, 0
	s_add_i32 s54, s76, s14
	s_mov_b32 m0, s54
	s_nop 0
	global_load_lds_dwordx4 v147, s[48:49]
	s_add_i32 m0, s54, 0x2000
	s_nop 0
	global_load_lds_dwordx4 v146, s[48:49]
	s_mov_b32 m0, s62
	v_lshl_add_u64 v[190:191], s[52:53], 0, v[0:1]
	v_lshl_add_u64 v[190:191], v[190:191], 0, s[16:17]
	global_load_lds_dwordx4 v[190:191], off
	s_mov_b32 m0, s63
	v_lshl_add_u64 v[190:191], s[52:53], 0, v[138:139]
	v_lshl_add_u64 v[190:191], v[190:191], 0, s[16:17]
	global_load_lds_dwordx4 v[190:191], off
	s_waitcnt vmcnt(8)
	s_waitcnt lgkmcnt(0)
	s_setprio 1
	s_barrier
	s_waitcnt lgkmcnt(0)
	v_mfma_f32_16x16x32_bf16 v[110:113], v[130:133], v[170:173], v[110:113]
	v_mfma_f32_16x16x32_bf16 v[106:109], v[140:143], v[170:173], v[106:109]
	v_mfma_f32_16x16x32_bf16 v[94:97], v[130:133], v[178:181], v[94:97]
	v_mfma_f32_16x16x32_bf16 v[90:93], v[140:143], v[178:181], v[90:93]
	v_mfma_f32_16x16x32_bf16 v[78:81], v[130:133], v[186:189], v[78:81]
	v_mfma_f32_16x16x32_bf16 v[74:77], v[140:143], v[186:189], v[74:77]
	v_mfma_f32_16x16x32_bf16 v[70:73], v[130:133], v[198:201], v[70:73]
	v_mfma_f32_16x16x32_bf16 v[66:69], v[140:143], v[198:201], v[66:69]
	v_mfma_f32_16x16x32_bf16 v[110:113], v[134:137], v[174:177], v[110:113]
	v_mfma_f32_16x16x32_bf16 v[106:109], v[150:153], v[174:177], v[106:109]
	v_mfma_f32_16x16x32_bf16 v[94:97], v[134:137], v[182:185], v[94:97]
	v_mfma_f32_16x16x32_bf16 v[90:93], v[150:153], v[182:185], v[90:93]
	v_mfma_f32_16x16x32_bf16 v[78:81], v[134:137], v[194:197], v[78:81]
	v_mfma_f32_16x16x32_bf16 v[74:77], v[150:153], v[194:197], v[74:77]
	v_mfma_f32_16x16x32_bf16 v[70:73], v[134:137], v[202:205], v[70:73]
	v_mfma_f32_16x16x32_bf16 v[66:69], v[150:153], v[202:205], v[66:69]
	v_mfma_f32_16x16x32_bf16 v[46:49], v[154:157], v[170:173], v[46:49]
	v_mfma_f32_16x16x32_bf16 v[42:45], v[162:165], v[170:173], v[42:45]
	v_mfma_f32_16x16x32_bf16 v[26:29], v[154:157], v[178:181], v[26:29]
	v_mfma_f32_16x16x32_bf16 v[22:25], v[162:165], v[178:181], v[22:25]
	v_mfma_f32_16x16x32_bf16 v[6:9], v[154:157], v[186:189], v[6:9]
	v_mfma_f32_16x16x32_bf16 v[2:5], v[162:165], v[186:189], v[2:5]
	v_mfma_f32_16x16x32_bf16 v[18:21], v[154:157], v[198:201], v[18:21]
	v_mfma_f32_16x16x32_bf16 v[30:33], v[162:165], v[198:201], v[30:33]
	v_mfma_f32_16x16x32_bf16 v[46:49], v[158:161], v[174:177], v[46:49]
	v_mfma_f32_16x16x32_bf16 v[42:45], v[166:169], v[174:177], v[42:45]
	v_mfma_f32_16x16x32_bf16 v[26:29], v[158:161], v[182:185], v[26:29]
	v_mfma_f32_16x16x32_bf16 v[22:25], v[166:169], v[182:185], v[22:25]
	v_mfma_f32_16x16x32_bf16 v[6:9], v[158:161], v[194:197], v[6:9]
	v_mfma_f32_16x16x32_bf16 v[2:5], v[166:169], v[194:197], v[2:5]
	v_mfma_f32_16x16x32_bf16 v[18:21], v[158:161], v[202:205], v[18:21]
	v_mfma_f32_16x16x32_bf16 v[30:33], v[166:169], v[202:205], v[30:33]
	s_barrier
	s_setprio 0
	s_add_u32 s72, s72, 0x10000
	s_addc_u32 s73, s73, 0
	s_cmp_ge_i32 s74, s59
	s_mov_b64 s[48:49], s[50:51]
	s_mov_b32 s52, s74
	s_cbranch_scc0 .LBB0_707

.LBB0_890:
	s_add_u32 s34, s26, 0x10000
	s_addc_u32 s35, s27, 0
	s_and_b64 s[30:31], s[48:49], exec
	s_cselect_b32 s47, s41, s35
	s_cselect_b32 s46, s40, s34
	s_add_u32 s65, s28, 0x10000
	s_addc_u32 s66, s29, 0
	s_add_u32 s30, s46, 0x8000
	s_addc_u32 s31, s47, 0
	s_add_i32 s67, 0, 0x10000
	s_and_b64 s[34:35], s[48:49], exec
	s_cselect_b32 s35, s45, s66
	s_cselect_b32 s34, s44, s65
	s_add_i32 s70, 0, 0x14000
	v_add_u32_e32 v114, s67, v236
	v_add_u32_e32 v115, s70, v236
	ds_read_b128 v[2:5], v114
	s_waitcnt lgkmcnt(0)
	ds_read_b128 v[6:9], v114 offset:1024
	ds_read_b128 v[10:13], v114 offset:2048
	ds_read_b128 v[14:17], v114 offset:3072
	ds_read_b128 v[18:21], v115
	ds_read_b128 v[22:25], v115 offset:1024
	ds_read_b128 v[26:29], v115 offset:2048
	ds_read_b128 v[30:33], v115 offset:3072
	s_add_u32 s68, s26, 0xc000
	s_addc_u32 s69, s27, 0
	s_add_i32 s65, s20, 0xc000
	s_mov_b32 m0, s65
	s_add_i32 s66, s20, 0xe000
	ds_read_b128 v[34:37], v237
	ds_read_b128 v[38:41], v237 offset:1024
	ds_read_b128 v[42:45], v237 offset:2048
	ds_read_b128 v[46:49], v237 offset:3072
	ds_read_b128 v[50:53], v237 offset:4096
	ds_read_b128 v[54:57], v237 offset:5120
	ds_read_b128 v[58:61], v237 offset:6144
	ds_read_b128 v[62:65], v237 offset:7168
	s_nop 0
	global_load_lds_dwordx4 v235, s[68:69]
	s_mov_b32 m0, s66
	s_nop 0
	global_load_lds_dwordx4 v226, s[68:69]
	s_waitcnt vmcnt(8)
	s_waitcnt lgkmcnt(0)
	s_setprio 1
	s_barrier
	s_waitcnt lgkmcnt(0)
	v_mfma_f32_16x16x32_bf16 v[90:93], v[2:5], v[58:61], 0
	v_mfma_f32_16x16x32_bf16 v[66:69], v[2:5], v[34:37], 0
	v_mfma_f32_16x16x32_bf16 v[70:73], v[10:13], v[34:37], 0
	v_mfma_f32_16x16x32_bf16 v[74:77], v[2:5], v[42:45], 0
	v_mfma_f32_16x16x32_bf16 v[78:81], v[10:13], v[42:45], 0
	v_mfma_f32_16x16x32_bf16 v[82:85], v[2:5], v[50:53], 0
	v_mfma_f32_16x16x32_bf16 v[86:89], v[10:13], v[50:53], 0
	v_mfma_f32_16x16x32_bf16 v[98:101], v[6:9], v[62:65], v[90:93]
	v_mfma_f32_16x16x32_bf16 v[90:93], v[10:13], v[58:61], 0
	v_mfma_f32_16x16x32_bf16 v[66:69], v[6:9], v[38:41], v[66:69]
	v_mfma_f32_16x16x32_bf16 v[70:73], v[14:17], v[38:41], v[70:73]
	v_mfma_f32_16x16x32_bf16 v[74:77], v[6:9], v[46:49], v[74:77]
	v_mfma_f32_16x16x32_bf16 v[78:81], v[14:17], v[46:49], v[78:81]
	v_mfma_f32_16x16x32_bf16 v[82:85], v[6:9], v[54:57], v[82:85]
	v_mfma_f32_16x16x32_bf16 v[86:89], v[14:17], v[54:57], v[86:89]
	v_mfma_f32_16x16x32_bf16 v[102:105], v[14:17], v[62:65], v[90:93]
	v_mfma_f32_16x16x32_bf16 v[90:93], v[18:21], v[34:37], 0
	v_mfma_f32_16x16x32_bf16 v[34:37], v[26:29], v[34:37], 0
	v_mfma_f32_16x16x32_bf16 v[118:121], v[22:25], v[38:41], v[90:93]
	v_mfma_f32_16x16x32_bf16 v[34:37], v[30:33], v[38:41], v[34:37]
	v_mfma_f32_16x16x32_bf16 v[38:41], v[18:21], v[42:45], 0
	v_mfma_f32_16x16x32_bf16 v[42:45], v[26:29], v[42:45], 0
	v_mfma_f32_16x16x32_bf16 v[38:41], v[22:25], v[46:49], v[38:41]
	v_mfma_f32_16x16x32_bf16 v[42:45], v[30:33], v[46:49], v[42:45]
	v_mfma_f32_16x16x32_bf16 v[46:49], v[18:21], v[50:53], 0
	v_mfma_f32_16x16x32_bf16 v[50:53], v[26:29], v[50:53], 0
	v_mfma_f32_16x16x32_bf16 v[46:49], v[22:25], v[54:57], v[46:49]
	v_mfma_f32_16x16x32_bf16 v[50:53], v[30:33], v[54:57], v[50:53]
	v_mfma_f32_16x16x32_bf16 v[54:57], v[18:21], v[58:61], 0
	v_mfma_f32_16x16x32_bf16 v[58:61], v[26:29], v[58:61], 0
	v_mfma_f32_16x16x32_bf16 v[54:57], v[22:25], v[62:65], v[54:57]
	v_mfma_f32_16x16x32_bf16 v[58:61], v[30:33], v[62:65], v[58:61]
	s_barrier
	s_setprio 0
	s_add_i32 s67, s67, s18
	s_add_i32 s68, s67, 0x2000
	s_mov_b32 m0, s67
	s_add_u32 s72, s34, 0x4000
	ds_read_b128 v[62:65], v237 offset:16384
	ds_read_b128 v[90:93], v237 offset:17408
	ds_read_b128 v[94:97], v237 offset:18432
	ds_read_b128 v[106:109], v237 offset:19456
	ds_read_b128 v[110:113], v237 offset:20480
	ds_read_b128 v[122:125], v237 offset:21504
	ds_read_b128 v[126:129], v237 offset:22528
	ds_read_b128 v[130:133], v237 offset:23552
	s_addc_u32 s73, s35, 0
	global_load_lds_dwordx4 v227, s[34:35]
	s_mov_b32 m0, s68
	s_add_i32 s69, s70, s18
	s_add_i32 s70, s69, 0x2000
	global_load_lds_dwordx4 v0, s[34:35]
	s_mov_b32 m0, s69
	s_nop 0
	global_load_lds_dwordx4 v227, s[72:73]
	s_mov_b32 m0, s70
	s_nop 0
	global_load_lds_dwordx4 v0, s[72:73]
	s_mov_b32 m0, s20
	s_nop 0
	global_load_lds_dwordx4 v235, s[46:47]
	s_mov_b32 m0, s25
	s_nop 0
	global_load_lds_dwordx4 v226, s[46:47]
	s_waitcnt vmcnt(8)
	s_waitcnt lgkmcnt(0)
	s_setprio 1
	s_barrier
	s_waitcnt lgkmcnt(0)
	v_mfma_f32_16x16x32_bf16 v[134:137], v[2:5], v[62:65], 0
	v_mfma_f32_16x16x32_bf16 v[142:145], v[2:5], v[94:97], 0
	v_mfma_f32_16x16x32_bf16 v[150:153], v[2:5], v[110:113], 0
	v_mfma_f32_16x16x32_bf16 v[2:5], v[2:5], v[126:129], 0
	v_mfma_f32_16x16x32_bf16 v[134:137], v[6:9], v[90:93], v[134:137]
	v_mfma_f32_16x16x32_bf16 v[142:145], v[6:9], v[106:109], v[142:145]
	v_mfma_f32_16x16x32_bf16 v[150:153], v[6:9], v[122:125], v[150:153]
	v_mfma_f32_16x16x32_bf16 v[2:5], v[6:9], v[130:133], v[2:5]
	v_mfma_f32_16x16x32_bf16 v[6:9], v[10:13], v[126:129], 0
	v_mfma_f32_16x16x32_bf16 v[138:141], v[10:13], v[62:65], 0
	v_mfma_f32_16x16x32_bf16 v[146:149], v[10:13], v[94:97], 0
	v_mfma_f32_16x16x32_bf16 v[154:157], v[10:13], v[110:113], 0
	v_mfma_f32_16x16x32_bf16 v[6:9], v[14:17], v[130:133], v[6:9]
	v_mfma_f32_16x16x32_bf16 v[138:141], v[14:17], v[90:93], v[138:141]
	v_mfma_f32_16x16x32_bf16 v[146:149], v[14:17], v[106:109], v[146:149]
	v_mfma_f32_16x16x32_bf16 v[154:157], v[14:17], v[122:125], v[154:157]
	v_mfma_f32_16x16x32_bf16 v[10:13], v[18:21], v[62:65], 0
	v_mfma_f32_16x16x32_bf16 v[158:161], v[22:25], v[90:93], v[10:13]
	v_mfma_f32_16x16x32_bf16 v[10:13], v[26:29], v[62:65], 0
	v_mfma_f32_16x16x32_bf16 v[162:165], v[30:33], v[90:93], v[10:13]
	v_mfma_f32_16x16x32_bf16 v[10:13], v[18:21], v[94:97], 0
	v_mfma_f32_16x16x32_bf16 v[174:177], v[22:25], v[106:109], v[10:13]
	v_mfma_f32_16x16x32_bf16 v[10:13], v[26:29], v[94:97], 0
	v_mfma_f32_16x16x32_bf16 v[178:181], v[30:33], v[106:109], v[10:13]
	v_mfma_f32_16x16x32_bf16 v[10:13], v[18:21], v[110:113], 0
	v_mfma_f32_16x16x32_bf16 v[182:185], v[22:25], v[122:125], v[10:13]
	v_mfma_f32_16x16x32_bf16 v[10:13], v[26:29], v[110:113], 0
	v_mfma_f32_16x16x32_bf16 v[122:125], v[30:33], v[122:125], v[10:13]
	v_mfma_f32_16x16x32_bf16 v[10:13], v[18:21], v[126:129], 0
	v_mfma_f32_16x16x32_bf16 v[186:189], v[22:25], v[130:133], v[10:13]
	v_mfma_f32_16x16x32_bf16 v[10:13], v[26:29], v[126:129], 0
	v_mfma_f32_16x16x32_bf16 v[130:133], v[30:33], v[130:133], v[10:13]
	s_barrier
	s_setprio 0
	s_add_i32 s71, 0, 0x18000
	s_add_i32 s74, 0, 0x1c000
	v_add_u32_e32 v116, s71, v236
	v_add_u32_e32 v117, s74, v236
	s_nop 0
	ds_read_b128 v[10:13], v116
	ds_read_b128 v[14:17], v116 offset:1024
	ds_read_b128 v[18:21], v116 offset:2048
	ds_read_b128 v[22:25], v116 offset:3072
	ds_read_b128 v[194:197], v117
	ds_read_b128 v[198:201], v117 offset:1024
	ds_read_b128 v[202:205], v117 offset:2048
	ds_read_b128 v[206:209], v117 offset:3072
	s_add_u32 s46, s46, 0x4000
	s_addc_u32 s47, s47, 0
	s_mov_b32 m0, s54
	ds_read_b128 v[26:29], v237 offset:32768
	ds_read_b128 v[30:33], v237 offset:33792
	ds_read_b128 v[62:65], v237 offset:34816
	ds_read_b128 v[210:213], v237 offset:35840
	ds_read_b128 v[214:217], v237 offset:36864
	ds_read_b128 v[218:221], v237 offset:37888
	ds_read_b128 v[222:225], v237 offset:38912
	ds_read_b128 v[238:241], v237 offset:39936
	s_nop 0
	global_load_lds_dwordx4 v235, s[46:47]
	s_mov_b32 m0, s55
	s_nop 0
	global_load_lds_dwordx4 v226, s[46:47]
	s_waitcnt vmcnt(8)
	s_waitcnt lgkmcnt(0)
	s_setprio 1
	s_barrier
	s_waitcnt lgkmcnt(0)
	v_mfma_f32_16x16x32_bf16 v[66:69], v[10:13], v[26:29], v[66:69]
	v_mfma_f32_16x16x32_bf16 v[166:169], v[14:17], v[30:33], v[66:69]
	v_mfma_f32_16x16x32_bf16 v[66:69], v[18:21], v[26:29], v[70:73]
	v_mfma_f32_16x16x32_bf16 v[170:173], v[22:25], v[30:33], v[66:69]
	v_mfma_f32_16x16x32_bf16 v[66:69], v[10:13], v[62:65], v[74:77]
	v_mfma_f32_16x16x32_bf16 v[110:113], v[14:17], v[210:213], v[66:69]
	v_mfma_f32_16x16x32_bf16 v[66:69], v[18:21], v[62:65], v[78:81]
	v_mfma_f32_16x16x32_bf16 v[106:109], v[22:25], v[210:213], v[66:69]
	v_mfma_f32_16x16x32_bf16 v[66:69], v[10:13], v[214:217], v[82:85]
	v_mfma_f32_16x16x32_bf16 v[94:97], v[14:17], v[218:221], v[66:69]
	v_mfma_f32_16x16x32_bf16 v[66:69], v[18:21], v[214:217], v[86:89]
	v_mfma_f32_16x16x32_bf16 v[90:93], v[22:25], v[218:221], v[66:69]
	v_mfma_f32_16x16x32_bf16 v[66:69], v[10:13], v[222:225], v[98:101]
	v_mfma_f32_16x16x32_bf16 v[78:81], v[14:17], v[238:241], v[66:69]
	v_mfma_f32_16x16x32_bf16 v[66:69], v[18:21], v[222:225], v[102:105]
	v_mfma_f32_16x16x32_bf16 v[70:73], v[22:25], v[238:241], v[66:69]
	v_mfma_f32_16x16x32_bf16 v[66:69], v[194:197], v[26:29], v[118:121]
	v_mfma_f32_16x16x32_bf16 v[26:29], v[202:205], v[26:29], v[34:37]
	v_mfma_f32_16x16x32_bf16 v[118:121], v[206:209], v[30:33], v[26:29]
	v_mfma_f32_16x16x32_bf16 v[26:29], v[194:197], v[62:65], v[38:41]
	v_mfma_f32_16x16x32_bf16 v[102:105], v[198:201], v[210:213], v[26:29]
	v_mfma_f32_16x16x32_bf16 v[26:29], v[202:205], v[62:65], v[42:45]
	v_mfma_f32_16x16x32_bf16 v[98:101], v[206:209], v[210:213], v[26:29]
	v_mfma_f32_16x16x32_bf16 v[26:29], v[194:197], v[214:217], v[46:49]
	v_mfma_f32_16x16x32_bf16 v[86:89], v[198:201], v[218:221], v[26:29]
	v_mfma_f32_16x16x32_bf16 v[26:29], v[202:205], v[214:217], v[50:53]
	v_mfma_f32_16x16x32_bf16 v[82:85], v[206:209], v[218:221], v[26:29]
	v_mfma_f32_16x16x32_bf16 v[26:29], v[194:197], v[222:225], v[54:57]
	v_mfma_f32_16x16x32_bf16 v[62:65], v[198:201], v[238:241], v[26:29]
	v_mfma_f32_16x16x32_bf16 v[26:29], v[202:205], v[222:225], v[58:61]
	v_mfma_f32_16x16x32_bf16 v[126:129], v[198:201], v[30:33], v[66:69]
	v_mfma_f32_16x16x32_bf16 v[54:57], v[206:209], v[238:241], v[26:29]
	s_barrier
	s_setprio 0
	s_add_u32 s72, s34, 0x8000
	s_addc_u32 s73, s35, 0
	s_add_i32 s46, s71, s18
	s_add_i32 s47, s46, 0x2000
	s_mov_b32 m0, s46
	s_add_u32 s34, s34, 0xc000
	ds_read_b128 v[34:37], v237 offset:49152
	ds_read_b128 v[38:41], v237 offset:50176
	ds_read_b128 v[210:213], v237 offset:51200
	ds_read_b128 v[214:217], v237 offset:52224
	ds_read_b128 v[218:221], v237 offset:53248
	ds_read_b128 v[222:225], v237 offset:54272
	ds_read_b128 v[238:241], v237 offset:55296
	ds_read_b128 v[242:245], v237 offset:56320
	s_addc_u32 s35, s35, 0
	global_load_lds_dwordx4 v227, s[72:73]
	s_mov_b32 m0, s47
	s_add_i32 s71, s74, s18
	s_nop 0
	global_load_lds_dwordx4 v0, s[72:73]
	s_mov_b32 m0, s71
	s_add_i32 s72, s71, 0x2000
	s_nop 0
	global_load_lds_dwordx4 v227, s[34:35]
	s_mov_b32 m0, s72
	s_nop 0
	global_load_lds_dwordx4 v0, s[34:35]
	s_mov_b32 m0, s58
	s_nop 0
	global_load_lds_dwordx4 v235, s[30:31]
	s_mov_b32 m0, s59
	s_nop 0
	global_load_lds_dwordx4 v226, s[30:31]
	s_waitcnt vmcnt(8)
	s_waitcnt lgkmcnt(0)
	s_setprio 1
	s_barrier
	s_waitcnt lgkmcnt(0)
	v_mfma_f32_16x16x32_bf16 v[26:29], v[10:13], v[34:37], v[134:137]
	v_mfma_f32_16x16x32_bf16 v[74:77], v[14:17], v[38:41], v[26:29]
	v_mfma_f32_16x16x32_bf16 v[26:29], v[18:21], v[34:37], v[138:141]
	v_mfma_f32_16x16x32_bf16 v[66:69], v[22:25], v[38:41], v[26:29]
	v_mfma_f32_16x16x32_bf16 v[26:29], v[10:13], v[210:213], v[142:145]
	v_mfma_f32_16x16x32_bf16 v[46:49], v[14:17], v[214:217], v[26:29]
	v_mfma_f32_16x16x32_bf16 v[26:29], v[18:21], v[210:213], v[146:149]
	v_mfma_f32_16x16x32_bf16 v[42:45], v[22:25], v[214:217], v[26:29]
	v_mfma_f32_16x16x32_bf16 v[26:29], v[10:13], v[218:221], v[150:153]
	v_mfma_f32_16x16x32_bf16 v[2:5], v[10:13], v[238:241], v[2:5]
	v_mfma_f32_16x16x32_bf16 v[30:33], v[14:17], v[222:225], v[26:29]
	v_mfma_f32_16x16x32_bf16 v[26:29], v[18:21], v[218:221], v[154:157]
	v_mfma_f32_16x16x32_bf16 v[14:17], v[14:17], v[242:245], v[2:5]
	v_mfma_f32_16x16x32_bf16 v[2:5], v[18:21], v[238:241], v[6:9]
	v_mfma_f32_16x16x32_bf16 v[26:29], v[22:25], v[222:225], v[26:29]
	v_mfma_f32_16x16x32_bf16 v[10:13], v[22:25], v[242:245], v[2:5]
	v_mfma_f32_16x16x32_bf16 v[2:5], v[194:197], v[34:37], v[158:161]
	v_mfma_f32_16x16x32_bf16 v[58:61], v[198:201], v[38:41], v[2:5]
	v_mfma_f32_16x16x32_bf16 v[2:5], v[202:205], v[34:37], v[162:165]
	v_mfma_f32_16x16x32_bf16 v[50:53], v[206:209], v[38:41], v[2:5]
	v_mfma_f32_16x16x32_bf16 v[2:5], v[194:197], v[210:213], v[174:177]
	v_mfma_f32_16x16x32_bf16 v[38:41], v[198:201], v[214:217], v[2:5]
	v_mfma_f32_16x16x32_bf16 v[2:5], v[202:205], v[210:213], v[178:181]
	v_mfma_f32_16x16x32_bf16 v[34:37], v[206:209], v[214:217], v[2:5]
	v_mfma_f32_16x16x32_bf16 v[2:5], v[194:197], v[218:221], v[182:185]
	v_mfma_f32_16x16x32_bf16 v[22:25], v[198:201], v[222:225], v[2:5]
	v_mfma_f32_16x16x32_bf16 v[2:5], v[202:205], v[218:221], v[122:125]
	v_mfma_f32_16x16x32_bf16 v[18:21], v[206:209], v[222:225], v[2:5]
	v_mfma_f32_16x16x32_bf16 v[2:5], v[194:197], v[238:241], v[186:189]
	v_mfma_f32_16x16x32_bf16 v[6:9], v[198:201], v[242:245], v[2:5]
	v_mfma_f32_16x16x32_bf16 v[2:5], v[202:205], v[238:241], v[130:133]
	v_mfma_f32_16x16x32_bf16 v[2:5], v[206:209], v[242:245], v[2:5]
	s_barrier
	s_setprio 0
	s_andn2_b64 vcc, exec, s[50:51]
	s_cbranch_vccnz .LBB0_893
	s_add_u32 s73, s28, 0x20000
	s_addc_u32 s74, s29, 0
	s_add_u32 s26, s26, 0x1c000
	s_addc_u32 s27, s27, 0
	s_mov_b32 s75, 4
.LBB0_892:
	ds_read_b128 v[122:125], v114
	ds_read_b128 v[130:133], v114 offset:1024
	ds_read_b128 v[134:137], v114 offset:2048
	ds_read_b128 v[138:141], v114 offset:3072
	ds_read_b128 v[142:145], v115
	ds_read_b128 v[146:149], v115 offset:1024
	ds_read_b128 v[150:153], v115 offset:2048
	ds_read_b128 v[154:157], v115 offset:3072
	s_add_u32 s28, s26, 0x4000
	s_addc_u32 s29, s27, 0
	s_cmp_eq_u32 s56, s75
	s_cselect_b32 s34, s40, s28
	s_cselect_b32 s35, s41, s29
	s_cselect_b32 s30, s44, s73
	s_cselect_b32 s31, s45, s74
	s_add_u32 s28, s34, 0x8000
	s_addc_u32 s29, s35, 0
	s_mov_b32 m0, s65
	ds_read_b128 v[158:161], v237
	ds_read_b128 v[162:165], v237 offset:1024
	ds_read_b128 v[174:177], v237 offset:2048
	ds_read_b128 v[178:181], v237 offset:3072
	ds_read_b128 v[182:185], v237 offset:4096
	ds_read_b128 v[186:189], v237 offset:5120
	ds_read_b128 v[194:197], v237 offset:6144
	ds_read_b128 v[198:201], v237 offset:7168
	s_nop 0
	global_load_lds_dwordx4 v235, s[26:27]
	s_mov_b32 m0, s66
	s_nop 0
	global_load_lds_dwordx4 v226, s[26:27]
	s_waitcnt vmcnt(8)
	s_waitcnt lgkmcnt(0)
	s_setprio 1
	s_barrier
	s_waitcnt lgkmcnt(0)
	v_mfma_f32_16x16x32_bf16 v[166:169], v[122:125], v[158:161], v[166:169]
	v_mfma_f32_16x16x32_bf16 v[170:173], v[134:137], v[158:161], v[170:173]
	v_mfma_f32_16x16x32_bf16 v[110:113], v[122:125], v[174:177], v[110:113]
	v_mfma_f32_16x16x32_bf16 v[106:109], v[134:137], v[174:177], v[106:109]
	v_mfma_f32_16x16x32_bf16 v[94:97], v[122:125], v[182:185], v[94:97]
	v_mfma_f32_16x16x32_bf16 v[90:93], v[134:137], v[182:185], v[90:93]
	v_mfma_f32_16x16x32_bf16 v[78:81], v[122:125], v[194:197], v[78:81]
	v_mfma_f32_16x16x32_bf16 v[70:73], v[134:137], v[194:197], v[70:73]
	v_mfma_f32_16x16x32_bf16 v[166:169], v[130:133], v[162:165], v[166:169]
	v_mfma_f32_16x16x32_bf16 v[170:173], v[138:141], v[162:165], v[170:173]
	v_mfma_f32_16x16x32_bf16 v[110:113], v[130:133], v[178:181], v[110:113]
	v_mfma_f32_16x16x32_bf16 v[106:109], v[138:141], v[178:181], v[106:109]
	v_mfma_f32_16x16x32_bf16 v[94:97], v[130:133], v[186:189], v[94:97]
	v_mfma_f32_16x16x32_bf16 v[90:93], v[138:141], v[186:189], v[90:93]
	v_mfma_f32_16x16x32_bf16 v[78:81], v[130:133], v[198:201], v[78:81]
	v_mfma_f32_16x16x32_bf16 v[70:73], v[138:141], v[198:201], v[70:73]
	v_mfma_f32_16x16x32_bf16 v[126:129], v[142:145], v[158:161], v[126:129]
	v_mfma_f32_16x16x32_bf16 v[118:121], v[150:153], v[158:161], v[118:121]
	v_mfma_f32_16x16x32_bf16 v[102:105], v[142:145], v[174:177], v[102:105]
	v_mfma_f32_16x16x32_bf16 v[98:101], v[150:153], v[174:177], v[98:101]
	v_mfma_f32_16x16x32_bf16 v[86:89], v[142:145], v[182:185], v[86:89]
	v_mfma_f32_16x16x32_bf16 v[82:85], v[150:153], v[182:185], v[82:85]
	v_mfma_f32_16x16x32_bf16 v[62:65], v[142:145], v[194:197], v[62:65]
	v_mfma_f32_16x16x32_bf16 v[54:57], v[150:153], v[194:197], v[54:57]
	v_mfma_f32_16x16x32_bf16 v[126:129], v[146:149], v[162:165], v[126:129]
	v_mfma_f32_16x16x32_bf16 v[118:121], v[154:157], v[162:165], v[118:121]
	v_mfma_f32_16x16x32_bf16 v[102:105], v[146:149], v[178:181], v[102:105]
	v_mfma_f32_16x16x32_bf16 v[98:101], v[154:157], v[178:181], v[98:101]
	v_mfma_f32_16x16x32_bf16 v[86:89], v[146:149], v[186:189], v[86:89]
	v_mfma_f32_16x16x32_bf16 v[82:85], v[154:157], v[186:189], v[82:85]
	v_mfma_f32_16x16x32_bf16 v[62:65], v[146:149], v[198:201], v[62:65]
	v_mfma_f32_16x16x32_bf16 v[54:57], v[154:157], v[198:201], v[54:57]
	s_barrier
	s_setprio 0
	s_mov_b32 m0, s67
	ds_read_b128 v[158:161], v237 offset:16384
	ds_read_b128 v[162:165], v237 offset:17408
	ds_read_b128 v[174:177], v237 offset:18432
	ds_read_b128 v[178:181], v237 offset:19456
	ds_read_b128 v[182:185], v237 offset:20480
	ds_read_b128 v[186:189], v237 offset:21504
	ds_read_b128 v[194:197], v237 offset:22528
	ds_read_b128 v[198:201], v237 offset:23552
	s_add_u32 s76, s30, 0x4000
	global_load_lds_dwordx4 v227, s[30:31]
	s_mov_b32 m0, s68
	s_addc_u32 s77, s31, 0
	global_load_lds_dwordx4 v0, s[30:31]
	s_mov_b32 m0, s69
	s_nop 0
	global_load_lds_dwordx4 v227, s[76:77]
	s_mov_b32 m0, s70
	s_nop 0
	global_load_lds_dwordx4 v0, s[76:77]
	s_mov_b32 m0, s20
	s_nop 0
	global_load_lds_dwordx4 v235, s[34:35]
	s_mov_b32 m0, s25
	s_nop 0
	global_load_lds_dwordx4 v226, s[34:35]
	s_waitcnt vmcnt(8)
	s_waitcnt lgkmcnt(0)
	s_setprio 1
	s_barrier
	s_waitcnt lgkmcnt(0)
	v_mfma_f32_16x16x32_bf16 v[74:77], v[122:125], v[158:161], v[74:77]
	v_mfma_f32_16x16x32_bf16 v[66:69], v[134:137], v[158:161], v[66:69]
	v_mfma_f32_16x16x32_bf16 v[46:49], v[122:125], v[174:177], v[46:49]
	v_mfma_f32_16x16x32_bf16 v[42:45], v[134:137], v[174:177], v[42:45]
	v_mfma_f32_16x16x32_bf16 v[30:33], v[122:125], v[182:185], v[30:33]
	v_mfma_f32_16x16x32_bf16 v[26:29], v[134:137], v[182:185], v[26:29]
	v_mfma_f32_16x16x32_bf16 v[14:17], v[122:125], v[194:197], v[14:17]
	v_mfma_f32_16x16x32_bf16 v[10:13], v[134:137], v[194:197], v[10:13]
	v_mfma_f32_16x16x32_bf16 v[74:77], v[130:133], v[162:165], v[74:77]
	v_mfma_f32_16x16x32_bf16 v[66:69], v[138:141], v[162:165], v[66:69]
	v_mfma_f32_16x16x32_bf16 v[46:49], v[130:133], v[178:181], v[46:49]
	v_mfma_f32_16x16x32_bf16 v[42:45], v[138:141], v[178:181], v[42:45]
	v_mfma_f32_16x16x32_bf16 v[30:33], v[130:133], v[186:189], v[30:33]
	v_mfma_f32_16x16x32_bf16 v[26:29], v[138:141], v[186:189], v[26:29]
	v_mfma_f32_16x16x32_bf16 v[14:17], v[130:133], v[198:201], v[14:17]
	v_mfma_f32_16x16x32_bf16 v[10:13], v[138:141], v[198:201], v[10:13]
	v_mfma_f32_16x16x32_bf16 v[58:61], v[142:145], v[158:161], v[58:61]
	v_mfma_f32_16x16x32_bf16 v[50:53], v[150:153], v[158:161], v[50:53]
	v_mfma_f32_16x16x32_bf16 v[38:41], v[142:145], v[174:177], v[38:41]
	v_mfma_f32_16x16x32_bf16 v[34:37], v[150:153], v[174:177], v[34:37]
	v_mfma_f32_16x16x32_bf16 v[22:25], v[142:145], v[182:185], v[22:25]
	v_mfma_f32_16x16x32_bf16 v[18:21], v[150:153], v[182:185], v[18:21]
	v_mfma_f32_16x16x32_bf16 v[6:9], v[142:145], v[194:197], v[6:9]
	v_mfma_f32_16x16x32_bf16 v[2:5], v[150:153], v[194:197], v[2:5]
	v_mfma_f32_16x16x32_bf16 v[58:61], v[146:149], v[162:165], v[58:61]
	v_mfma_f32_16x16x32_bf16 v[50:53], v[154:157], v[162:165], v[50:53]
	v_mfma_f32_16x16x32_bf16 v[38:41], v[146:149], v[178:181], v[38:41]
	v_mfma_f32_16x16x32_bf16 v[34:37], v[154:157], v[178:181], v[34:37]
	v_mfma_f32_16x16x32_bf16 v[22:25], v[146:149], v[186:189], v[22:25]
	v_mfma_f32_16x16x32_bf16 v[18:21], v[154:157], v[186:189], v[18:21]
	v_mfma_f32_16x16x32_bf16 v[6:9], v[146:149], v[198:201], v[6:9]
	v_mfma_f32_16x16x32_bf16 v[2:5], v[154:157], v[198:201], v[2:5]
	s_barrier
	s_setprio 0
	ds_read_b128 v[122:125], v116
	ds_read_b128 v[130:133], v116 offset:1024
	ds_read_b128 v[134:137], v116 offset:2048
	ds_read_b128 v[138:141], v116 offset:3072
	ds_read_b128 v[142:145], v117
	ds_read_b128 v[146:149], v117 offset:1024
	ds_read_b128 v[150:153], v117 offset:2048
	ds_read_b128 v[154:157], v117 offset:3072
	s_add_u32 s34, s34, 0x4000
	s_addc_u32 s35, s35, 0
	s_mov_b32 m0, s54
	ds_read_b128 v[158:161], v237 offset:32768
	ds_read_b128 v[162:165], v237 offset:33792
	ds_read_b128 v[174:177], v237 offset:34816
	ds_read_b128 v[178:181], v237 offset:35840
	ds_read_b128 v[182:185], v237 offset:36864
	ds_read_b128 v[186:189], v237 offset:37888
	ds_read_b128 v[194:197], v237 offset:38912
	ds_read_b128 v[198:201], v237 offset:39936
	s_nop 0
	global_load_lds_dwordx4 v235, s[34:35]
	s_mov_b32 m0, s55
	s_nop 0
	global_load_lds_dwordx4 v226, s[34:35]
	s_waitcnt vmcnt(8)
	s_waitcnt lgkmcnt(0)
	s_setprio 1
	s_barrier
	s_waitcnt lgkmcnt(0)
	v_mfma_f32_16x16x32_bf16 v[166:169], v[122:125], v[158:161], v[166:169]
	v_mfma_f32_16x16x32_bf16 v[170:173], v[134:137], v[158:161], v[170:173]
	v_mfma_f32_16x16x32_bf16 v[110:113], v[122:125], v[174:177], v[110:113]
	v_mfma_f32_16x16x32_bf16 v[106:109], v[134:137], v[174:177], v[106:109]
	v_mfma_f32_16x16x32_bf16 v[94:97], v[122:125], v[182:185], v[94:97]
	v_mfma_f32_16x16x32_bf16 v[90:93], v[134:137], v[182:185], v[90:93]
	v_mfma_f32_16x16x32_bf16 v[78:81], v[122:125], v[194:197], v[78:81]
	v_mfma_f32_16x16x32_bf16 v[70:73], v[134:137], v[194:197], v[70:73]
	v_mfma_f32_16x16x32_bf16 v[166:169], v[130:133], v[162:165], v[166:169]
	v_mfma_f32_16x16x32_bf16 v[170:173], v[138:141], v[162:165], v[170:173]
	v_mfma_f32_16x16x32_bf16 v[110:113], v[130:133], v[178:181], v[110:113]
	v_mfma_f32_16x16x32_bf16 v[106:109], v[138:141], v[178:181], v[106:109]
	v_mfma_f32_16x16x32_bf16 v[94:97], v[130:133], v[186:189], v[94:97]
	v_mfma_f32_16x16x32_bf16 v[90:93], v[138:141], v[186:189], v[90:93]
	v_mfma_f32_16x16x32_bf16 v[78:81], v[130:133], v[198:201], v[78:81]
	v_mfma_f32_16x16x32_bf16 v[70:73], v[138:141], v[198:201], v[70:73]
	v_mfma_f32_16x16x32_bf16 v[126:129], v[142:145], v[158:161], v[126:129]
	v_mfma_f32_16x16x32_bf16 v[118:121], v[150:153], v[158:161], v[118:121]
	v_mfma_f32_16x16x32_bf16 v[102:105], v[142:145], v[174:177], v[102:105]
	v_mfma_f32_16x16x32_bf16 v[98:101], v[150:153], v[174:177], v[98:101]
	v_mfma_f32_16x16x32_bf16 v[86:89], v[142:145], v[182:185], v[86:89]
	v_mfma_f32_16x16x32_bf16 v[82:85], v[150:153], v[182:185], v[82:85]
	v_mfma_f32_16x16x32_bf16 v[62:65], v[142:145], v[194:197], v[62:65]
	v_mfma_f32_16x16x32_bf16 v[54:57], v[150:153], v[194:197], v[54:57]
	v_mfma_f32_16x16x32_bf16 v[126:129], v[146:149], v[162:165], v[126:129]
	v_mfma_f32_16x16x32_bf16 v[118:121], v[154:157], v[162:165], v[118:121]
	v_mfma_f32_16x16x32_bf16 v[102:105], v[146:149], v[178:181], v[102:105]
	v_mfma_f32_16x16x32_bf16 v[98:101], v[154:157], v[178:181], v[98:101]
	v_mfma_f32_16x16x32_bf16 v[86:89], v[146:149], v[186:189], v[86:89]
	v_mfma_f32_16x16x32_bf16 v[82:85], v[154:157], v[186:189], v[82:85]
	v_mfma_f32_16x16x32_bf16 v[62:65], v[146:149], v[198:201], v[62:65]
	v_mfma_f32_16x16x32_bf16 v[54:57], v[154:157], v[198:201], v[54:57]
	s_barrier
	s_setprio 0
	s_add_u32 s34, s30, 0x8000
	s_mov_b32 m0, s46
	s_addc_u32 s35, s31, 0
	ds_read_b128 v[158:161], v237 offset:49152
	ds_read_b128 v[162:165], v237 offset:50176
	ds_read_b128 v[174:177], v237 offset:51200
	ds_read_b128 v[178:181], v237 offset:52224
	ds_read_b128 v[182:185], v237 offset:53248
	ds_read_b128 v[186:189], v237 offset:54272
	ds_read_b128 v[194:197], v237 offset:55296
	ds_read_b128 v[198:201], v237 offset:56320
	s_add_u32 s30, s30, 0xc000
	global_load_lds_dwordx4 v227, s[34:35]
	s_mov_b32 m0, s47
	s_addc_u32 s31, s31, 0
	global_load_lds_dwordx4 v0, s[34:35]
	s_mov_b32 m0, s71
	s_nop 0
	global_load_lds_dwordx4 v227, s[30:31]
	s_mov_b32 m0, s72
	s_nop 0
	global_load_lds_dwordx4 v0, s[30:31]
	s_mov_b32 m0, s58
	s_nop 0
	global_load_lds_dwordx4 v235, s[28:29]
	s_mov_b32 m0, s59
	s_nop 0
	global_load_lds_dwordx4 v226, s[28:29]
	s_waitcnt vmcnt(8)
	s_waitcnt lgkmcnt(0)
	s_setprio 1
	s_barrier
	s_waitcnt lgkmcnt(0)
	v_mfma_f32_16x16x32_bf16 v[74:77], v[122:125], v[158:161], v[74:77]
	v_mfma_f32_16x16x32_bf16 v[66:69], v[134:137], v[158:161], v[66:69]
	v_mfma_f32_16x16x32_bf16 v[46:49], v[122:125], v[174:177], v[46:49]
	v_mfma_f32_16x16x32_bf16 v[42:45], v[134:137], v[174:177], v[42:45]
	v_mfma_f32_16x16x32_bf16 v[30:33], v[122:125], v[182:185], v[30:33]
	v_mfma_f32_16x16x32_bf16 v[26:29], v[134:137], v[182:185], v[26:29]
	v_mfma_f32_16x16x32_bf16 v[14:17], v[122:125], v[194:197], v[14:17]
	v_mfma_f32_16x16x32_bf16 v[10:13], v[134:137], v[194:197], v[10:13]
	v_mfma_f32_16x16x32_bf16 v[74:77], v[130:133], v[162:165], v[74:77]
	v_mfma_f32_16x16x32_bf16 v[66:69], v[138:141], v[162:165], v[66:69]
	v_mfma_f32_16x16x32_bf16 v[46:49], v[130:133], v[178:181], v[46:49]
	v_mfma_f32_16x16x32_bf16 v[42:45], v[138:141], v[178:181], v[42:45]
	v_mfma_f32_16x16x32_bf16 v[30:33], v[130:133], v[186:189], v[30:33]
	v_mfma_f32_16x16x32_bf16 v[26:29], v[138:141], v[186:189], v[26:29]
	v_mfma_f32_16x16x32_bf16 v[14:17], v[130:133], v[198:201], v[14:17]
	v_mfma_f32_16x16x32_bf16 v[10:13], v[138:141], v[198:201], v[10:13]
	v_mfma_f32_16x16x32_bf16 v[58:61], v[142:145], v[158:161], v[58:61]
	v_mfma_f32_16x16x32_bf16 v[50:53], v[150:153], v[158:161], v[50:53]
	v_mfma_f32_16x16x32_bf16 v[38:41], v[142:145], v[174:177], v[38:41]
	v_mfma_f32_16x16x32_bf16 v[34:37], v[150:153], v[174:177], v[34:37]
	v_mfma_f32_16x16x32_bf16 v[22:25], v[142:145], v[182:185], v[22:25]
	v_mfma_f32_16x16x32_bf16 v[18:21], v[150:153], v[182:185], v[18:21]
	v_mfma_f32_16x16x32_bf16 v[6:9], v[142:145], v[194:197], v[6:9]
	v_mfma_f32_16x16x32_bf16 v[2:5], v[150:153], v[194:197], v[2:5]
	v_mfma_f32_16x16x32_bf16 v[58:61], v[146:149], v[162:165], v[58:61]
	v_mfma_f32_16x16x32_bf16 v[50:53], v[154:157], v[162:165], v[50:53]
	v_mfma_f32_16x16x32_bf16 v[38:41], v[146:149], v[178:181], v[38:41]
	v_mfma_f32_16x16x32_bf16 v[34:37], v[154:157], v[178:181], v[34:37]
	v_mfma_f32_16x16x32_bf16 v[22:25], v[146:149], v[186:189], v[22:25]
	v_mfma_f32_16x16x32_bf16 v[18:21], v[154:157], v[186:189], v[18:21]
	v_mfma_f32_16x16x32_bf16 v[6:9], v[146:149], v[198:201], v[6:9]
	v_mfma_f32_16x16x32_bf16 v[2:5], v[154:157], v[198:201], v[2:5]
	s_barrier
	s_setprio 0
	s_add_i32 s28, s75, 2
	s_add_u32 s73, s73, 0x10000
	s_addc_u32 s74, s74, 0
	s_add_u32 s26, s26, 0x10000
	s_addc_u32 s27, s27, 0
	s_cmp_lt_i32 s75, s56
	s_mov_b32 s75, s28
	s_cbranch_scc1 .LBB0_892

.LBB0_965:
	s_add_u32 s34, s28, 0x10000
	s_addc_u32 s35, s29, 0
	s_and_b64 s[30:31], s[48:49], exec
	s_cselect_b32 s57, s43, s35
	s_cselect_b32 s56, s42, s34
	s_add_u32 s58, s26, 0x100
	s_addc_u32 s59, s27, 0
	s_add_u32 s30, s56, 0x8000
	s_addc_u32 s31, s57, 0
	s_add_i32 s74, 0, 0x10000
	s_and_b64 s[34:35], s[48:49], exec
	s_cselect_b32 s35, s55, s59
	s_cselect_b32 s34, s54, s58
	s_add_i32 s76, 0, 0x14000
	v_add_u32_e32 v132, s74, v218
	v_add_u32_e32 v133, s76, v218
	ds_read_b128 v[2:5], v132
	ds_read_b128 v[6:9], v132 offset:1024
	ds_read_b128 v[10:13], v132 offset:2048
	ds_read_b128 v[14:17], v132 offset:3072
	ds_read_b128 v[18:21], v133
	ds_read_b128 v[22:25], v133 offset:1024
	ds_read_b128 v[26:29], v133 offset:2048
	ds_read_b128 v[30:33], v133 offset:3072
	s_add_u32 s58, s28, 0xc000
	s_addc_u32 s59, s29, 0
	s_add_i32 s72, s18, 0xc000
	s_mov_b32 m0, s72
	s_add_i32 s73, s18, 0xe000
	ds_read_b128 v[34:37], v219
	ds_read_b128 v[38:41], v219 offset:1024
	ds_read_b128 v[42:45], v219 offset:2048
	ds_read_b128 v[46:49], v219 offset:3072
	ds_read_b128 v[50:53], v219 offset:4096
	ds_read_b128 v[54:57], v219 offset:5120
	ds_read_b128 v[58:61], v219 offset:6144
	ds_read_b128 v[62:65], v219 offset:7168
	s_nop 0
	global_load_lds_dwordx4 v217, s[58:59]
	s_mov_b32 m0, s73
	s_nop 0
	global_load_lds_dwordx4 v216, s[58:59]
	s_waitcnt vmcnt(8)
	s_waitcnt lgkmcnt(0)
	s_setprio 1
	s_barrier
	s_waitcnt lgkmcnt(0)
	v_mfma_f32_16x16x32_bf16 v[86:89], v[10:13], v[50:53], 0
	v_mfma_f32_16x16x32_bf16 v[90:93], v[14:17], v[54:57], v[86:89]
	v_mfma_f32_16x16x32_bf16 v[86:89], v[2:5], v[58:61], 0
	v_mfma_f32_16x16x32_bf16 v[66:69], v[2:5], v[34:37], 0
	v_mfma_f32_16x16x32_bf16 v[70:73], v[10:13], v[34:37], 0
	v_mfma_f32_16x16x32_bf16 v[74:77], v[2:5], v[42:45], 0
	v_mfma_f32_16x16x32_bf16 v[78:81], v[10:13], v[42:45], 0
	v_mfma_f32_16x16x32_bf16 v[82:85], v[2:5], v[50:53], 0
	v_mfma_f32_16x16x32_bf16 v[94:97], v[6:9], v[62:65], v[86:89]
	v_mfma_f32_16x16x32_bf16 v[86:89], v[10:13], v[58:61], 0
	v_mfma_f32_16x16x32_bf16 v[66:69], v[6:9], v[38:41], v[66:69]
	v_mfma_f32_16x16x32_bf16 v[70:73], v[14:17], v[38:41], v[70:73]
	v_mfma_f32_16x16x32_bf16 v[74:77], v[6:9], v[46:49], v[74:77]
	v_mfma_f32_16x16x32_bf16 v[78:81], v[14:17], v[46:49], v[78:81]
	v_mfma_f32_16x16x32_bf16 v[82:85], v[6:9], v[54:57], v[82:85]
	v_mfma_f32_16x16x32_bf16 v[106:109], v[14:17], v[62:65], v[86:89]
	v_mfma_f32_16x16x32_bf16 v[86:89], v[18:21], v[34:37], 0
	v_mfma_f32_16x16x32_bf16 v[34:37], v[26:29], v[34:37], 0
	v_mfma_f32_16x16x32_bf16 v[110:113], v[22:25], v[38:41], v[86:89]
	v_mfma_f32_16x16x32_bf16 v[34:37], v[30:33], v[38:41], v[34:37]
	v_mfma_f32_16x16x32_bf16 v[38:41], v[18:21], v[42:45], 0
	v_mfma_f32_16x16x32_bf16 v[42:45], v[26:29], v[42:45], 0
	v_mfma_f32_16x16x32_bf16 v[38:41], v[22:25], v[46:49], v[38:41]
	v_mfma_f32_16x16x32_bf16 v[42:45], v[30:33], v[46:49], v[42:45]
	v_mfma_f32_16x16x32_bf16 v[46:49], v[18:21], v[50:53], 0
	v_mfma_f32_16x16x32_bf16 v[50:53], v[26:29], v[50:53], 0
	v_mfma_f32_16x16x32_bf16 v[136:139], v[30:33], v[54:57], v[50:53]
	v_mfma_f32_16x16x32_bf16 v[50:53], v[18:21], v[58:61], 0
	v_mfma_f32_16x16x32_bf16 v[140:143], v[22:25], v[62:65], v[50:53]
	v_mfma_f32_16x16x32_bf16 v[50:53], v[26:29], v[58:61], 0
	v_mfma_f32_16x16x32_bf16 v[46:49], v[22:25], v[54:57], v[46:49]
	v_mfma_f32_16x16x32_bf16 v[58:61], v[30:33], v[62:65], v[50:53]
	s_barrier
	s_setprio 0
	s_add_i32 s74, s74, s15
	s_add_i32 s75, s74, 0x2000
	s_mov_b32 m0, s74
	s_add_u32 s58, s34, s36
	ds_read_b128 v[50:53], v219 offset:16384
	ds_read_b128 v[54:57], v219 offset:17408
	ds_read_b128 v[62:65], v219 offset:18432
	ds_read_b128 v[86:89], v219 offset:19456
	ds_read_b128 v[98:101], v219 offset:20480
	ds_read_b128 v[102:105], v219 offset:21504
	ds_read_b128 v[114:117], v219 offset:22528
	ds_read_b128 v[118:121], v219 offset:23552
	s_addc_u32 s59, s35, s37
	global_load_lds_dwordx4 v0, s[34:35]
	s_mov_b32 m0, s75
	s_add_i32 s76, s76, s15
	s_add_i32 s77, s76, 0x2000
	global_load_lds_dwordx4 v130, s[34:35]
	s_mov_b32 m0, s76
	s_nop 0
	global_load_lds_dwordx4 v0, s[58:59]
	s_mov_b32 m0, s77
	s_nop 0
	global_load_lds_dwordx4 v130, s[58:59]
	s_mov_b32 m0, s18
	s_nop 0
	global_load_lds_dwordx4 v217, s[56:57]
	s_mov_b32 m0, s20
	s_nop 0
	global_load_lds_dwordx4 v216, s[56:57]
	s_waitcnt vmcnt(8)
	s_waitcnt lgkmcnt(0)
	s_setprio 1
	s_barrier
	s_waitcnt lgkmcnt(0)
	v_mfma_f32_16x16x32_bf16 v[122:125], v[2:5], v[50:53], 0
	v_mfma_f32_16x16x32_bf16 v[144:147], v[6:9], v[54:57], v[122:125]
	v_mfma_f32_16x16x32_bf16 v[122:125], v[10:13], v[50:53], 0
	v_mfma_f32_16x16x32_bf16 v[148:151], v[14:17], v[54:57], v[122:125]
	v_mfma_f32_16x16x32_bf16 v[122:125], v[2:5], v[62:65], 0
	v_mfma_f32_16x16x32_bf16 v[152:155], v[6:9], v[86:89], v[122:125]
	v_mfma_f32_16x16x32_bf16 v[122:125], v[10:13], v[62:65], 0
	v_mfma_f32_16x16x32_bf16 v[156:159], v[14:17], v[86:89], v[122:125]
	v_mfma_f32_16x16x32_bf16 v[122:125], v[2:5], v[98:101], 0
	v_mfma_f32_16x16x32_bf16 v[2:5], v[2:5], v[114:117], 0
	v_mfma_f32_16x16x32_bf16 v[160:163], v[6:9], v[102:105], v[122:125]
	v_mfma_f32_16x16x32_bf16 v[2:5], v[6:9], v[118:121], v[2:5]
	v_mfma_f32_16x16x32_bf16 v[6:9], v[10:13], v[114:117], 0
	v_mfma_f32_16x16x32_bf16 v[122:125], v[10:13], v[98:101], 0
	v_mfma_f32_16x16x32_bf16 v[10:13], v[14:17], v[118:121], v[6:9]
	v_mfma_f32_16x16x32_bf16 v[164:167], v[14:17], v[102:105], v[122:125]
	v_mfma_f32_16x16x32_bf16 v[6:9], v[18:21], v[50:53], 0
	v_mfma_f32_16x16x32_bf16 v[14:17], v[22:25], v[54:57], v[6:9]
	v_mfma_f32_16x16x32_bf16 v[6:9], v[26:29], v[50:53], 0
	v_mfma_f32_16x16x32_bf16 v[168:171], v[30:33], v[54:57], v[6:9]
	v_mfma_f32_16x16x32_bf16 v[6:9], v[18:21], v[62:65], 0
	v_mfma_f32_16x16x32_bf16 v[172:175], v[22:25], v[86:89], v[6:9]
	v_mfma_f32_16x16x32_bf16 v[6:9], v[26:29], v[62:65], 0
	v_mfma_f32_16x16x32_bf16 v[176:179], v[30:33], v[86:89], v[6:9]
	v_mfma_f32_16x16x32_bf16 v[6:9], v[18:21], v[98:101], 0
	v_mfma_f32_16x16x32_bf16 v[180:183], v[22:25], v[102:105], v[6:9]
	v_mfma_f32_16x16x32_bf16 v[6:9], v[26:29], v[98:101], 0
	v_mfma_f32_16x16x32_bf16 v[184:187], v[30:33], v[102:105], v[6:9]
	v_mfma_f32_16x16x32_bf16 v[6:9], v[18:21], v[114:117], 0
	v_mfma_f32_16x16x32_bf16 v[188:191], v[22:25], v[118:121], v[6:9]
	v_mfma_f32_16x16x32_bf16 v[6:9], v[26:29], v[114:117], 0
	v_mfma_f32_16x16x32_bf16 v[194:197], v[30:33], v[118:121], v[6:9]
	s_barrier
	s_setprio 0
	s_add_i32 s78, 0, 0x18000
	s_add_i32 s80, 0, 0x1c000
	v_add_u32_e32 v134, s78, v218
	v_add_u32_e32 v135, s80, v218
	s_nop 0
	ds_read_b128 v[6:9], v134
	ds_read_b128 v[26:29], v134 offset:1024
	ds_read_b128 v[30:33], v134 offset:2048
	ds_read_b128 v[198:201], v134 offset:3072
	ds_read_b128 v[202:205], v135
	ds_read_b128 v[206:209], v135 offset:1024
	ds_read_b128 v[210:213], v135 offset:2048
	ds_read_b128 v[220:223], v135 offset:3072
	s_add_u32 s56, s56, 0x4000
	s_addc_u32 s57, s57, 0
	s_mov_b32 m0, s25
	ds_read_b128 v[18:21], v219 offset:32768
	ds_read_b128 v[22:25], v219 offset:33792
	ds_read_b128 v[62:65], v219 offset:34816
	ds_read_b128 v[224:227], v219 offset:35840
	ds_read_b128 v[232:235], v219 offset:36864
	ds_read_b128 v[236:239], v219 offset:37888
	ds_read_b128 v[240:243], v219 offset:38912
	ds_read_b128 v[244:247], v219 offset:39936
	s_nop 0
	global_load_lds_dwordx4 v217, s[56:57]
	s_mov_b32 m0, s60
	s_nop 0
	global_load_lds_dwordx4 v216, s[56:57]
	s_waitcnt vmcnt(8)
	s_waitcnt lgkmcnt(0)
	s_setprio 1
	s_barrier
	s_waitcnt lgkmcnt(0)
	v_mfma_f32_16x16x32_bf16 v[50:53], v[6:9], v[18:21], v[66:69]
	v_mfma_f32_16x16x32_bf16 v[126:129], v[26:29], v[22:25], v[50:53]
	v_mfma_f32_16x16x32_bf16 v[50:53], v[30:33], v[18:21], v[70:73]
	v_mfma_f32_16x16x32_bf16 v[122:125], v[198:201], v[22:25], v[50:53]
	v_mfma_f32_16x16x32_bf16 v[50:53], v[6:9], v[62:65], v[74:77]
	v_mfma_f32_16x16x32_bf16 v[102:105], v[26:29], v[224:227], v[50:53]
	v_mfma_f32_16x16x32_bf16 v[50:53], v[30:33], v[62:65], v[78:81]
	v_mfma_f32_16x16x32_bf16 v[98:101], v[198:201], v[224:227], v[50:53]
	v_mfma_f32_16x16x32_bf16 v[50:53], v[6:9], v[232:235], v[82:85]
	v_mfma_f32_16x16x32_bf16 v[86:89], v[26:29], v[236:239], v[50:53]
	v_mfma_f32_16x16x32_bf16 v[50:53], v[30:33], v[232:235], v[90:93]
	v_mfma_f32_16x16x32_bf16 v[82:85], v[198:201], v[236:239], v[50:53]
	v_mfma_f32_16x16x32_bf16 v[50:53], v[6:9], v[240:243], v[94:97]
	v_mfma_f32_16x16x32_bf16 v[54:57], v[26:29], v[244:247], v[50:53]
	v_mfma_f32_16x16x32_bf16 v[50:53], v[30:33], v[240:243], v[106:109]
	v_mfma_f32_16x16x32_bf16 v[50:53], v[198:201], v[244:247], v[50:53]
	v_mfma_f32_16x16x32_bf16 v[66:69], v[202:205], v[18:21], v[110:113]
	v_mfma_f32_16x16x32_bf16 v[18:21], v[210:213], v[18:21], v[34:37]
	v_mfma_f32_16x16x32_bf16 v[114:117], v[220:223], v[22:25], v[18:21]
	v_mfma_f32_16x16x32_bf16 v[18:21], v[202:205], v[62:65], v[38:41]
	v_mfma_f32_16x16x32_bf16 v[110:113], v[206:209], v[224:227], v[18:21]
	v_mfma_f32_16x16x32_bf16 v[18:21], v[210:213], v[62:65], v[42:45]
	v_mfma_f32_16x16x32_bf16 v[106:109], v[220:223], v[224:227], v[18:21]
	v_mfma_f32_16x16x32_bf16 v[18:21], v[202:205], v[232:235], v[46:49]
	v_mfma_f32_16x16x32_bf16 v[94:97], v[206:209], v[236:239], v[18:21]
	v_mfma_f32_16x16x32_bf16 v[18:21], v[210:213], v[232:235], v[136:139]
	v_mfma_f32_16x16x32_bf16 v[90:93], v[220:223], v[236:239], v[18:21]
	v_mfma_f32_16x16x32_bf16 v[18:21], v[202:205], v[240:243], v[140:143]
	v_mfma_f32_16x16x32_bf16 v[62:65], v[206:209], v[244:247], v[18:21]
	v_mfma_f32_16x16x32_bf16 v[18:21], v[210:213], v[240:243], v[58:61]
	v_mfma_f32_16x16x32_bf16 v[118:121], v[206:209], v[22:25], v[66:69]
	v_mfma_f32_16x16x32_bf16 v[58:61], v[220:223], v[244:247], v[18:21]
	s_barrier
	s_setprio 0
	ds_read_b128 v[42:45], v219 offset:49152
	ds_read_b128 v[46:49], v219 offset:50176
	ds_read_b128 v[136:139], v219 offset:51200
	ds_read_b128 v[140:143], v219 offset:52224
	ds_read_b128 v[224:227], v219 offset:53248
	ds_read_b128 v[232:235], v219 offset:54272
	ds_read_b128 v[236:239], v219 offset:55296
	ds_read_b128 v[240:243], v219 offset:56320
	s_add_i32 s78, s78, s15
	v_lshl_add_u64 v[18:19], s[34:35], 0, v[0:1]
	v_lshl_add_u64 v[18:19], v[18:19], 0, s[16:17]
	s_mov_b32 m0, s78
	v_mov_b32_e32 v131, v1
	global_load_lds_dwordx4 v[18:19], off
	s_add_i32 s79, s78, 0x2000
	v_lshl_add_u64 v[18:19], s[34:35], 0, v[130:131]
	v_lshl_add_u64 v[18:19], v[18:19], 0, s[16:17]
	s_mov_b32 m0, s79
	s_add_i32 s80, s80, s15
	global_load_lds_dwordx4 v[18:19], off
	s_mov_b32 m0, s80
	v_lshl_add_u64 v[18:19], s[58:59], 0, v[0:1]
	v_lshl_add_u64 v[18:19], v[18:19], 0, s[16:17]
	global_load_lds_dwordx4 v[18:19], off
	s_nop 0
	v_lshl_add_u64 v[18:19], s[58:59], 0, v[130:131]
	s_add_i32 s58, s80, 0x2000
	v_lshl_add_u64 v[18:19], v[18:19], 0, s[16:17]
	s_mov_b32 m0, s58
	s_nop 0
	global_load_lds_dwordx4 v[18:19], off
	s_mov_b32 m0, s65
	s_nop 0
	global_load_lds_dwordx4 v217, s[30:31]
	s_mov_b32 m0, s66
	s_nop 0
	global_load_lds_dwordx4 v216, s[30:31]
	s_waitcnt vmcnt(8)
	s_waitcnt lgkmcnt(0)
	s_setprio 1
	s_barrier
	s_waitcnt lgkmcnt(0)
	v_mfma_f32_16x16x32_bf16 v[18:21], v[6:9], v[42:45], v[144:147]
	v_mfma_f32_16x16x32_bf16 v[70:73], v[26:29], v[46:49], v[18:21]
	v_mfma_f32_16x16x32_bf16 v[18:21], v[30:33], v[42:45], v[148:151]
	v_mfma_f32_16x16x32_bf16 v[66:69], v[198:201], v[46:49], v[18:21]
	v_mfma_f32_16x16x32_bf16 v[18:21], v[6:9], v[136:139], v[152:155]
	v_mfma_f32_16x16x32_bf16 v[38:41], v[26:29], v[140:143], v[18:21]
	v_mfma_f32_16x16x32_bf16 v[18:21], v[30:33], v[136:139], v[156:159]
	v_mfma_f32_16x16x32_bf16 v[34:37], v[198:201], v[140:143], v[18:21]
	v_mfma_f32_16x16x32_bf16 v[18:21], v[6:9], v[224:227], v[160:163]
	v_mfma_f32_16x16x32_bf16 v[2:5], v[6:9], v[236:239], v[2:5]
	v_mfma_f32_16x16x32_bf16 v[22:25], v[26:29], v[232:235], v[18:21]
	v_mfma_f32_16x16x32_bf16 v[18:21], v[30:33], v[224:227], v[164:167]
	v_mfma_f32_16x16x32_bf16 v[6:9], v[26:29], v[240:243], v[2:5]
	v_mfma_f32_16x16x32_bf16 v[2:5], v[30:33], v[236:239], v[10:13]
	v_mfma_f32_16x16x32_bf16 v[18:21], v[198:201], v[232:235], v[18:21]
	v_mfma_f32_16x16x32_bf16 v[2:5], v[198:201], v[240:243], v[2:5]
	v_mfma_f32_16x16x32_bf16 v[10:13], v[202:205], v[42:45], v[14:17]
	v_mfma_f32_16x16x32_bf16 v[78:81], v[206:209], v[46:49], v[10:13]
	v_mfma_f32_16x16x32_bf16 v[10:13], v[210:213], v[42:45], v[168:171]
	v_mfma_f32_16x16x32_bf16 v[74:77], v[220:223], v[46:49], v[10:13]
	v_mfma_f32_16x16x32_bf16 v[10:13], v[202:205], v[136:139], v[172:175]
	v_mfma_f32_16x16x32_bf16 v[46:49], v[206:209], v[140:143], v[10:13]
	v_mfma_f32_16x16x32_bf16 v[10:13], v[210:213], v[136:139], v[176:179]
	v_mfma_f32_16x16x32_bf16 v[42:45], v[220:223], v[140:143], v[10:13]
	v_mfma_f32_16x16x32_bf16 v[10:13], v[202:205], v[224:227], v[180:183]
	v_mfma_f32_16x16x32_bf16 v[30:33], v[206:209], v[232:235], v[10:13]
	v_mfma_f32_16x16x32_bf16 v[10:13], v[210:213], v[224:227], v[184:187]
	v_mfma_f32_16x16x32_bf16 v[26:29], v[220:223], v[232:235], v[10:13]
	v_mfma_f32_16x16x32_bf16 v[10:13], v[202:205], v[236:239], v[188:191]
	v_mfma_f32_16x16x32_bf16 v[14:17], v[206:209], v[240:243], v[10:13]
	v_mfma_f32_16x16x32_bf16 v[10:13], v[210:213], v[236:239], v[194:197]
	v_mfma_f32_16x16x32_bf16 v[10:13], v[220:223], v[240:243], v[10:13]
	s_barrier
	s_setprio 0
	s_andn2_b64 vcc, exec, s[50:51]
	s_cbranch_vccnz .LBB0_968
	s_add_u32 s59, s26, 0x200
	s_addc_u32 s81, s27, 0
	s_add_u32 s26, s28, 0x1c000
	s_addc_u32 s27, s29, 0
	s_mov_b32 s82, 4
.LBB0_967:
	ds_read_b128 v[136:139], v132
	ds_read_b128 v[140:143], v132 offset:1024
	ds_read_b128 v[144:147], v132 offset:2048
	ds_read_b128 v[148:151], v132 offset:3072
	ds_read_b128 v[152:155], v133
	ds_read_b128 v[156:159], v133 offset:1024
	ds_read_b128 v[160:163], v133 offset:2048
	ds_read_b128 v[164:167], v133 offset:3072
	s_add_u32 s28, s26, 0x4000
	s_addc_u32 s29, s27, 0
	s_cmp_eq_u32 s63, s82
	s_cselect_b32 s34, s42, s28
	s_cselect_b32 s35, s43, s29
	s_cselect_b32 s30, s54, s59
	s_cselect_b32 s31, s55, s81
	s_add_u32 s28, s34, 0x8000
	s_addc_u32 s29, s35, 0
	s_mov_b32 m0, s72
	ds_read_b128 v[168:171], v219
	ds_read_b128 v[172:175], v219 offset:1024
	ds_read_b128 v[176:179], v219 offset:2048
	ds_read_b128 v[180:183], v219 offset:3072
	ds_read_b128 v[184:187], v219 offset:4096
	ds_read_b128 v[188:191], v219 offset:5120
	ds_read_b128 v[194:197], v219 offset:6144
	ds_read_b128 v[198:201], v219 offset:7168
	s_nop 0
	global_load_lds_dwordx4 v217, s[26:27]
	s_mov_b32 m0, s73
	s_nop 0
	global_load_lds_dwordx4 v216, s[26:27]
	s_waitcnt vmcnt(8)
	s_waitcnt lgkmcnt(0)
	s_setprio 1
	s_barrier
	s_waitcnt lgkmcnt(0)
	v_mfma_f32_16x16x32_bf16 v[126:129], v[136:139], v[168:171], v[126:129]
	v_mfma_f32_16x16x32_bf16 v[122:125], v[144:147], v[168:171], v[122:125]
	v_mfma_f32_16x16x32_bf16 v[102:105], v[136:139], v[176:179], v[102:105]
	v_mfma_f32_16x16x32_bf16 v[98:101], v[144:147], v[176:179], v[98:101]
	v_mfma_f32_16x16x32_bf16 v[86:89], v[136:139], v[184:187], v[86:89]
	v_mfma_f32_16x16x32_bf16 v[82:85], v[144:147], v[184:187], v[82:85]
	v_mfma_f32_16x16x32_bf16 v[54:57], v[136:139], v[194:197], v[54:57]
	v_mfma_f32_16x16x32_bf16 v[50:53], v[144:147], v[194:197], v[50:53]
	v_mfma_f32_16x16x32_bf16 v[126:129], v[140:143], v[172:175], v[126:129]
	v_mfma_f32_16x16x32_bf16 v[122:125], v[148:151], v[172:175], v[122:125]
	v_mfma_f32_16x16x32_bf16 v[102:105], v[140:143], v[180:183], v[102:105]
	v_mfma_f32_16x16x32_bf16 v[98:101], v[148:151], v[180:183], v[98:101]
	v_mfma_f32_16x16x32_bf16 v[86:89], v[140:143], v[188:191], v[86:89]
	v_mfma_f32_16x16x32_bf16 v[82:85], v[148:151], v[188:191], v[82:85]
	v_mfma_f32_16x16x32_bf16 v[54:57], v[140:143], v[198:201], v[54:57]
	v_mfma_f32_16x16x32_bf16 v[50:53], v[148:151], v[198:201], v[50:53]
	v_mfma_f32_16x16x32_bf16 v[118:121], v[152:155], v[168:171], v[118:121]
	v_mfma_f32_16x16x32_bf16 v[114:117], v[160:163], v[168:171], v[114:117]
	v_mfma_f32_16x16x32_bf16 v[110:113], v[152:155], v[176:179], v[110:113]
	v_mfma_f32_16x16x32_bf16 v[106:109], v[160:163], v[176:179], v[106:109]
	v_mfma_f32_16x16x32_bf16 v[94:97], v[152:155], v[184:187], v[94:97]
	v_mfma_f32_16x16x32_bf16 v[90:93], v[160:163], v[184:187], v[90:93]
	v_mfma_f32_16x16x32_bf16 v[62:65], v[152:155], v[194:197], v[62:65]
	v_mfma_f32_16x16x32_bf16 v[58:61], v[160:163], v[194:197], v[58:61]
	v_mfma_f32_16x16x32_bf16 v[118:121], v[156:159], v[172:175], v[118:121]
	v_mfma_f32_16x16x32_bf16 v[114:117], v[164:167], v[172:175], v[114:117]
	v_mfma_f32_16x16x32_bf16 v[110:113], v[156:159], v[180:183], v[110:113]
	v_mfma_f32_16x16x32_bf16 v[106:109], v[164:167], v[180:183], v[106:109]
	v_mfma_f32_16x16x32_bf16 v[94:97], v[156:159], v[188:191], v[94:97]
	v_mfma_f32_16x16x32_bf16 v[90:93], v[164:167], v[188:191], v[90:93]
	v_mfma_f32_16x16x32_bf16 v[62:65], v[156:159], v[198:201], v[62:65]
	v_mfma_f32_16x16x32_bf16 v[58:61], v[164:167], v[198:201], v[58:61]
	s_barrier
	s_setprio 0
	s_mov_b32 m0, s74
	ds_read_b128 v[168:171], v219 offset:16384
	ds_read_b128 v[172:175], v219 offset:17408
	ds_read_b128 v[176:179], v219 offset:18432
	ds_read_b128 v[180:183], v219 offset:19456
	ds_read_b128 v[184:187], v219 offset:20480
	ds_read_b128 v[188:191], v219 offset:21504
	ds_read_b128 v[194:197], v219 offset:22528
	ds_read_b128 v[198:201], v219 offset:23552
	s_add_u32 s56, s30, s36
	global_load_lds_dwordx4 v0, s[30:31]
	s_mov_b32 m0, s75
	s_addc_u32 s57, s31, s37
	global_load_lds_dwordx4 v130, s[30:31]
	s_mov_b32 m0, s76
	s_nop 0
	global_load_lds_dwordx4 v0, s[56:57]
	s_mov_b32 m0, s77
	s_nop 0
	global_load_lds_dwordx4 v130, s[56:57]
	s_mov_b32 m0, s18
	s_nop 0
	global_load_lds_dwordx4 v217, s[34:35]
	s_mov_b32 m0, s20
	s_nop 0
	global_load_lds_dwordx4 v216, s[34:35]
	s_waitcnt vmcnt(8)
	s_waitcnt lgkmcnt(0)
	s_setprio 1
	s_barrier
	s_waitcnt lgkmcnt(0)
	v_mfma_f32_16x16x32_bf16 v[70:73], v[136:139], v[168:171], v[70:73]
	v_mfma_f32_16x16x32_bf16 v[66:69], v[144:147], v[168:171], v[66:69]
	v_mfma_f32_16x16x32_bf16 v[38:41], v[136:139], v[176:179], v[38:41]
	v_mfma_f32_16x16x32_bf16 v[34:37], v[144:147], v[176:179], v[34:37]
	v_mfma_f32_16x16x32_bf16 v[22:25], v[136:139], v[184:187], v[22:25]
	v_mfma_f32_16x16x32_bf16 v[18:21], v[144:147], v[184:187], v[18:21]
	v_mfma_f32_16x16x32_bf16 v[6:9], v[136:139], v[194:197], v[6:9]
	v_mfma_f32_16x16x32_bf16 v[2:5], v[144:147], v[194:197], v[2:5]
	v_mfma_f32_16x16x32_bf16 v[70:73], v[140:143], v[172:175], v[70:73]
	v_mfma_f32_16x16x32_bf16 v[66:69], v[148:151], v[172:175], v[66:69]
	v_mfma_f32_16x16x32_bf16 v[38:41], v[140:143], v[180:183], v[38:41]
	v_mfma_f32_16x16x32_bf16 v[34:37], v[148:151], v[180:183], v[34:37]
	v_mfma_f32_16x16x32_bf16 v[22:25], v[140:143], v[188:191], v[22:25]
	v_mfma_f32_16x16x32_bf16 v[18:21], v[148:151], v[188:191], v[18:21]
	v_mfma_f32_16x16x32_bf16 v[6:9], v[140:143], v[198:201], v[6:9]
	v_mfma_f32_16x16x32_bf16 v[2:5], v[148:151], v[198:201], v[2:5]
	v_mfma_f32_16x16x32_bf16 v[78:81], v[152:155], v[168:171], v[78:81]
	v_mfma_f32_16x16x32_bf16 v[74:77], v[160:163], v[168:171], v[74:77]
	v_mfma_f32_16x16x32_bf16 v[46:49], v[152:155], v[176:179], v[46:49]
	v_mfma_f32_16x16x32_bf16 v[42:45], v[160:163], v[176:179], v[42:45]
	v_mfma_f32_16x16x32_bf16 v[30:33], v[152:155], v[184:187], v[30:33]
	v_mfma_f32_16x16x32_bf16 v[26:29], v[160:163], v[184:187], v[26:29]
	v_mfma_f32_16x16x32_bf16 v[14:17], v[152:155], v[194:197], v[14:17]
	v_mfma_f32_16x16x32_bf16 v[10:13], v[160:163], v[194:197], v[10:13]
	v_mfma_f32_16x16x32_bf16 v[78:81], v[156:159], v[172:175], v[78:81]
	v_mfma_f32_16x16x32_bf16 v[74:77], v[164:167], v[172:175], v[74:77]
	v_mfma_f32_16x16x32_bf16 v[46:49], v[156:159], v[180:183], v[46:49]
	v_mfma_f32_16x16x32_bf16 v[42:45], v[164:167], v[180:183], v[42:45]
	v_mfma_f32_16x16x32_bf16 v[30:33], v[156:159], v[188:191], v[30:33]
	v_mfma_f32_16x16x32_bf16 v[26:29], v[164:167], v[188:191], v[26:29]
	v_mfma_f32_16x16x32_bf16 v[14:17], v[156:159], v[198:201], v[14:17]
	v_mfma_f32_16x16x32_bf16 v[10:13], v[164:167], v[198:201], v[10:13]
	s_barrier
	s_setprio 0
	ds_read_b128 v[136:139], v134
	ds_read_b128 v[140:143], v134 offset:1024
	ds_read_b128 v[144:147], v134 offset:2048
	ds_read_b128 v[148:151], v134 offset:3072
	ds_read_b128 v[152:155], v135
	ds_read_b128 v[156:159], v135 offset:1024
	ds_read_b128 v[160:163], v135 offset:2048
	ds_read_b128 v[164:167], v135 offset:3072
	s_add_u32 s34, s34, 0x4000
	s_addc_u32 s35, s35, 0
	s_mov_b32 m0, s25
	ds_read_b128 v[168:171], v219 offset:32768
	ds_read_b128 v[172:175], v219 offset:33792
	ds_read_b128 v[176:179], v219 offset:34816
	ds_read_b128 v[180:183], v219 offset:35840
	ds_read_b128 v[184:187], v219 offset:36864
	ds_read_b128 v[188:191], v219 offset:37888
	ds_read_b128 v[194:197], v219 offset:38912
	ds_read_b128 v[198:201], v219 offset:39936
	s_nop 0
	global_load_lds_dwordx4 v217, s[34:35]
	s_mov_b32 m0, s60
	s_nop 0
	global_load_lds_dwordx4 v216, s[34:35]
	s_waitcnt vmcnt(8)
	s_waitcnt lgkmcnt(0)
	s_setprio 1
	s_barrier
	s_waitcnt lgkmcnt(0)
	v_mfma_f32_16x16x32_bf16 v[126:129], v[136:139], v[168:171], v[126:129]
	v_mfma_f32_16x16x32_bf16 v[122:125], v[144:147], v[168:171], v[122:125]
	v_mfma_f32_16x16x32_bf16 v[102:105], v[136:139], v[176:179], v[102:105]
	v_mfma_f32_16x16x32_bf16 v[98:101], v[144:147], v[176:179], v[98:101]
	v_mfma_f32_16x16x32_bf16 v[86:89], v[136:139], v[184:187], v[86:89]
	v_mfma_f32_16x16x32_bf16 v[82:85], v[144:147], v[184:187], v[82:85]
	v_mfma_f32_16x16x32_bf16 v[54:57], v[136:139], v[194:197], v[54:57]
	v_mfma_f32_16x16x32_bf16 v[50:53], v[144:147], v[194:197], v[50:53]
	v_mfma_f32_16x16x32_bf16 v[126:129], v[140:143], v[172:175], v[126:129]
	v_mfma_f32_16x16x32_bf16 v[122:125], v[148:151], v[172:175], v[122:125]
	v_mfma_f32_16x16x32_bf16 v[102:105], v[140:143], v[180:183], v[102:105]
	v_mfma_f32_16x16x32_bf16 v[98:101], v[148:151], v[180:183], v[98:101]
	v_mfma_f32_16x16x32_bf16 v[86:89], v[140:143], v[188:191], v[86:89]
	v_mfma_f32_16x16x32_bf16 v[82:85], v[148:151], v[188:191], v[82:85]
	v_mfma_f32_16x16x32_bf16 v[54:57], v[140:143], v[198:201], v[54:57]
	v_mfma_f32_16x16x32_bf16 v[50:53], v[148:151], v[198:201], v[50:53]
	v_mfma_f32_16x16x32_bf16 v[118:121], v[152:155], v[168:171], v[118:121]
	v_mfma_f32_16x16x32_bf16 v[114:117], v[160:163], v[168:171], v[114:117]
	v_mfma_f32_16x16x32_bf16 v[110:113], v[152:155], v[176:179], v[110:113]
	v_mfma_f32_16x16x32_bf16 v[106:109], v[160:163], v[176:179], v[106:109]
	v_mfma_f32_16x16x32_bf16 v[94:97], v[152:155], v[184:187], v[94:97]
	v_mfma_f32_16x16x32_bf16 v[90:93], v[160:163], v[184:187], v[90:93]
	v_mfma_f32_16x16x32_bf16 v[62:65], v[152:155], v[194:197], v[62:65]
	v_mfma_f32_16x16x32_bf16 v[58:61], v[160:163], v[194:197], v[58:61]
	v_mfma_f32_16x16x32_bf16 v[118:121], v[156:159], v[172:175], v[118:121]
	v_mfma_f32_16x16x32_bf16 v[114:117], v[164:167], v[172:175], v[114:117]
	v_mfma_f32_16x16x32_bf16 v[110:113], v[156:159], v[180:183], v[110:113]
	v_mfma_f32_16x16x32_bf16 v[106:109], v[164:167], v[180:183], v[106:109]
	v_mfma_f32_16x16x32_bf16 v[94:97], v[156:159], v[188:191], v[94:97]
	v_mfma_f32_16x16x32_bf16 v[90:93], v[164:167], v[188:191], v[90:93]
	v_mfma_f32_16x16x32_bf16 v[62:65], v[156:159], v[198:201], v[62:65]
	v_mfma_f32_16x16x32_bf16 v[58:61], v[164:167], v[198:201], v[58:61]
	s_barrier
	s_setprio 0
	ds_read_b128 v[168:171], v219 offset:49152
	ds_read_b128 v[172:175], v219 offset:50176
	ds_read_b128 v[176:179], v219 offset:51200
	ds_read_b128 v[180:183], v219 offset:52224
	ds_read_b128 v[184:187], v219 offset:53248
	ds_read_b128 v[188:191], v219 offset:54272
	ds_read_b128 v[194:197], v219 offset:55296
	ds_read_b128 v[198:201], v219 offset:56320
	s_mov_b32 m0, s78
	v_lshl_add_u64 v[202:203], s[30:31], 0, v[0:1]
	v_lshl_add_u64 v[202:203], v[202:203], 0, s[16:17]
	v_mov_b32_e32 v131, v1
	global_load_lds_dwordx4 v[202:203], off
	s_mov_b32 m0, s79
	v_lshl_add_u64 v[202:203], s[30:31], 0, v[130:131]
	v_lshl_add_u64 v[202:203], v[202:203], 0, s[16:17]
	global_load_lds_dwordx4 v[202:203], off
	s_mov_b32 m0, s80
	v_lshl_add_u64 v[202:203], s[56:57], 0, v[0:1]
	v_lshl_add_u64 v[202:203], v[202:203], 0, s[16:17]
	global_load_lds_dwordx4 v[202:203], off
	s_mov_b32 m0, s58
	v_lshl_add_u64 v[202:203], s[56:57], 0, v[130:131]
	v_lshl_add_u64 v[202:203], v[202:203], 0, s[16:17]
	global_load_lds_dwordx4 v[202:203], off
	s_mov_b32 m0, s65
	s_nop 0
	global_load_lds_dwordx4 v217, s[28:29]
	s_mov_b32 m0, s66
	s_nop 0
	global_load_lds_dwordx4 v216, s[28:29]
	s_waitcnt vmcnt(8)
	s_waitcnt lgkmcnt(0)
	s_setprio 1
	s_barrier
	s_waitcnt lgkmcnt(0)
	v_mfma_f32_16x16x32_bf16 v[70:73], v[136:139], v[168:171], v[70:73]
	v_mfma_f32_16x16x32_bf16 v[66:69], v[144:147], v[168:171], v[66:69]
	v_mfma_f32_16x16x32_bf16 v[38:41], v[136:139], v[176:179], v[38:41]
	v_mfma_f32_16x16x32_bf16 v[34:37], v[144:147], v[176:179], v[34:37]
	v_mfma_f32_16x16x32_bf16 v[22:25], v[136:139], v[184:187], v[22:25]
	v_mfma_f32_16x16x32_bf16 v[18:21], v[144:147], v[184:187], v[18:21]
	v_mfma_f32_16x16x32_bf16 v[6:9], v[136:139], v[194:197], v[6:9]
	v_mfma_f32_16x16x32_bf16 v[2:5], v[144:147], v[194:197], v[2:5]
	v_mfma_f32_16x16x32_bf16 v[70:73], v[140:143], v[172:175], v[70:73]
	v_mfma_f32_16x16x32_bf16 v[66:69], v[148:151], v[172:175], v[66:69]
	v_mfma_f32_16x16x32_bf16 v[38:41], v[140:143], v[180:183], v[38:41]
	v_mfma_f32_16x16x32_bf16 v[34:37], v[148:151], v[180:183], v[34:37]
	v_mfma_f32_16x16x32_bf16 v[22:25], v[140:143], v[188:191], v[22:25]
	v_mfma_f32_16x16x32_bf16 v[18:21], v[148:151], v[188:191], v[18:21]
	v_mfma_f32_16x16x32_bf16 v[6:9], v[140:143], v[198:201], v[6:9]
	v_mfma_f32_16x16x32_bf16 v[2:5], v[148:151], v[198:201], v[2:5]
	v_mfma_f32_16x16x32_bf16 v[78:81], v[152:155], v[168:171], v[78:81]
	v_mfma_f32_16x16x32_bf16 v[74:77], v[160:163], v[168:171], v[74:77]
	v_mfma_f32_16x16x32_bf16 v[46:49], v[152:155], v[176:179], v[46:49]
	v_mfma_f32_16x16x32_bf16 v[42:45], v[160:163], v[176:179], v[42:45]
	v_mfma_f32_16x16x32_bf16 v[30:33], v[152:155], v[184:187], v[30:33]
	v_mfma_f32_16x16x32_bf16 v[26:29], v[160:163], v[184:187], v[26:29]
	v_mfma_f32_16x16x32_bf16 v[14:17], v[152:155], v[194:197], v[14:17]
	v_mfma_f32_16x16x32_bf16 v[10:13], v[160:163], v[194:197], v[10:13]
	v_mfma_f32_16x16x32_bf16 v[78:81], v[156:159], v[172:175], v[78:81]
	v_mfma_f32_16x16x32_bf16 v[74:77], v[164:167], v[172:175], v[74:77]
	v_mfma_f32_16x16x32_bf16 v[46:49], v[156:159], v[180:183], v[46:49]
	v_mfma_f32_16x16x32_bf16 v[42:45], v[164:167], v[180:183], v[42:45]
	v_mfma_f32_16x16x32_bf16 v[30:33], v[156:159], v[188:191], v[30:33]
	v_mfma_f32_16x16x32_bf16 v[26:29], v[164:167], v[188:191], v[26:29]
	v_mfma_f32_16x16x32_bf16 v[14:17], v[156:159], v[198:201], v[14:17]
	v_mfma_f32_16x16x32_bf16 v[10:13], v[164:167], v[198:201], v[10:13]
	s_barrier
	s_setprio 0
	s_add_i32 s28, s82, 2
	s_add_u32 s59, s59, 0x100
	s_addc_u32 s81, s81, 0
	s_add_u32 s26, s26, 0x10000
	s_addc_u32 s27, s27, 0
	s_cmp_lt_i32 s82, s63
	s_mov_b32 s82, s28
	s_cbranch_scc1 .LBB0_967

.LBB0_1072:
	s_add_u32 s21, s26, 0x10000
	s_addc_u32 s34, s27, 0
	s_and_b64 s[30:31], s[48:49], exec
	s_cselect_b32 s55, s43, s34
	s_cselect_b32 s54, s42, s21
	s_add_u32 s21, s28, 0x100
	s_addc_u32 s56, s29, 0
	s_add_u32 s30, s54, 0x8000
	s_addc_u32 s31, s55, 0
	s_add_i32 s71, 0, 0x10000
	s_and_b64 s[34:35], s[48:49], exec
	s_cselect_b32 s35, s45, s56
	s_cselect_b32 s34, s44, s21
	s_add_i32 s73, 0, 0x14000
	v_add_u32_e32 v114, s71, v237
	v_add_u32_e32 v115, s73, v237
	ds_read_b128 v[2:5], v114
	s_waitcnt lgkmcnt(0)
	ds_read_b128 v[6:9], v114 offset:1024
	ds_read_b128 v[10:13], v114 offset:2048
	ds_read_b128 v[14:17], v114 offset:3072
	ds_read_b128 v[18:21], v115
	ds_read_b128 v[22:25], v115 offset:1024
	ds_read_b128 v[26:29], v115 offset:2048
	ds_read_b128 v[30:33], v115 offset:3072
	s_add_u32 s56, s26, 0xc000
	s_addc_u32 s57, s27, 0
	s_add_i32 s21, s20, 0xc000
	s_mov_b32 m0, s21
	s_add_i32 s70, s20, 0xe000
	ds_read_b128 v[34:37], v238
	ds_read_b128 v[38:41], v238 offset:1024
	ds_read_b128 v[42:45], v238 offset:2048
	ds_read_b128 v[46:49], v238 offset:3072
	ds_read_b128 v[50:53], v238 offset:4096
	ds_read_b128 v[54:57], v238 offset:5120
	ds_read_b128 v[58:61], v238 offset:6144
	ds_read_b128 v[62:65], v238 offset:7168
	s_nop 0
	global_load_lds_dwordx4 v236, s[56:57]
	s_mov_b32 m0, s70
	s_nop 0
	global_load_lds_dwordx4 v235, s[56:57]
	s_waitcnt vmcnt(8)
	s_waitcnt lgkmcnt(0)
	s_setprio 1
	s_barrier
	s_waitcnt lgkmcnt(0)
	v_mfma_f32_16x16x32_bf16 v[90:93], v[2:5], v[58:61], 0
	v_mfma_f32_16x16x32_bf16 v[66:69], v[2:5], v[34:37], 0
	v_mfma_f32_16x16x32_bf16 v[70:73], v[10:13], v[34:37], 0
	v_mfma_f32_16x16x32_bf16 v[74:77], v[2:5], v[42:45], 0
	v_mfma_f32_16x16x32_bf16 v[78:81], v[10:13], v[42:45], 0
	v_mfma_f32_16x16x32_bf16 v[82:85], v[2:5], v[50:53], 0
	v_mfma_f32_16x16x32_bf16 v[86:89], v[10:13], v[50:53], 0
	v_mfma_f32_16x16x32_bf16 v[98:101], v[6:9], v[62:65], v[90:93]
	v_mfma_f32_16x16x32_bf16 v[90:93], v[10:13], v[58:61], 0
	v_mfma_f32_16x16x32_bf16 v[66:69], v[6:9], v[38:41], v[66:69]
	v_mfma_f32_16x16x32_bf16 v[70:73], v[14:17], v[38:41], v[70:73]
	v_mfma_f32_16x16x32_bf16 v[74:77], v[6:9], v[46:49], v[74:77]
	v_mfma_f32_16x16x32_bf16 v[78:81], v[14:17], v[46:49], v[78:81]
	v_mfma_f32_16x16x32_bf16 v[82:85], v[6:9], v[54:57], v[82:85]
	v_mfma_f32_16x16x32_bf16 v[86:89], v[14:17], v[54:57], v[86:89]
	v_mfma_f32_16x16x32_bf16 v[102:105], v[14:17], v[62:65], v[90:93]
	v_mfma_f32_16x16x32_bf16 v[90:93], v[18:21], v[34:37], 0
	v_mfma_f32_16x16x32_bf16 v[34:37], v[26:29], v[34:37], 0
	v_mfma_f32_16x16x32_bf16 v[118:121], v[22:25], v[38:41], v[90:93]
	v_mfma_f32_16x16x32_bf16 v[34:37], v[30:33], v[38:41], v[34:37]
	v_mfma_f32_16x16x32_bf16 v[38:41], v[18:21], v[42:45], 0
	v_mfma_f32_16x16x32_bf16 v[42:45], v[26:29], v[42:45], 0
	v_mfma_f32_16x16x32_bf16 v[38:41], v[22:25], v[46:49], v[38:41]
	v_mfma_f32_16x16x32_bf16 v[42:45], v[30:33], v[46:49], v[42:45]
	v_mfma_f32_16x16x32_bf16 v[46:49], v[18:21], v[50:53], 0
	v_mfma_f32_16x16x32_bf16 v[50:53], v[26:29], v[50:53], 0
	v_mfma_f32_16x16x32_bf16 v[46:49], v[22:25], v[54:57], v[46:49]
	v_mfma_f32_16x16x32_bf16 v[50:53], v[30:33], v[54:57], v[50:53]
	v_mfma_f32_16x16x32_bf16 v[54:57], v[18:21], v[58:61], 0
	v_mfma_f32_16x16x32_bf16 v[58:61], v[26:29], v[58:61], 0
	v_mfma_f32_16x16x32_bf16 v[54:57], v[22:25], v[62:65], v[54:57]
	v_mfma_f32_16x16x32_bf16 v[58:61], v[30:33], v[62:65], v[58:61]
	s_barrier
	s_setprio 0
	s_add_i32 s71, s71, s18
	s_add_i32 s72, s71, 0x2000
	s_mov_b32 m0, s71
	s_add_u32 s56, s34, s36
	ds_read_b128 v[62:65], v238 offset:16384
	ds_read_b128 v[90:93], v238 offset:17408
	ds_read_b128 v[94:97], v238 offset:18432
	ds_read_b128 v[106:109], v238 offset:19456
	ds_read_b128 v[110:113], v238 offset:20480
	ds_read_b128 v[122:125], v238 offset:21504
	ds_read_b128 v[126:129], v238 offset:22528
	ds_read_b128 v[130:133], v238 offset:23552
	s_addc_u32 s57, s35, s37
	global_load_lds_dwordx4 v0, s[34:35]
	s_mov_b32 m0, s72
	s_add_i32 s73, s73, s18
	s_add_i32 s74, s73, 0x2000
	global_load_lds_dwordx4 v210, s[34:35]
	s_mov_b32 m0, s73
	s_nop 0
	global_load_lds_dwordx4 v0, s[56:57]
	s_mov_b32 m0, s74
	s_nop 0
	global_load_lds_dwordx4 v210, s[56:57]
	s_mov_b32 m0, s20
	s_nop 0
	global_load_lds_dwordx4 v236, s[54:55]
	s_mov_b32 m0, s25
	s_nop 0
	global_load_lds_dwordx4 v235, s[54:55]
	s_waitcnt vmcnt(8)
	s_waitcnt lgkmcnt(0)
	s_setprio 1
	s_barrier
	s_waitcnt lgkmcnt(0)
	v_mfma_f32_16x16x32_bf16 v[134:137], v[2:5], v[62:65], 0
	v_mfma_f32_16x16x32_bf16 v[142:145], v[2:5], v[94:97], 0
	v_mfma_f32_16x16x32_bf16 v[150:153], v[2:5], v[110:113], 0
	v_mfma_f32_16x16x32_bf16 v[2:5], v[2:5], v[126:129], 0
	v_mfma_f32_16x16x32_bf16 v[134:137], v[6:9], v[90:93], v[134:137]
	v_mfma_f32_16x16x32_bf16 v[142:145], v[6:9], v[106:109], v[142:145]
	v_mfma_f32_16x16x32_bf16 v[150:153], v[6:9], v[122:125], v[150:153]
	v_mfma_f32_16x16x32_bf16 v[2:5], v[6:9], v[130:133], v[2:5]
	v_mfma_f32_16x16x32_bf16 v[6:9], v[10:13], v[126:129], 0
	v_mfma_f32_16x16x32_bf16 v[138:141], v[10:13], v[62:65], 0
	v_mfma_f32_16x16x32_bf16 v[146:149], v[10:13], v[94:97], 0
	v_mfma_f32_16x16x32_bf16 v[154:157], v[10:13], v[110:113], 0
	v_mfma_f32_16x16x32_bf16 v[6:9], v[14:17], v[130:133], v[6:9]
	v_mfma_f32_16x16x32_bf16 v[138:141], v[14:17], v[90:93], v[138:141]
	v_mfma_f32_16x16x32_bf16 v[146:149], v[14:17], v[106:109], v[146:149]
	v_mfma_f32_16x16x32_bf16 v[154:157], v[14:17], v[122:125], v[154:157]
	v_mfma_f32_16x16x32_bf16 v[10:13], v[18:21], v[62:65], 0
	v_mfma_f32_16x16x32_bf16 v[158:161], v[22:25], v[90:93], v[10:13]
	v_mfma_f32_16x16x32_bf16 v[10:13], v[26:29], v[62:65], 0
	v_mfma_f32_16x16x32_bf16 v[170:173], v[30:33], v[90:93], v[10:13]
	v_mfma_f32_16x16x32_bf16 v[10:13], v[18:21], v[94:97], 0
	v_mfma_f32_16x16x32_bf16 v[174:177], v[22:25], v[106:109], v[10:13]
	v_mfma_f32_16x16x32_bf16 v[10:13], v[26:29], v[94:97], 0
	v_mfma_f32_16x16x32_bf16 v[178:181], v[30:33], v[106:109], v[10:13]
	v_mfma_f32_16x16x32_bf16 v[10:13], v[18:21], v[110:113], 0
	v_mfma_f32_16x16x32_bf16 v[182:185], v[22:25], v[122:125], v[10:13]
	v_mfma_f32_16x16x32_bf16 v[10:13], v[26:29], v[110:113], 0
	v_mfma_f32_16x16x32_bf16 v[186:189], v[30:33], v[122:125], v[10:13]
	v_mfma_f32_16x16x32_bf16 v[10:13], v[18:21], v[126:129], 0
	v_mfma_f32_16x16x32_bf16 v[194:197], v[22:25], v[130:133], v[10:13]
	v_mfma_f32_16x16x32_bf16 v[10:13], v[26:29], v[126:129], 0
	v_mfma_f32_16x16x32_bf16 v[126:129], v[30:33], v[130:133], v[10:13]
	s_barrier
	s_setprio 0
	s_add_i32 s75, 0, 0x18000
	s_add_i32 s77, 0, 0x1c000
	v_add_u32_e32 v116, s75, v237
	v_add_u32_e32 v117, s77, v237
	s_nop 0
	ds_read_b128 v[10:13], v116
	ds_read_b128 v[14:17], v116 offset:1024
	ds_read_b128 v[18:21], v116 offset:2048
	ds_read_b128 v[22:25], v116 offset:3072
	ds_read_b128 v[130:133], v117
	ds_read_b128 v[198:201], v117 offset:1024
	ds_read_b128 v[202:205], v117 offset:2048
	ds_read_b128 v[206:209], v117 offset:3072
	s_add_u32 s54, s54, 0x4000
	s_addc_u32 s55, s55, 0
	s_mov_b32 m0, s58
	ds_read_b128 v[26:29], v238 offset:32768
	ds_read_b128 v[30:33], v238 offset:33792
	ds_read_b128 v[62:65], v238 offset:34816
	ds_read_b128 v[212:215], v238 offset:35840
	ds_read_b128 v[216:219], v238 offset:36864
	ds_read_b128 v[220:223], v238 offset:37888
	ds_read_b128 v[224:227], v238 offset:38912
	ds_read_b128 v[240:243], v238 offset:39936
	s_nop 0
	global_load_lds_dwordx4 v236, s[54:55]
	s_mov_b32 m0, s59
	s_nop 0
	global_load_lds_dwordx4 v235, s[54:55]
	s_waitcnt vmcnt(8)
	s_waitcnt lgkmcnt(0)
	s_setprio 1
	s_barrier
	s_waitcnt lgkmcnt(0)
	v_mfma_f32_16x16x32_bf16 v[66:69], v[10:13], v[26:29], v[66:69]
	v_mfma_f32_16x16x32_bf16 v[162:165], v[14:17], v[30:33], v[66:69]
	v_mfma_f32_16x16x32_bf16 v[66:69], v[18:21], v[26:29], v[70:73]
	v_mfma_f32_16x16x32_bf16 v[166:169], v[22:25], v[30:33], v[66:69]
	v_mfma_f32_16x16x32_bf16 v[66:69], v[10:13], v[62:65], v[74:77]
	v_mfma_f32_16x16x32_bf16 v[110:113], v[14:17], v[212:215], v[66:69]
	v_mfma_f32_16x16x32_bf16 v[66:69], v[18:21], v[62:65], v[78:81]
	v_mfma_f32_16x16x32_bf16 v[106:109], v[22:25], v[212:215], v[66:69]
	v_mfma_f32_16x16x32_bf16 v[66:69], v[10:13], v[216:219], v[82:85]
	v_mfma_f32_16x16x32_bf16 v[94:97], v[14:17], v[220:223], v[66:69]
	v_mfma_f32_16x16x32_bf16 v[66:69], v[18:21], v[216:219], v[86:89]
	v_mfma_f32_16x16x32_bf16 v[90:93], v[22:25], v[220:223], v[66:69]
	v_mfma_f32_16x16x32_bf16 v[66:69], v[10:13], v[224:227], v[98:101]
	v_mfma_f32_16x16x32_bf16 v[70:73], v[14:17], v[240:243], v[66:69]
	v_mfma_f32_16x16x32_bf16 v[66:69], v[18:21], v[224:227], v[102:105]
	v_mfma_f32_16x16x32_bf16 v[66:69], v[22:25], v[240:243], v[66:69]
	v_mfma_f32_16x16x32_bf16 v[74:77], v[130:133], v[26:29], v[118:121]
	v_mfma_f32_16x16x32_bf16 v[26:29], v[202:205], v[26:29], v[34:37]
	v_mfma_f32_16x16x32_bf16 v[118:121], v[206:209], v[30:33], v[26:29]
	v_mfma_f32_16x16x32_bf16 v[26:29], v[130:133], v[62:65], v[38:41]
	v_mfma_f32_16x16x32_bf16 v[102:105], v[198:201], v[212:215], v[26:29]
	v_mfma_f32_16x16x32_bf16 v[26:29], v[202:205], v[62:65], v[42:45]
	v_mfma_f32_16x16x32_bf16 v[98:101], v[206:209], v[212:215], v[26:29]
	v_mfma_f32_16x16x32_bf16 v[26:29], v[130:133], v[216:219], v[46:49]
	v_mfma_f32_16x16x32_bf16 v[86:89], v[198:201], v[220:223], v[26:29]
	v_mfma_f32_16x16x32_bf16 v[26:29], v[202:205], v[216:219], v[50:53]
	v_mfma_f32_16x16x32_bf16 v[82:85], v[206:209], v[220:223], v[26:29]
	v_mfma_f32_16x16x32_bf16 v[26:29], v[130:133], v[224:227], v[54:57]
	v_mfma_f32_16x16x32_bf16 v[54:57], v[198:201], v[240:243], v[26:29]
	v_mfma_f32_16x16x32_bf16 v[26:29], v[202:205], v[224:227], v[58:61]
	v_mfma_f32_16x16x32_bf16 v[122:125], v[198:201], v[30:33], v[74:77]
	v_mfma_f32_16x16x32_bf16 v[50:53], v[206:209], v[240:243], v[26:29]
	s_barrier
	s_setprio 0
	ds_read_b128 v[34:37], v238 offset:49152
	ds_read_b128 v[38:41], v238 offset:50176
	ds_read_b128 v[212:215], v238 offset:51200
	ds_read_b128 v[216:219], v238 offset:52224
	ds_read_b128 v[220:223], v238 offset:53248
	ds_read_b128 v[224:227], v238 offset:54272
	ds_read_b128 v[240:243], v238 offset:55296
	ds_read_b128 v[244:247], v238 offset:56320
	s_add_i32 s75, s75, s18
	v_lshl_add_u64 v[26:27], s[34:35], 0, v[0:1]
	v_lshl_add_u64 v[26:27], v[26:27], 0, s[16:17]
	s_mov_b32 m0, s75
	v_mov_b32_e32 v211, v1
	global_load_lds_dwordx4 v[26:27], off
	s_add_i32 s76, s75, 0x2000
	v_lshl_add_u64 v[26:27], s[34:35], 0, v[210:211]
	v_lshl_add_u64 v[26:27], v[26:27], 0, s[16:17]
	s_mov_b32 m0, s76
	s_add_i32 s77, s77, s18
	global_load_lds_dwordx4 v[26:27], off
	s_mov_b32 m0, s77
	v_lshl_add_u64 v[26:27], s[56:57], 0, v[0:1]
	v_lshl_add_u64 v[26:27], v[26:27], 0, s[16:17]
	global_load_lds_dwordx4 v[26:27], off
	s_nop 0
	v_lshl_add_u64 v[26:27], s[56:57], 0, v[210:211]
	s_add_i32 s56, s77, 0x2000
	v_lshl_add_u64 v[26:27], v[26:27], 0, s[16:17]
	s_mov_b32 m0, s56
	s_nop 0
	global_load_lds_dwordx4 v[26:27], off
	s_mov_b32 m0, s62
	s_nop 0
	global_load_lds_dwordx4 v236, s[30:31]
	s_mov_b32 m0, s63
	s_nop 0
	global_load_lds_dwordx4 v235, s[30:31]
	s_waitcnt vmcnt(8)
	s_waitcnt lgkmcnt(0)
	s_setprio 1
	s_barrier
	s_waitcnt lgkmcnt(0)
	v_mfma_f32_16x16x32_bf16 v[26:29], v[10:13], v[34:37], v[134:137]
	v_mfma_f32_16x16x32_bf16 v[78:81], v[14:17], v[38:41], v[26:29]
	v_mfma_f32_16x16x32_bf16 v[26:29], v[18:21], v[34:37], v[138:141]
	v_mfma_f32_16x16x32_bf16 v[74:77], v[22:25], v[38:41], v[26:29]
	v_mfma_f32_16x16x32_bf16 v[26:29], v[10:13], v[212:215], v[142:145]
	v_mfma_f32_16x16x32_bf16 v[46:49], v[14:17], v[216:219], v[26:29]
	v_mfma_f32_16x16x32_bf16 v[26:29], v[18:21], v[212:215], v[146:149]
	v_mfma_f32_16x16x32_bf16 v[42:45], v[22:25], v[216:219], v[26:29]
	v_mfma_f32_16x16x32_bf16 v[26:29], v[10:13], v[220:223], v[150:153]
	v_mfma_f32_16x16x32_bf16 v[2:5], v[10:13], v[240:243], v[2:5]
	v_mfma_f32_16x16x32_bf16 v[30:33], v[14:17], v[224:227], v[26:29]
	v_mfma_f32_16x16x32_bf16 v[26:29], v[18:21], v[220:223], v[154:157]
	v_mfma_f32_16x16x32_bf16 v[14:17], v[14:17], v[244:247], v[2:5]
	v_mfma_f32_16x16x32_bf16 v[2:5], v[18:21], v[240:243], v[6:9]
	v_mfma_f32_16x16x32_bf16 v[26:29], v[22:25], v[224:227], v[26:29]
	v_mfma_f32_16x16x32_bf16 v[10:13], v[22:25], v[244:247], v[2:5]
	v_mfma_f32_16x16x32_bf16 v[2:5], v[130:133], v[34:37], v[158:161]
	v_mfma_f32_16x16x32_bf16 v[62:65], v[198:201], v[38:41], v[2:5]
	v_mfma_f32_16x16x32_bf16 v[2:5], v[202:205], v[34:37], v[170:173]
	v_mfma_f32_16x16x32_bf16 v[58:61], v[206:209], v[38:41], v[2:5]
	v_mfma_f32_16x16x32_bf16 v[2:5], v[130:133], v[212:215], v[174:177]
	v_mfma_f32_16x16x32_bf16 v[38:41], v[198:201], v[216:219], v[2:5]
	v_mfma_f32_16x16x32_bf16 v[2:5], v[202:205], v[212:215], v[178:181]
	v_mfma_f32_16x16x32_bf16 v[34:37], v[206:209], v[216:219], v[2:5]
	v_mfma_f32_16x16x32_bf16 v[2:5], v[130:133], v[220:223], v[182:185]
	v_mfma_f32_16x16x32_bf16 v[22:25], v[198:201], v[224:227], v[2:5]
	v_mfma_f32_16x16x32_bf16 v[2:5], v[202:205], v[220:223], v[186:189]
	v_mfma_f32_16x16x32_bf16 v[18:21], v[206:209], v[224:227], v[2:5]
	v_mfma_f32_16x16x32_bf16 v[2:5], v[130:133], v[240:243], v[194:197]
	v_mfma_f32_16x16x32_bf16 v[6:9], v[198:201], v[244:247], v[2:5]
	v_mfma_f32_16x16x32_bf16 v[2:5], v[202:205], v[240:243], v[126:129]
	v_mfma_f32_16x16x32_bf16 v[2:5], v[206:209], v[244:247], v[2:5]
	s_barrier
	s_setprio 0
	s_andn2_b64 vcc, exec, s[50:51]
	s_cbranch_vccnz .LBB0_1075
	s_add_u32 s57, s28, 0x200
	s_addc_u32 s78, s29, 0
	s_add_u32 s26, s26, 0x1c000
	s_addc_u32 s27, s27, 0
	s_mov_b32 s79, 4
.LBB0_1074:
	ds_read_b128 v[126:129], v114
	ds_read_b128 v[130:133], v114 offset:1024
	ds_read_b128 v[134:137], v114 offset:2048
	ds_read_b128 v[138:141], v114 offset:3072
	ds_read_b128 v[142:145], v115
	ds_read_b128 v[146:149], v115 offset:1024
	ds_read_b128 v[150:153], v115 offset:2048
	ds_read_b128 v[154:157], v115 offset:3072
	s_add_u32 s28, s26, 0x4000
	s_addc_u32 s29, s27, 0
	s_cmp_eq_u32 s60, s79
	s_cselect_b32 s34, s42, s28
	s_cselect_b32 s35, s43, s29
	s_cselect_b32 s30, s44, s57
	s_cselect_b32 s31, s45, s78
	s_add_u32 s28, s34, 0x8000
	s_addc_u32 s29, s35, 0
	s_mov_b32 m0, s21
	ds_read_b128 v[158:161], v238
	ds_read_b128 v[170:173], v238 offset:1024
	ds_read_b128 v[174:177], v238 offset:2048
	ds_read_b128 v[178:181], v238 offset:3072
	ds_read_b128 v[182:185], v238 offset:4096
	ds_read_b128 v[186:189], v238 offset:5120
	ds_read_b128 v[194:197], v238 offset:6144
	ds_read_b128 v[198:201], v238 offset:7168
	s_nop 0
	global_load_lds_dwordx4 v236, s[26:27]
	s_mov_b32 m0, s70
	s_nop 0
	global_load_lds_dwordx4 v235, s[26:27]
	s_waitcnt vmcnt(8)
	s_waitcnt lgkmcnt(0)
	s_setprio 1
	s_barrier
	s_waitcnt lgkmcnt(0)
	v_mfma_f32_16x16x32_bf16 v[162:165], v[126:129], v[158:161], v[162:165]
	v_mfma_f32_16x16x32_bf16 v[166:169], v[134:137], v[158:161], v[166:169]
	v_mfma_f32_16x16x32_bf16 v[110:113], v[126:129], v[174:177], v[110:113]
	v_mfma_f32_16x16x32_bf16 v[106:109], v[134:137], v[174:177], v[106:109]
	v_mfma_f32_16x16x32_bf16 v[94:97], v[126:129], v[182:185], v[94:97]
	v_mfma_f32_16x16x32_bf16 v[90:93], v[134:137], v[182:185], v[90:93]
	v_mfma_f32_16x16x32_bf16 v[70:73], v[126:129], v[194:197], v[70:73]
	v_mfma_f32_16x16x32_bf16 v[66:69], v[134:137], v[194:197], v[66:69]
	v_mfma_f32_16x16x32_bf16 v[162:165], v[130:133], v[170:173], v[162:165]
	v_mfma_f32_16x16x32_bf16 v[166:169], v[138:141], v[170:173], v[166:169]
	v_mfma_f32_16x16x32_bf16 v[110:113], v[130:133], v[178:181], v[110:113]
	v_mfma_f32_16x16x32_bf16 v[106:109], v[138:141], v[178:181], v[106:109]
	v_mfma_f32_16x16x32_bf16 v[94:97], v[130:133], v[186:189], v[94:97]
	v_mfma_f32_16x16x32_bf16 v[90:93], v[138:141], v[186:189], v[90:93]
	v_mfma_f32_16x16x32_bf16 v[70:73], v[130:133], v[198:201], v[70:73]
	v_mfma_f32_16x16x32_bf16 v[66:69], v[138:141], v[198:201], v[66:69]
	v_mfma_f32_16x16x32_bf16 v[122:125], v[142:145], v[158:161], v[122:125]
	v_mfma_f32_16x16x32_bf16 v[118:121], v[150:153], v[158:161], v[118:121]
	v_mfma_f32_16x16x32_bf16 v[102:105], v[142:145], v[174:177], v[102:105]
	v_mfma_f32_16x16x32_bf16 v[98:101], v[150:153], v[174:177], v[98:101]
	v_mfma_f32_16x16x32_bf16 v[86:89], v[142:145], v[182:185], v[86:89]
	v_mfma_f32_16x16x32_bf16 v[82:85], v[150:153], v[182:185], v[82:85]
	v_mfma_f32_16x16x32_bf16 v[54:57], v[142:145], v[194:197], v[54:57]
	v_mfma_f32_16x16x32_bf16 v[50:53], v[150:153], v[194:197], v[50:53]
	v_mfma_f32_16x16x32_bf16 v[122:125], v[146:149], v[170:173], v[122:125]
	v_mfma_f32_16x16x32_bf16 v[118:121], v[154:157], v[170:173], v[118:121]
	v_mfma_f32_16x16x32_bf16 v[102:105], v[146:149], v[178:181], v[102:105]
	v_mfma_f32_16x16x32_bf16 v[98:101], v[154:157], v[178:181], v[98:101]
	v_mfma_f32_16x16x32_bf16 v[86:89], v[146:149], v[186:189], v[86:89]
	v_mfma_f32_16x16x32_bf16 v[82:85], v[154:157], v[186:189], v[82:85]
	v_mfma_f32_16x16x32_bf16 v[54:57], v[146:149], v[198:201], v[54:57]
	v_mfma_f32_16x16x32_bf16 v[50:53], v[154:157], v[198:201], v[50:53]
	s_barrier
	s_setprio 0
	s_mov_b32 m0, s71
	ds_read_b128 v[158:161], v238 offset:16384
	ds_read_b128 v[170:173], v238 offset:17408
	ds_read_b128 v[174:177], v238 offset:18432
	ds_read_b128 v[178:181], v238 offset:19456
	ds_read_b128 v[182:185], v238 offset:20480
	ds_read_b128 v[186:189], v238 offset:21504
	ds_read_b128 v[194:197], v238 offset:22528
	ds_read_b128 v[198:201], v238 offset:23552
	s_add_u32 s54, s30, s36
	global_load_lds_dwordx4 v0, s[30:31]
	s_mov_b32 m0, s72
	s_addc_u32 s55, s31, s37
	global_load_lds_dwordx4 v210, s[30:31]
	s_mov_b32 m0, s73
	s_nop 0
	global_load_lds_dwordx4 v0, s[54:55]
	s_mov_b32 m0, s74
	s_nop 0
	global_load_lds_dwordx4 v210, s[54:55]
	s_mov_b32 m0, s20
	s_nop 0
	global_load_lds_dwordx4 v236, s[34:35]
	s_mov_b32 m0, s25
	s_nop 0
	global_load_lds_dwordx4 v235, s[34:35]
	s_waitcnt vmcnt(8)
	s_waitcnt lgkmcnt(0)
	s_setprio 1
	s_barrier
	s_waitcnt lgkmcnt(0)
	v_mfma_f32_16x16x32_bf16 v[78:81], v[126:129], v[158:161], v[78:81]
	v_mfma_f32_16x16x32_bf16 v[74:77], v[134:137], v[158:161], v[74:77]
	v_mfma_f32_16x16x32_bf16 v[46:49], v[126:129], v[174:177], v[46:49]
	v_mfma_f32_16x16x32_bf16 v[42:45], v[134:137], v[174:177], v[42:45]
	v_mfma_f32_16x16x32_bf16 v[30:33], v[126:129], v[182:185], v[30:33]
	v_mfma_f32_16x16x32_bf16 v[26:29], v[134:137], v[182:185], v[26:29]
	v_mfma_f32_16x16x32_bf16 v[14:17], v[126:129], v[194:197], v[14:17]
	v_mfma_f32_16x16x32_bf16 v[10:13], v[134:137], v[194:197], v[10:13]
	v_mfma_f32_16x16x32_bf16 v[78:81], v[130:133], v[170:173], v[78:81]
	v_mfma_f32_16x16x32_bf16 v[74:77], v[138:141], v[170:173], v[74:77]
	v_mfma_f32_16x16x32_bf16 v[46:49], v[130:133], v[178:181], v[46:49]
	v_mfma_f32_16x16x32_bf16 v[42:45], v[138:141], v[178:181], v[42:45]
	v_mfma_f32_16x16x32_bf16 v[30:33], v[130:133], v[186:189], v[30:33]
	v_mfma_f32_16x16x32_bf16 v[26:29], v[138:141], v[186:189], v[26:29]
	v_mfma_f32_16x16x32_bf16 v[14:17], v[130:133], v[198:201], v[14:17]
	v_mfma_f32_16x16x32_bf16 v[10:13], v[138:141], v[198:201], v[10:13]
	v_mfma_f32_16x16x32_bf16 v[62:65], v[142:145], v[158:161], v[62:65]
	v_mfma_f32_16x16x32_bf16 v[58:61], v[150:153], v[158:161], v[58:61]
	v_mfma_f32_16x16x32_bf16 v[38:41], v[142:145], v[174:177], v[38:41]
	v_mfma_f32_16x16x32_bf16 v[34:37], v[150:153], v[174:177], v[34:37]
	v_mfma_f32_16x16x32_bf16 v[22:25], v[142:145], v[182:185], v[22:25]
	v_mfma_f32_16x16x32_bf16 v[18:21], v[150:153], v[182:185], v[18:21]
	v_mfma_f32_16x16x32_bf16 v[6:9], v[142:145], v[194:197], v[6:9]
	v_mfma_f32_16x16x32_bf16 v[2:5], v[150:153], v[194:197], v[2:5]
	v_mfma_f32_16x16x32_bf16 v[62:65], v[146:149], v[170:173], v[62:65]
	v_mfma_f32_16x16x32_bf16 v[58:61], v[154:157], v[170:173], v[58:61]
	v_mfma_f32_16x16x32_bf16 v[38:41], v[146:149], v[178:181], v[38:41]
	v_mfma_f32_16x16x32_bf16 v[34:37], v[154:157], v[178:181], v[34:37]
	v_mfma_f32_16x16x32_bf16 v[22:25], v[146:149], v[186:189], v[22:25]
	v_mfma_f32_16x16x32_bf16 v[18:21], v[154:157], v[186:189], v[18:21]
	v_mfma_f32_16x16x32_bf16 v[6:9], v[146:149], v[198:201], v[6:9]
	v_mfma_f32_16x16x32_bf16 v[2:5], v[154:157], v[198:201], v[2:5]
	s_barrier
	s_setprio 0
	ds_read_b128 v[126:129], v116
	ds_read_b128 v[130:133], v116 offset:1024
	ds_read_b128 v[134:137], v116 offset:2048
	ds_read_b128 v[138:141], v116 offset:3072
	ds_read_b128 v[142:145], v117
	ds_read_b128 v[146:149], v117 offset:1024
	ds_read_b128 v[150:153], v117 offset:2048
	ds_read_b128 v[154:157], v117 offset:3072
	s_add_u32 s34, s34, 0x4000
	s_addc_u32 s35, s35, 0
	s_mov_b32 m0, s58
	ds_read_b128 v[158:161], v238 offset:32768
	ds_read_b128 v[170:173], v238 offset:33792
	ds_read_b128 v[174:177], v238 offset:34816
	ds_read_b128 v[178:181], v238 offset:35840
	ds_read_b128 v[182:185], v238 offset:36864
	ds_read_b128 v[186:189], v238 offset:37888
	ds_read_b128 v[194:197], v238 offset:38912
	ds_read_b128 v[198:201], v238 offset:39936
	s_nop 0
	global_load_lds_dwordx4 v236, s[34:35]
	s_mov_b32 m0, s59
	s_nop 0
	global_load_lds_dwordx4 v235, s[34:35]
	s_waitcnt vmcnt(8)
	s_waitcnt lgkmcnt(0)
	s_setprio 1
	s_barrier
	s_waitcnt lgkmcnt(0)
	v_mfma_f32_16x16x32_bf16 v[162:165], v[126:129], v[158:161], v[162:165]
	v_mfma_f32_16x16x32_bf16 v[166:169], v[134:137], v[158:161], v[166:169]
	v_mfma_f32_16x16x32_bf16 v[110:113], v[126:129], v[174:177], v[110:113]
	v_mfma_f32_16x16x32_bf16 v[106:109], v[134:137], v[174:177], v[106:109]
	v_mfma_f32_16x16x32_bf16 v[94:97], v[126:129], v[182:185], v[94:97]
	v_mfma_f32_16x16x32_bf16 v[90:93], v[134:137], v[182:185], v[90:93]
	v_mfma_f32_16x16x32_bf16 v[70:73], v[126:129], v[194:197], v[70:73]
	v_mfma_f32_16x16x32_bf16 v[66:69], v[134:137], v[194:197], v[66:69]
	v_mfma_f32_16x16x32_bf16 v[162:165], v[130:133], v[170:173], v[162:165]
	v_mfma_f32_16x16x32_bf16 v[166:169], v[138:141], v[170:173], v[166:169]
	v_mfma_f32_16x16x32_bf16 v[110:113], v[130:133], v[178:181], v[110:113]
	v_mfma_f32_16x16x32_bf16 v[106:109], v[138:141], v[178:181], v[106:109]
	v_mfma_f32_16x16x32_bf16 v[94:97], v[130:133], v[186:189], v[94:97]
	v_mfma_f32_16x16x32_bf16 v[90:93], v[138:141], v[186:189], v[90:93]
	v_mfma_f32_16x16x32_bf16 v[70:73], v[130:133], v[198:201], v[70:73]
	v_mfma_f32_16x16x32_bf16 v[66:69], v[138:141], v[198:201], v[66:69]
	v_mfma_f32_16x16x32_bf16 v[122:125], v[142:145], v[158:161], v[122:125]
	v_mfma_f32_16x16x32_bf16 v[118:121], v[150:153], v[158:161], v[118:121]
	v_mfma_f32_16x16x32_bf16 v[102:105], v[142:145], v[174:177], v[102:105]
	v_mfma_f32_16x16x32_bf16 v[98:101], v[150:153], v[174:177], v[98:101]
	v_mfma_f32_16x16x32_bf16 v[86:89], v[142:145], v[182:185], v[86:89]
	v_mfma_f32_16x16x32_bf16 v[82:85], v[150:153], v[182:185], v[82:85]
	v_mfma_f32_16x16x32_bf16 v[54:57], v[142:145], v[194:197], v[54:57]
	v_mfma_f32_16x16x32_bf16 v[50:53], v[150:153], v[194:197], v[50:53]
	v_mfma_f32_16x16x32_bf16 v[122:125], v[146:149], v[170:173], v[122:125]
	v_mfma_f32_16x16x32_bf16 v[118:121], v[154:157], v[170:173], v[118:121]
	v_mfma_f32_16x16x32_bf16 v[102:105], v[146:149], v[178:181], v[102:105]
	v_mfma_f32_16x16x32_bf16 v[98:101], v[154:157], v[178:181], v[98:101]
	v_mfma_f32_16x16x32_bf16 v[86:89], v[146:149], v[186:189], v[86:89]
	v_mfma_f32_16x16x32_bf16 v[82:85], v[154:157], v[186:189], v[82:85]
	v_mfma_f32_16x16x32_bf16 v[54:57], v[146:149], v[198:201], v[54:57]
	v_mfma_f32_16x16x32_bf16 v[50:53], v[154:157], v[198:201], v[50:53]
	s_barrier
	s_setprio 0
	ds_read_b128 v[158:161], v238 offset:49152
	ds_read_b128 v[170:173], v238 offset:50176
	ds_read_b128 v[174:177], v238 offset:51200
	ds_read_b128 v[178:181], v238 offset:52224
	ds_read_b128 v[182:185], v238 offset:53248
	ds_read_b128 v[186:189], v238 offset:54272
	ds_read_b128 v[194:197], v238 offset:55296
	ds_read_b128 v[198:201], v238 offset:56320
	s_mov_b32 m0, s75
	v_lshl_add_u64 v[190:191], s[30:31], 0, v[0:1]
	v_lshl_add_u64 v[190:191], v[190:191], 0, s[16:17]
	v_mov_b32_e32 v211, v1
	global_load_lds_dwordx4 v[190:191], off
	s_mov_b32 m0, s76
	v_lshl_add_u64 v[190:191], s[30:31], 0, v[210:211]
	v_lshl_add_u64 v[190:191], v[190:191], 0, s[16:17]
	global_load_lds_dwordx4 v[190:191], off
	s_mov_b32 m0, s77
	v_lshl_add_u64 v[190:191], s[54:55], 0, v[0:1]
	v_lshl_add_u64 v[190:191], v[190:191], 0, s[16:17]
	global_load_lds_dwordx4 v[190:191], off
	s_mov_b32 m0, s56
	v_lshl_add_u64 v[190:191], s[54:55], 0, v[210:211]
	v_lshl_add_u64 v[190:191], v[190:191], 0, s[16:17]
	global_load_lds_dwordx4 v[190:191], off
	s_mov_b32 m0, s62
	s_nop 0
	global_load_lds_dwordx4 v236, s[28:29]
	s_mov_b32 m0, s63
	s_nop 0
	global_load_lds_dwordx4 v235, s[28:29]
	s_waitcnt vmcnt(8)
	s_waitcnt lgkmcnt(0)
	s_setprio 1
	s_barrier
	s_waitcnt lgkmcnt(0)
	v_mfma_f32_16x16x32_bf16 v[78:81], v[126:129], v[158:161], v[78:81]
	v_mfma_f32_16x16x32_bf16 v[74:77], v[134:137], v[158:161], v[74:77]
	v_mfma_f32_16x16x32_bf16 v[46:49], v[126:129], v[174:177], v[46:49]
	v_mfma_f32_16x16x32_bf16 v[42:45], v[134:137], v[174:177], v[42:45]
	v_mfma_f32_16x16x32_bf16 v[30:33], v[126:129], v[182:185], v[30:33]
	v_mfma_f32_16x16x32_bf16 v[26:29], v[134:137], v[182:185], v[26:29]
	v_mfma_f32_16x16x32_bf16 v[14:17], v[126:129], v[194:197], v[14:17]
	v_mfma_f32_16x16x32_bf16 v[10:13], v[134:137], v[194:197], v[10:13]
	v_mfma_f32_16x16x32_bf16 v[78:81], v[130:133], v[170:173], v[78:81]
	v_mfma_f32_16x16x32_bf16 v[74:77], v[138:141], v[170:173], v[74:77]
	v_mfma_f32_16x16x32_bf16 v[46:49], v[130:133], v[178:181], v[46:49]
	v_mfma_f32_16x16x32_bf16 v[42:45], v[138:141], v[178:181], v[42:45]
	v_mfma_f32_16x16x32_bf16 v[30:33], v[130:133], v[186:189], v[30:33]
	v_mfma_f32_16x16x32_bf16 v[26:29], v[138:141], v[186:189], v[26:29]
	v_mfma_f32_16x16x32_bf16 v[14:17], v[130:133], v[198:201], v[14:17]
	v_mfma_f32_16x16x32_bf16 v[10:13], v[138:141], v[198:201], v[10:13]
	v_mfma_f32_16x16x32_bf16 v[62:65], v[142:145], v[158:161], v[62:65]
	v_mfma_f32_16x16x32_bf16 v[58:61], v[150:153], v[158:161], v[58:61]
	v_mfma_f32_16x16x32_bf16 v[38:41], v[142:145], v[174:177], v[38:41]
	v_mfma_f32_16x16x32_bf16 v[34:37], v[150:153], v[174:177], v[34:37]
	v_mfma_f32_16x16x32_bf16 v[22:25], v[142:145], v[182:185], v[22:25]
	v_mfma_f32_16x16x32_bf16 v[18:21], v[150:153], v[182:185], v[18:21]
	v_mfma_f32_16x16x32_bf16 v[6:9], v[142:145], v[194:197], v[6:9]
	v_mfma_f32_16x16x32_bf16 v[2:5], v[150:153], v[194:197], v[2:5]
	v_mfma_f32_16x16x32_bf16 v[62:65], v[146:149], v[170:173], v[62:65]
	v_mfma_f32_16x16x32_bf16 v[58:61], v[154:157], v[170:173], v[58:61]
	v_mfma_f32_16x16x32_bf16 v[38:41], v[146:149], v[178:181], v[38:41]
	v_mfma_f32_16x16x32_bf16 v[34:37], v[154:157], v[178:181], v[34:37]
	v_mfma_f32_16x16x32_bf16 v[22:25], v[146:149], v[186:189], v[22:25]
	v_mfma_f32_16x16x32_bf16 v[18:21], v[154:157], v[186:189], v[18:21]
	v_mfma_f32_16x16x32_bf16 v[6:9], v[146:149], v[198:201], v[6:9]
	v_mfma_f32_16x16x32_bf16 v[2:5], v[154:157], v[198:201], v[2:5]
	s_barrier
	s_setprio 0
	s_add_i32 s28, s79, 2
	s_add_u32 s57, s57, 0x100
	s_addc_u32 s78, s78, 0
	s_add_u32 s26, s26, 0x10000
	s_addc_u32 s27, s27, 0
	s_cmp_lt_i32 s79, s60
	s_mov_b32 s79, s28
	s_cbranch_scc1 .LBB0_1074

.LBB0_1147:
	s_or_b64 exec, exec, s[58:59]
	s_add_u32 s60, s54, 0x10000
	s_addc_u32 s61, s55, 0
	s_and_b64 s[58:59], s[34:35], exec
	s_cselect_b32 s65, s49, s61
	s_cselect_b32 s64, s48, s60
	s_add_u32 s60, s56, 0x10000
	s_addc_u32 s61, s57, 0
	s_and_b64 s[58:59], s[34:35], exec
	s_cselect_b32 s61, s51, s61
	s_cselect_b32 s60, s50, s60
	s_add_u32 s58, s64, 0x8000
	s_addc_u32 s59, s65, 0
	s_add_u32 s62, s60, 0x8000
	s_addc_u32 s63, s61, 0
	s_add_i32 s82, 0, 0x10000
	s_add_i32 s83, 0, 0x14000
	v_add_u32_e32 v132, s82, v140
	v_add_u32_e32 v133, s83, v140
	ds_read_b128 v[2:5], v132
	ds_read_b128 v[6:9], v132 offset:1024
	ds_read_b128 v[10:13], v132 offset:2048
	ds_read_b128 v[14:17], v132 offset:3072
	ds_read_b128 v[18:21], v133
	ds_read_b128 v[22:25], v133 offset:1024
	ds_read_b128 v[26:29], v133 offset:2048
	ds_read_b128 v[30:33], v133 offset:3072
	s_add_u32 s80, s54, 0xc000
	s_addc_u32 s81, s55, 0
	s_add_i32 s78, s15, 0xc000
	s_mov_b32 m0, s78
	s_add_i32 s79, s15, 0xe000
	ds_read_b128 v[34:37], v142
	ds_read_b128 v[38:41], v142 offset:1024
	ds_read_b128 v[42:45], v142 offset:2048
	ds_read_b128 v[46:49], v142 offset:3072
	ds_read_b128 v[50:53], v142 offset:4096
	ds_read_b128 v[54:57], v142 offset:5120
	ds_read_b128 v[58:61], v142 offset:6144
	ds_read_b128 v[62:65], v142 offset:7168
	s_nop 0
	global_load_lds_dwordx4 v136, s[80:81]
	s_mov_b32 m0, s79
	s_nop 0
	global_load_lds_dwordx4 v138, s[80:81]
	s_waitcnt vmcnt(8)
	s_waitcnt lgkmcnt(0)
	s_setprio 1
	s_barrier
	s_waitcnt lgkmcnt(0)
	v_mfma_f32_16x16x32_bf16 v[86:89], v[10:13], v[50:53], 0
	v_mfma_f32_16x16x32_bf16 v[90:93], v[14:17], v[54:57], v[86:89]
	v_mfma_f32_16x16x32_bf16 v[86:89], v[2:5], v[58:61], 0
	v_mfma_f32_16x16x32_bf16 v[66:69], v[2:5], v[34:37], 0
	v_mfma_f32_16x16x32_bf16 v[70:73], v[10:13], v[34:37], 0
	v_mfma_f32_16x16x32_bf16 v[74:77], v[2:5], v[42:45], 0
	v_mfma_f32_16x16x32_bf16 v[78:81], v[10:13], v[42:45], 0
	v_mfma_f32_16x16x32_bf16 v[82:85], v[2:5], v[50:53], 0
	v_mfma_f32_16x16x32_bf16 v[94:97], v[6:9], v[62:65], v[86:89]
	v_mfma_f32_16x16x32_bf16 v[86:89], v[10:13], v[58:61], 0
	v_mfma_f32_16x16x32_bf16 v[66:69], v[6:9], v[38:41], v[66:69]
	v_mfma_f32_16x16x32_bf16 v[70:73], v[14:17], v[38:41], v[70:73]
	v_mfma_f32_16x16x32_bf16 v[74:77], v[6:9], v[46:49], v[74:77]
	v_mfma_f32_16x16x32_bf16 v[78:81], v[14:17], v[46:49], v[78:81]
	v_mfma_f32_16x16x32_bf16 v[82:85], v[6:9], v[54:57], v[82:85]
	v_mfma_f32_16x16x32_bf16 v[106:109], v[14:17], v[62:65], v[86:89]
	v_mfma_f32_16x16x32_bf16 v[86:89], v[18:21], v[34:37], 0
	v_mfma_f32_16x16x32_bf16 v[34:37], v[26:29], v[34:37], 0
	v_mfma_f32_16x16x32_bf16 v[110:113], v[22:25], v[38:41], v[86:89]
	v_mfma_f32_16x16x32_bf16 v[34:37], v[30:33], v[38:41], v[34:37]
	v_mfma_f32_16x16x32_bf16 v[38:41], v[18:21], v[42:45], 0
	v_mfma_f32_16x16x32_bf16 v[42:45], v[26:29], v[42:45], 0
	v_mfma_f32_16x16x32_bf16 v[38:41], v[22:25], v[46:49], v[38:41]
	v_mfma_f32_16x16x32_bf16 v[42:45], v[30:33], v[46:49], v[42:45]
	v_mfma_f32_16x16x32_bf16 v[46:49], v[18:21], v[50:53], 0
	v_mfma_f32_16x16x32_bf16 v[50:53], v[26:29], v[50:53], 0
	v_mfma_f32_16x16x32_bf16 v[46:49], v[22:25], v[54:57], v[46:49]
	v_mfma_f32_16x16x32_bf16 v[50:53], v[30:33], v[54:57], v[50:53]
	v_mfma_f32_16x16x32_bf16 v[54:57], v[18:21], v[58:61], 0
	v_mfma_f32_16x16x32_bf16 v[144:147], v[22:25], v[62:65], v[54:57]
	v_mfma_f32_16x16x32_bf16 v[54:57], v[26:29], v[58:61], 0
	v_mfma_f32_16x16x32_bf16 v[58:61], v[30:33], v[62:65], v[54:57]
	s_barrier
	s_setprio 0
	s_add_i32 s80, s82, s14
	s_add_i32 s81, s80, 0x2000
	s_mov_b32 m0, s80
	s_add_u32 s84, s60, 0x4000
	s_nop 0
	ds_read_b128 v[54:57], v142 offset:16384
	ds_read_b128 v[62:65], v142 offset:17408
	ds_read_b128 v[86:89], v142 offset:18432
	ds_read_b128 v[98:101], v142 offset:19456
	ds_read_b128 v[102:105], v142 offset:20480
	ds_read_b128 v[114:117], v142 offset:21504
	ds_read_b128 v[118:121], v142 offset:22528
	ds_read_b128 v[122:125], v142 offset:23552
	s_addc_u32 s85, s61, 0
	global_load_lds_dwordx4 v137, s[60:61]
	s_mov_b32 m0, s81
	s_add_i32 s82, s83, s14
	s_add_i32 s83, s82, 0x2000
	global_load_lds_dwordx4 v139, s[60:61]
	s_mov_b32 m0, s82
	s_nop 0
	global_load_lds_dwordx4 v137, s[84:85]
	s_mov_b32 m0, s83
	s_nop 0
	global_load_lds_dwordx4 v139, s[84:85]
	s_mov_b32 m0, s15
	s_nop 0
	global_load_lds_dwordx4 v136, s[64:65]
	s_mov_b32 m0, s18
	s_nop 0
	global_load_lds_dwordx4 v138, s[64:65]
	s_waitcnt vmcnt(8)
	s_waitcnt lgkmcnt(0)
	s_setprio 1
	s_barrier
	s_waitcnt lgkmcnt(0)
	v_mfma_f32_16x16x32_bf16 v[126:129], v[2:5], v[54:57], 0
	v_mfma_f32_16x16x32_bf16 v[148:151], v[6:9], v[62:65], v[126:129]
	v_mfma_f32_16x16x32_bf16 v[126:129], v[10:13], v[54:57], 0
	v_mfma_f32_16x16x32_bf16 v[152:155], v[14:17], v[62:65], v[126:129]
	v_mfma_f32_16x16x32_bf16 v[126:129], v[2:5], v[86:89], 0
	v_mfma_f32_16x16x32_bf16 v[156:159], v[6:9], v[98:101], v[126:129]
	v_mfma_f32_16x16x32_bf16 v[126:129], v[10:13], v[86:89], 0
	v_mfma_f32_16x16x32_bf16 v[160:163], v[14:17], v[98:101], v[126:129]
	v_mfma_f32_16x16x32_bf16 v[126:129], v[2:5], v[102:105], 0
	v_mfma_f32_16x16x32_bf16 v[2:5], v[2:5], v[118:121], 0
	v_mfma_f32_16x16x32_bf16 v[164:167], v[6:9], v[114:117], v[126:129]
	v_mfma_f32_16x16x32_bf16 v[2:5], v[6:9], v[122:125], v[2:5]
	v_mfma_f32_16x16x32_bf16 v[6:9], v[10:13], v[118:121], 0
	v_mfma_f32_16x16x32_bf16 v[126:129], v[10:13], v[102:105], 0
	v_mfma_f32_16x16x32_bf16 v[10:13], v[14:17], v[122:125], v[6:9]
	v_mfma_f32_16x16x32_bf16 v[168:171], v[14:17], v[114:117], v[126:129]
	v_mfma_f32_16x16x32_bf16 v[6:9], v[18:21], v[54:57], 0
	v_mfma_f32_16x16x32_bf16 v[14:17], v[22:25], v[62:65], v[6:9]
	v_mfma_f32_16x16x32_bf16 v[6:9], v[26:29], v[54:57], 0
	v_mfma_f32_16x16x32_bf16 v[172:175], v[30:33], v[62:65], v[6:9]
	v_mfma_f32_16x16x32_bf16 v[6:9], v[18:21], v[86:89], 0
	v_mfma_f32_16x16x32_bf16 v[176:179], v[22:25], v[98:101], v[6:9]
	v_mfma_f32_16x16x32_bf16 v[6:9], v[26:29], v[86:89], 0
	v_mfma_f32_16x16x32_bf16 v[180:183], v[30:33], v[98:101], v[6:9]
	v_mfma_f32_16x16x32_bf16 v[6:9], v[18:21], v[102:105], 0
	v_mfma_f32_16x16x32_bf16 v[184:187], v[22:25], v[114:117], v[6:9]
	v_mfma_f32_16x16x32_bf16 v[6:9], v[26:29], v[102:105], 0
	v_mfma_f32_16x16x32_bf16 v[188:191], v[30:33], v[114:117], v[6:9]
	v_mfma_f32_16x16x32_bf16 v[6:9], v[18:21], v[118:121], 0
	v_mfma_f32_16x16x32_bf16 v[194:197], v[22:25], v[122:125], v[6:9]
	v_mfma_f32_16x16x32_bf16 v[6:9], v[26:29], v[118:121], 0
	v_mfma_f32_16x16x32_bf16 v[198:201], v[30:33], v[122:125], v[6:9]
	s_barrier
	s_setprio 0
	s_add_i32 s84, 0, 0x18000
	s_add_i32 s85, 0, 0x1c000
	v_add_u32_e32 v134, s84, v140
	v_add_u32_e32 v135, s85, v140
	s_nop 0
	ds_read_b128 v[6:9], v134
	ds_read_b128 v[26:29], v134 offset:1024
	ds_read_b128 v[30:33], v134 offset:2048
	ds_read_b128 v[202:205], v134 offset:3072
	ds_read_b128 v[206:209], v135
	ds_read_b128 v[210:213], v135 offset:1024
	ds_read_b128 v[214:217], v135 offset:2048
	ds_read_b128 v[218:221], v135 offset:3072
	s_add_u32 s64, s64, 0x4000
	s_addc_u32 s65, s65, 0
	s_mov_b32 m0, s20
	ds_read_b128 v[18:21], v142 offset:32768
	ds_read_b128 v[22:25], v142 offset:33792
	ds_read_b128 v[222:225], v142 offset:34816
	ds_read_b128 v[226:229], v142 offset:35840
	ds_read_b128 v[232:235], v142 offset:36864
	ds_read_b128 v[236:239], v142 offset:37888
	ds_read_b128 v[240:243], v142 offset:38912
	ds_read_b128 v[244:247], v142 offset:39936
	s_nop 0
	global_load_lds_dwordx4 v136, s[64:65]
	s_mov_b32 m0, s21
	s_nop 0
	global_load_lds_dwordx4 v138, s[64:65]
	s_waitcnt vmcnt(8)
	s_waitcnt lgkmcnt(0)
	s_setprio 1
	s_barrier
	s_waitcnt lgkmcnt(0)
	v_mfma_f32_16x16x32_bf16 v[54:57], v[6:9], v[18:21], v[66:69]
	v_mfma_f32_16x16x32_bf16 v[118:121], v[26:29], v[22:25], v[54:57]
	v_mfma_f32_16x16x32_bf16 v[54:57], v[30:33], v[18:21], v[70:73]
	v_mfma_f32_16x16x32_bf16 v[114:117], v[202:205], v[22:25], v[54:57]
	v_mfma_f32_16x16x32_bf16 v[54:57], v[6:9], v[222:225], v[74:77]
	v_mfma_f32_16x16x32_bf16 v[102:105], v[26:29], v[226:229], v[54:57]
	v_mfma_f32_16x16x32_bf16 v[54:57], v[30:33], v[222:225], v[78:81]
	v_mfma_f32_16x16x32_bf16 v[98:101], v[202:205], v[226:229], v[54:57]
	v_mfma_f32_16x16x32_bf16 v[54:57], v[6:9], v[232:235], v[82:85]
	v_mfma_f32_16x16x32_bf16 v[86:89], v[26:29], v[236:239], v[54:57]
	v_mfma_f32_16x16x32_bf16 v[54:57], v[30:33], v[232:235], v[90:93]
	v_mfma_f32_16x16x32_bf16 v[82:85], v[202:205], v[236:239], v[54:57]
	v_mfma_f32_16x16x32_bf16 v[54:57], v[6:9], v[240:243], v[94:97]
	v_mfma_f32_16x16x32_bf16 v[62:65], v[26:29], v[244:247], v[54:57]
	v_mfma_f32_16x16x32_bf16 v[54:57], v[30:33], v[240:243], v[106:109]
	v_mfma_f32_16x16x32_bf16 v[54:57], v[202:205], v[244:247], v[54:57]
	v_mfma_f32_16x16x32_bf16 v[66:69], v[206:209], v[18:21], v[110:113]
	v_mfma_f32_16x16x32_bf16 v[18:21], v[214:217], v[18:21], v[34:37]
	v_mfma_f32_16x16x32_bf16 v[122:125], v[218:221], v[22:25], v[18:21]
	v_mfma_f32_16x16x32_bf16 v[18:21], v[206:209], v[222:225], v[38:41]
	v_mfma_f32_16x16x32_bf16 v[110:113], v[210:213], v[226:229], v[18:21]
	v_mfma_f32_16x16x32_bf16 v[18:21], v[214:217], v[222:225], v[42:45]
	v_mfma_f32_16x16x32_bf16 v[106:109], v[218:221], v[226:229], v[18:21]
	v_mfma_f32_16x16x32_bf16 v[18:21], v[206:209], v[232:235], v[46:49]
	v_mfma_f32_16x16x32_bf16 v[94:97], v[210:213], v[236:239], v[18:21]
	v_mfma_f32_16x16x32_bf16 v[18:21], v[214:217], v[232:235], v[50:53]
	v_mfma_f32_16x16x32_bf16 v[90:93], v[218:221], v[236:239], v[18:21]
	v_mfma_f32_16x16x32_bf16 v[18:21], v[206:209], v[240:243], v[144:147]
	v_mfma_f32_16x16x32_bf16 v[78:81], v[210:213], v[244:247], v[18:21]
	v_mfma_f32_16x16x32_bf16 v[18:21], v[214:217], v[240:243], v[58:61]
	v_mfma_f32_16x16x32_bf16 v[126:129], v[210:213], v[22:25], v[66:69]
	v_mfma_f32_16x16x32_bf16 v[70:73], v[218:221], v[244:247], v[18:21]
	s_barrier
	s_setprio 0
	s_add_i32 s64, s84, s14
	s_add_i32 s65, s64, 0x2000
	s_mov_b32 m0, s64
	s_add_u32 s60, s60, 0xc000
	ds_read_b128 v[42:45], v142 offset:49152
	ds_read_b128 v[46:49], v142 offset:50176
	ds_read_b128 v[144:147], v142 offset:51200
	ds_read_b128 v[222:225], v142 offset:52224
	ds_read_b128 v[226:229], v142 offset:53248
	ds_read_b128 v[232:235], v142 offset:54272
	ds_read_b128 v[236:239], v142 offset:55296
	ds_read_b128 v[240:243], v142 offset:56320
	s_addc_u32 s61, s61, 0
	global_load_lds_dwordx4 v137, s[62:63]
	s_mov_b32 m0, s65
	s_add_i32 s84, s85, s14
	s_add_i32 s85, s84, 0x2000
	global_load_lds_dwordx4 v139, s[62:63]
	s_mov_b32 m0, s84
	s_nop 0
	global_load_lds_dwordx4 v137, s[60:61]
	s_mov_b32 m0, s85
	s_nop 0
	global_load_lds_dwordx4 v139, s[60:61]
	s_mov_b32 m0, s67
	s_nop 0
	global_load_lds_dwordx4 v136, s[58:59]
	s_mov_b32 m0, s68
	s_nop 0
	global_load_lds_dwordx4 v138, s[58:59]
	s_waitcnt vmcnt(8)
	s_waitcnt lgkmcnt(0)
	s_setprio 1
	s_barrier
	s_waitcnt lgkmcnt(0)
	v_mfma_f32_16x16x32_bf16 v[18:21], v[6:9], v[42:45], v[148:151]
	v_mfma_f32_16x16x32_bf16 v[58:61], v[26:29], v[46:49], v[18:21]
	v_mfma_f32_16x16x32_bf16 v[18:21], v[30:33], v[42:45], v[152:155]
	v_mfma_f32_16x16x32_bf16 v[50:53], v[202:205], v[46:49], v[18:21]
	v_mfma_f32_16x16x32_bf16 v[18:21], v[6:9], v[144:147], v[156:159]
	v_mfma_f32_16x16x32_bf16 v[38:41], v[26:29], v[222:225], v[18:21]
	v_mfma_f32_16x16x32_bf16 v[18:21], v[30:33], v[144:147], v[160:163]
	v_mfma_f32_16x16x32_bf16 v[34:37], v[202:205], v[222:225], v[18:21]
	v_mfma_f32_16x16x32_bf16 v[18:21], v[6:9], v[226:229], v[164:167]
	v_mfma_f32_16x16x32_bf16 v[2:5], v[6:9], v[236:239], v[2:5]
	v_mfma_f32_16x16x32_bf16 v[22:25], v[26:29], v[232:235], v[18:21]
	v_mfma_f32_16x16x32_bf16 v[18:21], v[30:33], v[226:229], v[168:171]
	v_mfma_f32_16x16x32_bf16 v[6:9], v[26:29], v[240:243], v[2:5]
	v_mfma_f32_16x16x32_bf16 v[2:5], v[30:33], v[236:239], v[10:13]
	v_mfma_f32_16x16x32_bf16 v[18:21], v[202:205], v[232:235], v[18:21]
	v_mfma_f32_16x16x32_bf16 v[2:5], v[202:205], v[240:243], v[2:5]
	v_mfma_f32_16x16x32_bf16 v[10:13], v[206:209], v[42:45], v[14:17]
	v_mfma_f32_16x16x32_bf16 v[74:77], v[210:213], v[46:49], v[10:13]
	v_mfma_f32_16x16x32_bf16 v[10:13], v[214:217], v[42:45], v[172:175]
	v_mfma_f32_16x16x32_bf16 v[66:69], v[218:221], v[46:49], v[10:13]
	v_mfma_f32_16x16x32_bf16 v[10:13], v[206:209], v[144:147], v[176:179]
	v_mfma_f32_16x16x32_bf16 v[46:49], v[210:213], v[222:225], v[10:13]
	v_mfma_f32_16x16x32_bf16 v[10:13], v[214:217], v[144:147], v[180:183]
	v_mfma_f32_16x16x32_bf16 v[42:45], v[218:221], v[222:225], v[10:13]
	v_mfma_f32_16x16x32_bf16 v[10:13], v[206:209], v[226:229], v[184:187]
	v_mfma_f32_16x16x32_bf16 v[30:33], v[210:213], v[232:235], v[10:13]
	v_mfma_f32_16x16x32_bf16 v[10:13], v[214:217], v[226:229], v[188:191]
	v_mfma_f32_16x16x32_bf16 v[26:29], v[218:221], v[232:235], v[10:13]
	v_mfma_f32_16x16x32_bf16 v[10:13], v[206:209], v[236:239], v[194:197]
	v_mfma_f32_16x16x32_bf16 v[14:17], v[210:213], v[240:243], v[10:13]
	v_mfma_f32_16x16x32_bf16 v[10:13], v[214:217], v[236:239], v[198:201]
	v_mfma_f32_16x16x32_bf16 v[10:13], v[218:221], v[240:243], v[10:13]
	s_barrier
	s_setprio 0
	s_andn2_b64 vcc, exec, s[38:39]
	s_cbranch_vccnz .LBB0_1153
	s_lshl_b32 s58, s72, 10
	s_xor_b32 s86, s58, 0x400
	s_add_u32 s87, s56, 0x20000
	s_addc_u32 s88, s57, 0
	v_ashrrev_i32_e32 v131, 31, v130
	s_add_u32 s54, s54, 0x1c000
	v_lshl_add_u64 v[130:131], v[130:131], 3, s[26:27]
	s_addc_u32 s55, s55, 0
	s_mov_b32 s89, 4

.LBB0_1151:
	s_or_b64 exec, exec, s[58:59]
	ds_read_b128 v[144:147], v132
	ds_read_b128 v[148:151], v132 offset:1024
	ds_read_b128 v[152:155], v132 offset:2048
	ds_read_b128 v[156:159], v132 offset:3072
	ds_read_b128 v[160:163], v133
	ds_read_b128 v[164:167], v133 offset:1024
	ds_read_b128 v[168:171], v133 offset:2048
	ds_read_b128 v[172:175], v133 offset:3072
	s_add_u32 s58, s54, 0x4000
	s_addc_u32 s59, s55, 0
	s_and_b64 s[56:57], s[56:57], exec
	s_cselect_b32 s62, s48, s58
	s_cselect_b32 s63, s49, s59
	s_cselect_b32 s59, s51, s88
	s_cselect_b32 s58, s50, s87
	s_add_u32 s56, s62, 0x8000
	s_addc_u32 s57, s63, 0
	s_add_u32 s60, s58, 0x8000
	s_addc_u32 s61, s59, 0
	s_mov_b32 m0, s78
	ds_read_b128 v[176:179], v142
	ds_read_b128 v[180:183], v142 offset:1024
	ds_read_b128 v[184:187], v142 offset:2048
	ds_read_b128 v[188:191], v142 offset:3072
	ds_read_b128 v[194:197], v142 offset:4096
	ds_read_b128 v[198:201], v142 offset:5120
	ds_read_b128 v[202:205], v142 offset:6144
	ds_read_b128 v[206:209], v142 offset:7168
	s_nop 0
	global_load_lds_dwordx4 v136, s[54:55]
	s_mov_b32 m0, s79
	s_nop 0
	global_load_lds_dwordx4 v138, s[54:55]
	s_waitcnt vmcnt(8)
	s_waitcnt lgkmcnt(0)
	s_setprio 1
	s_barrier
	s_waitcnt lgkmcnt(0)
	v_mfma_f32_16x16x32_bf16 v[118:121], v[144:147], v[176:179], v[118:121]
	v_mfma_f32_16x16x32_bf16 v[114:117], v[152:155], v[176:179], v[114:117]
	v_mfma_f32_16x16x32_bf16 v[102:105], v[144:147], v[184:187], v[102:105]
	v_mfma_f32_16x16x32_bf16 v[98:101], v[152:155], v[184:187], v[98:101]
	v_mfma_f32_16x16x32_bf16 v[86:89], v[144:147], v[194:197], v[86:89]
	v_mfma_f32_16x16x32_bf16 v[82:85], v[152:155], v[194:197], v[82:85]
	v_mfma_f32_16x16x32_bf16 v[62:65], v[144:147], v[202:205], v[62:65]
	v_mfma_f32_16x16x32_bf16 v[54:57], v[152:155], v[202:205], v[54:57]
	v_mfma_f32_16x16x32_bf16 v[118:121], v[148:151], v[180:183], v[118:121]
	v_mfma_f32_16x16x32_bf16 v[114:117], v[156:159], v[180:183], v[114:117]
	v_mfma_f32_16x16x32_bf16 v[102:105], v[148:151], v[188:191], v[102:105]
	v_mfma_f32_16x16x32_bf16 v[98:101], v[156:159], v[188:191], v[98:101]
	v_mfma_f32_16x16x32_bf16 v[86:89], v[148:151], v[198:201], v[86:89]
	v_mfma_f32_16x16x32_bf16 v[82:85], v[156:159], v[198:201], v[82:85]
	v_mfma_f32_16x16x32_bf16 v[62:65], v[148:151], v[206:209], v[62:65]
	v_mfma_f32_16x16x32_bf16 v[54:57], v[156:159], v[206:209], v[54:57]
	v_mfma_f32_16x16x32_bf16 v[126:129], v[160:163], v[176:179], v[126:129]
	v_mfma_f32_16x16x32_bf16 v[122:125], v[168:171], v[176:179], v[122:125]
	v_mfma_f32_16x16x32_bf16 v[110:113], v[160:163], v[184:187], v[110:113]
	v_mfma_f32_16x16x32_bf16 v[106:109], v[168:171], v[184:187], v[106:109]
	v_mfma_f32_16x16x32_bf16 v[94:97], v[160:163], v[194:197], v[94:97]
	v_mfma_f32_16x16x32_bf16 v[90:93], v[168:171], v[194:197], v[90:93]
	v_mfma_f32_16x16x32_bf16 v[78:81], v[160:163], v[202:205], v[78:81]
	v_mfma_f32_16x16x32_bf16 v[70:73], v[168:171], v[202:205], v[70:73]
	v_mfma_f32_16x16x32_bf16 v[126:129], v[164:167], v[180:183], v[126:129]
	v_mfma_f32_16x16x32_bf16 v[122:125], v[172:175], v[180:183], v[122:125]
	v_mfma_f32_16x16x32_bf16 v[110:113], v[164:167], v[188:191], v[110:113]
	v_mfma_f32_16x16x32_bf16 v[106:109], v[172:175], v[188:191], v[106:109]
	v_mfma_f32_16x16x32_bf16 v[94:97], v[164:167], v[198:201], v[94:97]
	v_mfma_f32_16x16x32_bf16 v[90:93], v[172:175], v[198:201], v[90:93]
	v_mfma_f32_16x16x32_bf16 v[78:81], v[164:167], v[206:209], v[78:81]
	v_mfma_f32_16x16x32_bf16 v[70:73], v[172:175], v[206:209], v[70:73]
	s_barrier
	s_setprio 0
	s_mov_b32 m0, s80
	ds_read_b128 v[176:179], v142 offset:16384
	ds_read_b128 v[180:183], v142 offset:17408
	ds_read_b128 v[184:187], v142 offset:18432
	ds_read_b128 v[188:191], v142 offset:19456
	ds_read_b128 v[194:197], v142 offset:20480
	ds_read_b128 v[198:201], v142 offset:21504
	ds_read_b128 v[202:205], v142 offset:22528
	ds_read_b128 v[206:209], v142 offset:23552
	s_add_u32 s90, s58, 0x4000
	global_load_lds_dwordx4 v137, s[58:59]
	s_mov_b32 m0, s81
	s_addc_u32 s91, s59, 0
	global_load_lds_dwordx4 v139, s[58:59]
	s_mov_b32 m0, s82
	s_nop 0
	global_load_lds_dwordx4 v137, s[90:91]
	s_mov_b32 m0, s83
	s_nop 0
	global_load_lds_dwordx4 v139, s[90:91]
	s_mov_b32 m0, s15
	s_nop 0
	global_load_lds_dwordx4 v136, s[62:63]
	s_mov_b32 m0, s18
	s_nop 0
	global_load_lds_dwordx4 v138, s[62:63]
	s_waitcnt vmcnt(8)
	s_waitcnt lgkmcnt(0)
	s_setprio 1
	s_barrier
	s_waitcnt lgkmcnt(0)
	v_mfma_f32_16x16x32_bf16 v[58:61], v[144:147], v[176:179], v[58:61]
	v_mfma_f32_16x16x32_bf16 v[50:53], v[152:155], v[176:179], v[50:53]
	v_mfma_f32_16x16x32_bf16 v[38:41], v[144:147], v[184:187], v[38:41]
	v_mfma_f32_16x16x32_bf16 v[34:37], v[152:155], v[184:187], v[34:37]
	v_mfma_f32_16x16x32_bf16 v[22:25], v[144:147], v[194:197], v[22:25]
	v_mfma_f32_16x16x32_bf16 v[18:21], v[152:155], v[194:197], v[18:21]
	v_mfma_f32_16x16x32_bf16 v[6:9], v[144:147], v[202:205], v[6:9]
	v_mfma_f32_16x16x32_bf16 v[2:5], v[152:155], v[202:205], v[2:5]
	v_mfma_f32_16x16x32_bf16 v[58:61], v[148:151], v[180:183], v[58:61]
	v_mfma_f32_16x16x32_bf16 v[50:53], v[156:159], v[180:183], v[50:53]
	v_mfma_f32_16x16x32_bf16 v[38:41], v[148:151], v[188:191], v[38:41]
	v_mfma_f32_16x16x32_bf16 v[34:37], v[156:159], v[188:191], v[34:37]
	v_mfma_f32_16x16x32_bf16 v[22:25], v[148:151], v[198:201], v[22:25]
	v_mfma_f32_16x16x32_bf16 v[18:21], v[156:159], v[198:201], v[18:21]
	v_mfma_f32_16x16x32_bf16 v[6:9], v[148:151], v[206:209], v[6:9]
	v_mfma_f32_16x16x32_bf16 v[2:5], v[156:159], v[206:209], v[2:5]
	v_mfma_f32_16x16x32_bf16 v[74:77], v[160:163], v[176:179], v[74:77]
	v_mfma_f32_16x16x32_bf16 v[66:69], v[168:171], v[176:179], v[66:69]
	v_mfma_f32_16x16x32_bf16 v[46:49], v[160:163], v[184:187], v[46:49]
	v_mfma_f32_16x16x32_bf16 v[42:45], v[168:171], v[184:187], v[42:45]
	v_mfma_f32_16x16x32_bf16 v[30:33], v[160:163], v[194:197], v[30:33]
	v_mfma_f32_16x16x32_bf16 v[26:29], v[168:171], v[194:197], v[26:29]
	v_mfma_f32_16x16x32_bf16 v[14:17], v[160:163], v[202:205], v[14:17]
	v_mfma_f32_16x16x32_bf16 v[10:13], v[168:171], v[202:205], v[10:13]
	v_mfma_f32_16x16x32_bf16 v[74:77], v[164:167], v[180:183], v[74:77]
	v_mfma_f32_16x16x32_bf16 v[66:69], v[172:175], v[180:183], v[66:69]
	v_mfma_f32_16x16x32_bf16 v[46:49], v[164:167], v[188:191], v[46:49]
	v_mfma_f32_16x16x32_bf16 v[42:45], v[172:175], v[188:191], v[42:45]
	v_mfma_f32_16x16x32_bf16 v[30:33], v[164:167], v[198:201], v[30:33]
	v_mfma_f32_16x16x32_bf16 v[26:29], v[172:175], v[198:201], v[26:29]
	v_mfma_f32_16x16x32_bf16 v[14:17], v[164:167], v[206:209], v[14:17]
	v_mfma_f32_16x16x32_bf16 v[10:13], v[172:175], v[206:209], v[10:13]
	s_barrier
	s_setprio 0
	ds_read_b128 v[144:147], v134
	ds_read_b128 v[148:151], v134 offset:1024
	ds_read_b128 v[152:155], v134 offset:2048
	ds_read_b128 v[156:159], v134 offset:3072
	ds_read_b128 v[160:163], v135
	ds_read_b128 v[164:167], v135 offset:1024
	ds_read_b128 v[168:171], v135 offset:2048
	ds_read_b128 v[172:175], v135 offset:3072
	s_add_u32 s62, s62, 0x4000
	s_addc_u32 s63, s63, 0
	s_mov_b32 m0, s20
	ds_read_b128 v[176:179], v142 offset:32768
	ds_read_b128 v[180:183], v142 offset:33792
	ds_read_b128 v[184:187], v142 offset:34816
	ds_read_b128 v[188:191], v142 offset:35840
	ds_read_b128 v[194:197], v142 offset:36864
	ds_read_b128 v[198:201], v142 offset:37888
	ds_read_b128 v[202:205], v142 offset:38912
	ds_read_b128 v[206:209], v142 offset:39936
	s_nop 0
	global_load_lds_dwordx4 v136, s[62:63]
	s_mov_b32 m0, s21
	s_nop 0
	global_load_lds_dwordx4 v138, s[62:63]
	s_waitcnt vmcnt(8)
	s_waitcnt lgkmcnt(0)
	s_setprio 1
	s_barrier
	s_waitcnt lgkmcnt(0)
	v_mfma_f32_16x16x32_bf16 v[118:121], v[144:147], v[176:179], v[118:121]
	v_mfma_f32_16x16x32_bf16 v[114:117], v[152:155], v[176:179], v[114:117]
	v_mfma_f32_16x16x32_bf16 v[102:105], v[144:147], v[184:187], v[102:105]
	v_mfma_f32_16x16x32_bf16 v[98:101], v[152:155], v[184:187], v[98:101]
	v_mfma_f32_16x16x32_bf16 v[86:89], v[144:147], v[194:197], v[86:89]
	v_mfma_f32_16x16x32_bf16 v[82:85], v[152:155], v[194:197], v[82:85]
	v_mfma_f32_16x16x32_bf16 v[62:65], v[144:147], v[202:205], v[62:65]
	v_mfma_f32_16x16x32_bf16 v[54:57], v[152:155], v[202:205], v[54:57]
	v_mfma_f32_16x16x32_bf16 v[118:121], v[148:151], v[180:183], v[118:121]
	v_mfma_f32_16x16x32_bf16 v[114:117], v[156:159], v[180:183], v[114:117]
	v_mfma_f32_16x16x32_bf16 v[102:105], v[148:151], v[188:191], v[102:105]
	v_mfma_f32_16x16x32_bf16 v[98:101], v[156:159], v[188:191], v[98:101]
	v_mfma_f32_16x16x32_bf16 v[86:89], v[148:151], v[198:201], v[86:89]
	v_mfma_f32_16x16x32_bf16 v[82:85], v[156:159], v[198:201], v[82:85]
	v_mfma_f32_16x16x32_bf16 v[62:65], v[148:151], v[206:209], v[62:65]
	v_mfma_f32_16x16x32_bf16 v[54:57], v[156:159], v[206:209], v[54:57]
	v_mfma_f32_16x16x32_bf16 v[126:129], v[160:163], v[176:179], v[126:129]
	v_mfma_f32_16x16x32_bf16 v[122:125], v[168:171], v[176:179], v[122:125]
	v_mfma_f32_16x16x32_bf16 v[110:113], v[160:163], v[184:187], v[110:113]
	v_mfma_f32_16x16x32_bf16 v[106:109], v[168:171], v[184:187], v[106:109]
	v_mfma_f32_16x16x32_bf16 v[94:97], v[160:163], v[194:197], v[94:97]
	v_mfma_f32_16x16x32_bf16 v[90:93], v[168:171], v[194:197], v[90:93]
	v_mfma_f32_16x16x32_bf16 v[78:81], v[160:163], v[202:205], v[78:81]
	v_mfma_f32_16x16x32_bf16 v[70:73], v[168:171], v[202:205], v[70:73]
	v_mfma_f32_16x16x32_bf16 v[126:129], v[164:167], v[180:183], v[126:129]
	v_mfma_f32_16x16x32_bf16 v[122:125], v[172:175], v[180:183], v[122:125]
	v_mfma_f32_16x16x32_bf16 v[110:113], v[164:167], v[188:191], v[110:113]
	v_mfma_f32_16x16x32_bf16 v[106:109], v[172:175], v[188:191], v[106:109]
	v_mfma_f32_16x16x32_bf16 v[94:97], v[164:167], v[198:201], v[94:97]
	v_mfma_f32_16x16x32_bf16 v[90:93], v[172:175], v[198:201], v[90:93]
	v_mfma_f32_16x16x32_bf16 v[78:81], v[164:167], v[206:209], v[78:81]
	v_mfma_f32_16x16x32_bf16 v[70:73], v[172:175], v[206:209], v[70:73]
	s_barrier
	s_setprio 0
	s_mov_b32 m0, s64
	ds_read_b128 v[176:179], v142 offset:49152
	ds_read_b128 v[180:183], v142 offset:50176
	ds_read_b128 v[184:187], v142 offset:51200
	ds_read_b128 v[188:191], v142 offset:52224
	ds_read_b128 v[194:197], v142 offset:53248
	ds_read_b128 v[198:201], v142 offset:54272
	ds_read_b128 v[202:205], v142 offset:55296
	ds_read_b128 v[206:209], v142 offset:56320
	s_add_u32 s58, s58, 0xc000
	global_load_lds_dwordx4 v137, s[60:61]
	s_mov_b32 m0, s65
	s_addc_u32 s59, s59, 0
	global_load_lds_dwordx4 v139, s[60:61]
	s_mov_b32 m0, s84
	s_nop 0
	global_load_lds_dwordx4 v137, s[58:59]
	s_mov_b32 m0, s85
	s_nop 0
	global_load_lds_dwordx4 v139, s[58:59]
	s_mov_b32 m0, s67
	s_nop 0
	global_load_lds_dwordx4 v136, s[56:57]
	s_mov_b32 m0, s68
	s_nop 0
	global_load_lds_dwordx4 v138, s[56:57]
	s_waitcnt vmcnt(8)
	s_waitcnt lgkmcnt(0)
	s_setprio 1
	s_barrier
	s_waitcnt lgkmcnt(0)
	v_mfma_f32_16x16x32_bf16 v[58:61], v[144:147], v[176:179], v[58:61]
	v_mfma_f32_16x16x32_bf16 v[50:53], v[152:155], v[176:179], v[50:53]
	v_mfma_f32_16x16x32_bf16 v[38:41], v[144:147], v[184:187], v[38:41]
	v_mfma_f32_16x16x32_bf16 v[34:37], v[152:155], v[184:187], v[34:37]
	v_mfma_f32_16x16x32_bf16 v[22:25], v[144:147], v[194:197], v[22:25]
	v_mfma_f32_16x16x32_bf16 v[18:21], v[152:155], v[194:197], v[18:21]
	v_mfma_f32_16x16x32_bf16 v[6:9], v[144:147], v[202:205], v[6:9]
	v_mfma_f32_16x16x32_bf16 v[2:5], v[152:155], v[202:205], v[2:5]
	v_mfma_f32_16x16x32_bf16 v[58:61], v[148:151], v[180:183], v[58:61]
	v_mfma_f32_16x16x32_bf16 v[50:53], v[156:159], v[180:183], v[50:53]
	v_mfma_f32_16x16x32_bf16 v[38:41], v[148:151], v[188:191], v[38:41]
	v_mfma_f32_16x16x32_bf16 v[34:37], v[156:159], v[188:191], v[34:37]
	v_mfma_f32_16x16x32_bf16 v[22:25], v[148:151], v[198:201], v[22:25]
	v_mfma_f32_16x16x32_bf16 v[18:21], v[156:159], v[198:201], v[18:21]
	v_mfma_f32_16x16x32_bf16 v[6:9], v[148:151], v[206:209], v[6:9]
	v_mfma_f32_16x16x32_bf16 v[2:5], v[156:159], v[206:209], v[2:5]
	v_mfma_f32_16x16x32_bf16 v[74:77], v[160:163], v[176:179], v[74:77]
	v_mfma_f32_16x16x32_bf16 v[66:69], v[168:171], v[176:179], v[66:69]
	v_mfma_f32_16x16x32_bf16 v[46:49], v[160:163], v[184:187], v[46:49]
	v_mfma_f32_16x16x32_bf16 v[42:45], v[168:171], v[184:187], v[42:45]
	v_mfma_f32_16x16x32_bf16 v[30:33], v[160:163], v[194:197], v[30:33]
	v_mfma_f32_16x16x32_bf16 v[26:29], v[168:171], v[194:197], v[26:29]
	v_mfma_f32_16x16x32_bf16 v[14:17], v[160:163], v[202:205], v[14:17]
	v_mfma_f32_16x16x32_bf16 v[10:13], v[168:171], v[202:205], v[10:13]
	v_mfma_f32_16x16x32_bf16 v[74:77], v[164:167], v[180:183], v[74:77]
	v_mfma_f32_16x16x32_bf16 v[66:69], v[172:175], v[180:183], v[66:69]
	v_mfma_f32_16x16x32_bf16 v[46:49], v[164:167], v[188:191], v[46:49]
	v_mfma_f32_16x16x32_bf16 v[42:45], v[172:175], v[188:191], v[42:45]
	v_mfma_f32_16x16x32_bf16 v[30:33], v[164:167], v[198:201], v[30:33]
	v_mfma_f32_16x16x32_bf16 v[26:29], v[172:175], v[198:201], v[26:29]
	v_mfma_f32_16x16x32_bf16 v[14:17], v[164:167], v[206:209], v[14:17]
	v_mfma_f32_16x16x32_bf16 v[10:13], v[172:175], v[206:209], v[10:13]
	s_barrier
	s_setprio 0
	s_add_i32 s56, s89, 2
	s_add_u32 s87, s87, 0x10000
	s_addc_u32 s88, s88, 0
	s_add_u32 s54, s54, 0x10000
	s_addc_u32 s55, s55, 0
	s_cmp_lt_i32 s89, s25
	s_cbranch_scc0 .LBB0_1153
	s_mov_b32 s89, s56
	s_branch .LBB0_1149

.LBB0_1225:
	s_add_u32 s34, s26, 0x10000
	s_addc_u32 s35, s27, 0
	s_and_b64 s[30:31], s[46:47], exec
	s_cselect_b32 s53, s39, s35
	s_cselect_b32 s52, s38, s34
	s_add_u32 s65, s28, 0x10000
	s_addc_u32 s66, s29, 0
	s_add_u32 s30, s52, 0x8000
	s_addc_u32 s31, s53, 0
	s_add_i32 s67, 0, 0x10000
	s_and_b64 s[34:35], s[46:47], exec
	s_cselect_b32 s35, s41, s66
	s_cselect_b32 s34, s40, s65
	s_add_i32 s70, 0, 0x14000
	v_add_u32_e32 v114, s67, v236
	v_add_u32_e32 v115, s70, v236
	ds_read_b128 v[2:5], v114
	s_waitcnt lgkmcnt(0)
	ds_read_b128 v[6:9], v114 offset:1024
	ds_read_b128 v[10:13], v114 offset:2048
	ds_read_b128 v[14:17], v114 offset:3072
	ds_read_b128 v[18:21], v115
	ds_read_b128 v[22:25], v115 offset:1024
	ds_read_b128 v[26:29], v115 offset:2048
	ds_read_b128 v[30:33], v115 offset:3072
	s_add_u32 s68, s26, 0xc000
	s_addc_u32 s69, s27, 0
	s_add_i32 s65, s20, 0xc000
	s_mov_b32 m0, s65
	s_add_i32 s66, s20, 0xe000
	ds_read_b128 v[34:37], v237
	ds_read_b128 v[38:41], v237 offset:1024
	ds_read_b128 v[42:45], v237 offset:2048
	ds_read_b128 v[46:49], v237 offset:3072
	ds_read_b128 v[50:53], v237 offset:4096
	ds_read_b128 v[54:57], v237 offset:5120
	ds_read_b128 v[58:61], v237 offset:6144
	ds_read_b128 v[62:65], v237 offset:7168
	s_nop 0
	global_load_lds_dwordx4 v235, s[68:69]
	s_mov_b32 m0, s66
	s_nop 0
	global_load_lds_dwordx4 v226, s[68:69]
	s_waitcnt vmcnt(8)
	s_waitcnt lgkmcnt(0)
	s_setprio 1
	s_barrier
	s_waitcnt lgkmcnt(0)
	v_mfma_f32_16x16x32_bf16 v[90:93], v[2:5], v[58:61], 0
	v_mfma_f32_16x16x32_bf16 v[66:69], v[2:5], v[34:37], 0
	v_mfma_f32_16x16x32_bf16 v[70:73], v[10:13], v[34:37], 0
	v_mfma_f32_16x16x32_bf16 v[74:77], v[2:5], v[42:45], 0
	v_mfma_f32_16x16x32_bf16 v[78:81], v[10:13], v[42:45], 0
	v_mfma_f32_16x16x32_bf16 v[82:85], v[2:5], v[50:53], 0
	v_mfma_f32_16x16x32_bf16 v[86:89], v[10:13], v[50:53], 0
	v_mfma_f32_16x16x32_bf16 v[98:101], v[6:9], v[62:65], v[90:93]
	v_mfma_f32_16x16x32_bf16 v[90:93], v[10:13], v[58:61], 0
	v_mfma_f32_16x16x32_bf16 v[66:69], v[6:9], v[38:41], v[66:69]
	v_mfma_f32_16x16x32_bf16 v[70:73], v[14:17], v[38:41], v[70:73]
	v_mfma_f32_16x16x32_bf16 v[74:77], v[6:9], v[46:49], v[74:77]
	v_mfma_f32_16x16x32_bf16 v[78:81], v[14:17], v[46:49], v[78:81]
	v_mfma_f32_16x16x32_bf16 v[82:85], v[6:9], v[54:57], v[82:85]
	v_mfma_f32_16x16x32_bf16 v[86:89], v[14:17], v[54:57], v[86:89]
	v_mfma_f32_16x16x32_bf16 v[102:105], v[14:17], v[62:65], v[90:93]
	v_mfma_f32_16x16x32_bf16 v[90:93], v[18:21], v[34:37], 0
	v_mfma_f32_16x16x32_bf16 v[34:37], v[26:29], v[34:37], 0
	v_mfma_f32_16x16x32_bf16 v[118:121], v[22:25], v[38:41], v[90:93]
	v_mfma_f32_16x16x32_bf16 v[34:37], v[30:33], v[38:41], v[34:37]
	v_mfma_f32_16x16x32_bf16 v[38:41], v[18:21], v[42:45], 0
	v_mfma_f32_16x16x32_bf16 v[42:45], v[26:29], v[42:45], 0
	v_mfma_f32_16x16x32_bf16 v[38:41], v[22:25], v[46:49], v[38:41]
	v_mfma_f32_16x16x32_bf16 v[42:45], v[30:33], v[46:49], v[42:45]
	v_mfma_f32_16x16x32_bf16 v[46:49], v[18:21], v[50:53], 0
	v_mfma_f32_16x16x32_bf16 v[50:53], v[26:29], v[50:53], 0
	v_mfma_f32_16x16x32_bf16 v[46:49], v[22:25], v[54:57], v[46:49]
	v_mfma_f32_16x16x32_bf16 v[50:53], v[30:33], v[54:57], v[50:53]
	v_mfma_f32_16x16x32_bf16 v[54:57], v[18:21], v[58:61], 0
	v_mfma_f32_16x16x32_bf16 v[58:61], v[26:29], v[58:61], 0
	v_mfma_f32_16x16x32_bf16 v[54:57], v[22:25], v[62:65], v[54:57]
	v_mfma_f32_16x16x32_bf16 v[58:61], v[30:33], v[62:65], v[58:61]
	s_barrier
	s_setprio 0
	s_add_i32 s67, s67, s18
	s_add_i32 s68, s67, 0x2000
	s_mov_b32 m0, s67
	s_add_u32 s72, s34, 0x4000
	ds_read_b128 v[62:65], v237 offset:16384
	ds_read_b128 v[90:93], v237 offset:17408
	ds_read_b128 v[94:97], v237 offset:18432
	ds_read_b128 v[106:109], v237 offset:19456
	ds_read_b128 v[110:113], v237 offset:20480
	ds_read_b128 v[122:125], v237 offset:21504
	ds_read_b128 v[126:129], v237 offset:22528
	ds_read_b128 v[130:133], v237 offset:23552
	s_addc_u32 s73, s35, 0
	global_load_lds_dwordx4 v227, s[34:35]
	s_mov_b32 m0, s68
	s_add_i32 s69, s70, s18
	s_add_i32 s70, s69, 0x2000
	global_load_lds_dwordx4 v0, s[34:35]
	s_mov_b32 m0, s69
	s_nop 0
	global_load_lds_dwordx4 v227, s[72:73]
	s_mov_b32 m0, s70
	s_nop 0
	global_load_lds_dwordx4 v0, s[72:73]
	s_mov_b32 m0, s20
	s_nop 0
	global_load_lds_dwordx4 v235, s[52:53]
	s_mov_b32 m0, s25
	s_nop 0
	global_load_lds_dwordx4 v226, s[52:53]
	s_waitcnt vmcnt(8)
	s_waitcnt lgkmcnt(0)
	s_setprio 1
	s_barrier
	s_waitcnt lgkmcnt(0)
	v_mfma_f32_16x16x32_bf16 v[134:137], v[2:5], v[62:65], 0
	v_mfma_f32_16x16x32_bf16 v[142:145], v[2:5], v[94:97], 0
	v_mfma_f32_16x16x32_bf16 v[150:153], v[2:5], v[110:113], 0
	v_mfma_f32_16x16x32_bf16 v[2:5], v[2:5], v[126:129], 0
	v_mfma_f32_16x16x32_bf16 v[134:137], v[6:9], v[90:93], v[134:137]
	v_mfma_f32_16x16x32_bf16 v[142:145], v[6:9], v[106:109], v[142:145]
	v_mfma_f32_16x16x32_bf16 v[150:153], v[6:9], v[122:125], v[150:153]
	v_mfma_f32_16x16x32_bf16 v[2:5], v[6:9], v[130:133], v[2:5]
	v_mfma_f32_16x16x32_bf16 v[6:9], v[10:13], v[126:129], 0
	v_mfma_f32_16x16x32_bf16 v[138:141], v[10:13], v[62:65], 0
	v_mfma_f32_16x16x32_bf16 v[146:149], v[10:13], v[94:97], 0
	v_mfma_f32_16x16x32_bf16 v[154:157], v[10:13], v[110:113], 0
	v_mfma_f32_16x16x32_bf16 v[6:9], v[14:17], v[130:133], v[6:9]
	v_mfma_f32_16x16x32_bf16 v[138:141], v[14:17], v[90:93], v[138:141]
	v_mfma_f32_16x16x32_bf16 v[146:149], v[14:17], v[106:109], v[146:149]
	v_mfma_f32_16x16x32_bf16 v[154:157], v[14:17], v[122:125], v[154:157]
	v_mfma_f32_16x16x32_bf16 v[10:13], v[18:21], v[62:65], 0
	v_mfma_f32_16x16x32_bf16 v[158:161], v[22:25], v[90:93], v[10:13]
	v_mfma_f32_16x16x32_bf16 v[10:13], v[26:29], v[62:65], 0
	v_mfma_f32_16x16x32_bf16 v[162:165], v[30:33], v[90:93], v[10:13]
	v_mfma_f32_16x16x32_bf16 v[10:13], v[18:21], v[94:97], 0
	v_mfma_f32_16x16x32_bf16 v[174:177], v[22:25], v[106:109], v[10:13]
	v_mfma_f32_16x16x32_bf16 v[10:13], v[26:29], v[94:97], 0
	v_mfma_f32_16x16x32_bf16 v[178:181], v[30:33], v[106:109], v[10:13]
	v_mfma_f32_16x16x32_bf16 v[10:13], v[18:21], v[110:113], 0
	v_mfma_f32_16x16x32_bf16 v[182:185], v[22:25], v[122:125], v[10:13]
	v_mfma_f32_16x16x32_bf16 v[10:13], v[26:29], v[110:113], 0
	v_mfma_f32_16x16x32_bf16 v[122:125], v[30:33], v[122:125], v[10:13]
	v_mfma_f32_16x16x32_bf16 v[10:13], v[18:21], v[126:129], 0
	v_mfma_f32_16x16x32_bf16 v[186:189], v[22:25], v[130:133], v[10:13]
	v_mfma_f32_16x16x32_bf16 v[10:13], v[26:29], v[126:129], 0
	v_mfma_f32_16x16x32_bf16 v[130:133], v[30:33], v[130:133], v[10:13]
	s_barrier
	s_setprio 0
	s_add_i32 s71, 0, 0x18000
	s_add_i32 s74, 0, 0x1c000
	v_add_u32_e32 v116, s71, v236
	v_add_u32_e32 v117, s74, v236
	s_nop 0
	ds_read_b128 v[10:13], v116
	ds_read_b128 v[14:17], v116 offset:1024
	ds_read_b128 v[18:21], v116 offset:2048
	ds_read_b128 v[22:25], v116 offset:3072
	ds_read_b128 v[194:197], v117
	ds_read_b128 v[198:201], v117 offset:1024
	ds_read_b128 v[202:205], v117 offset:2048
	ds_read_b128 v[206:209], v117 offset:3072
	s_add_u32 s52, s52, 0x4000
	s_addc_u32 s53, s53, 0
	s_mov_b32 m0, s54
	ds_read_b128 v[26:29], v237 offset:32768
	ds_read_b128 v[30:33], v237 offset:33792
	ds_read_b128 v[62:65], v237 offset:34816
	ds_read_b128 v[210:213], v237 offset:35840
	ds_read_b128 v[214:217], v237 offset:36864
	ds_read_b128 v[218:221], v237 offset:37888
	ds_read_b128 v[222:225], v237 offset:38912
	ds_read_b128 v[238:241], v237 offset:39936
	s_nop 0
	global_load_lds_dwordx4 v235, s[52:53]
	s_mov_b32 m0, s55
	s_nop 0
	global_load_lds_dwordx4 v226, s[52:53]
	s_waitcnt vmcnt(8)
	s_waitcnt lgkmcnt(0)
	s_setprio 1
	s_barrier
	s_waitcnt lgkmcnt(0)
	v_mfma_f32_16x16x32_bf16 v[66:69], v[10:13], v[26:29], v[66:69]
	v_mfma_f32_16x16x32_bf16 v[166:169], v[14:17], v[30:33], v[66:69]
	v_mfma_f32_16x16x32_bf16 v[66:69], v[18:21], v[26:29], v[70:73]
	v_mfma_f32_16x16x32_bf16 v[170:173], v[22:25], v[30:33], v[66:69]
	v_mfma_f32_16x16x32_bf16 v[66:69], v[10:13], v[62:65], v[74:77]
	v_mfma_f32_16x16x32_bf16 v[110:113], v[14:17], v[210:213], v[66:69]
	v_mfma_f32_16x16x32_bf16 v[66:69], v[18:21], v[62:65], v[78:81]
	v_mfma_f32_16x16x32_bf16 v[106:109], v[22:25], v[210:213], v[66:69]
	v_mfma_f32_16x16x32_bf16 v[66:69], v[10:13], v[214:217], v[82:85]
	v_mfma_f32_16x16x32_bf16 v[94:97], v[14:17], v[218:221], v[66:69]
	v_mfma_f32_16x16x32_bf16 v[66:69], v[18:21], v[214:217], v[86:89]
	v_mfma_f32_16x16x32_bf16 v[90:93], v[22:25], v[218:221], v[66:69]
	v_mfma_f32_16x16x32_bf16 v[66:69], v[10:13], v[222:225], v[98:101]
	v_mfma_f32_16x16x32_bf16 v[78:81], v[14:17], v[238:241], v[66:69]
	v_mfma_f32_16x16x32_bf16 v[66:69], v[18:21], v[222:225], v[102:105]
	v_mfma_f32_16x16x32_bf16 v[70:73], v[22:25], v[238:241], v[66:69]
	v_mfma_f32_16x16x32_bf16 v[66:69], v[194:197], v[26:29], v[118:121]
	v_mfma_f32_16x16x32_bf16 v[26:29], v[202:205], v[26:29], v[34:37]
	v_mfma_f32_16x16x32_bf16 v[118:121], v[206:209], v[30:33], v[26:29]
	v_mfma_f32_16x16x32_bf16 v[26:29], v[194:197], v[62:65], v[38:41]
	v_mfma_f32_16x16x32_bf16 v[102:105], v[198:201], v[210:213], v[26:29]
	v_mfma_f32_16x16x32_bf16 v[26:29], v[202:205], v[62:65], v[42:45]
	v_mfma_f32_16x16x32_bf16 v[98:101], v[206:209], v[210:213], v[26:29]
	v_mfma_f32_16x16x32_bf16 v[26:29], v[194:197], v[214:217], v[46:49]
	v_mfma_f32_16x16x32_bf16 v[86:89], v[198:201], v[218:221], v[26:29]
	v_mfma_f32_16x16x32_bf16 v[26:29], v[202:205], v[214:217], v[50:53]
	v_mfma_f32_16x16x32_bf16 v[82:85], v[206:209], v[218:221], v[26:29]
	v_mfma_f32_16x16x32_bf16 v[26:29], v[194:197], v[222:225], v[54:57]
	v_mfma_f32_16x16x32_bf16 v[62:65], v[198:201], v[238:241], v[26:29]
	v_mfma_f32_16x16x32_bf16 v[26:29], v[202:205], v[222:225], v[58:61]
	v_mfma_f32_16x16x32_bf16 v[126:129], v[198:201], v[30:33], v[66:69]
	v_mfma_f32_16x16x32_bf16 v[54:57], v[206:209], v[238:241], v[26:29]
	s_barrier
	s_setprio 0
	s_add_u32 s72, s34, 0x8000
	s_addc_u32 s73, s35, 0
	s_add_i32 s52, s71, s18
	s_add_i32 s53, s52, 0x2000
	s_mov_b32 m0, s52
	s_add_u32 s34, s34, 0xc000
	ds_read_b128 v[34:37], v237 offset:49152
	ds_read_b128 v[38:41], v237 offset:50176
	ds_read_b128 v[210:213], v237 offset:51200
	ds_read_b128 v[214:217], v237 offset:52224
	ds_read_b128 v[218:221], v237 offset:53248
	ds_read_b128 v[222:225], v237 offset:54272
	ds_read_b128 v[238:241], v237 offset:55296
	ds_read_b128 v[242:245], v237 offset:56320
	s_addc_u32 s35, s35, 0
	global_load_lds_dwordx4 v227, s[72:73]
	s_mov_b32 m0, s53
	s_add_i32 s71, s74, s18
	s_nop 0
	global_load_lds_dwordx4 v0, s[72:73]
	s_mov_b32 m0, s71
	s_add_i32 s72, s71, 0x2000
	s_nop 0
	global_load_lds_dwordx4 v227, s[34:35]
	s_mov_b32 m0, s72
	s_nop 0
	global_load_lds_dwordx4 v0, s[34:35]
	s_mov_b32 m0, s58
	s_nop 0
	global_load_lds_dwordx4 v235, s[30:31]
	s_mov_b32 m0, s59
	s_nop 0
	global_load_lds_dwordx4 v226, s[30:31]
	s_waitcnt vmcnt(8)
	s_waitcnt lgkmcnt(0)
	s_setprio 1
	s_barrier
	s_waitcnt lgkmcnt(0)
	v_mfma_f32_16x16x32_bf16 v[26:29], v[10:13], v[34:37], v[134:137]
	v_mfma_f32_16x16x32_bf16 v[74:77], v[14:17], v[38:41], v[26:29]
	v_mfma_f32_16x16x32_bf16 v[26:29], v[18:21], v[34:37], v[138:141]
	v_mfma_f32_16x16x32_bf16 v[66:69], v[22:25], v[38:41], v[26:29]
	v_mfma_f32_16x16x32_bf16 v[26:29], v[10:13], v[210:213], v[142:145]
	v_mfma_f32_16x16x32_bf16 v[46:49], v[14:17], v[214:217], v[26:29]
	v_mfma_f32_16x16x32_bf16 v[26:29], v[18:21], v[210:213], v[146:149]
	v_mfma_f32_16x16x32_bf16 v[42:45], v[22:25], v[214:217], v[26:29]
	v_mfma_f32_16x16x32_bf16 v[26:29], v[10:13], v[218:221], v[150:153]
	v_mfma_f32_16x16x32_bf16 v[2:5], v[10:13], v[238:241], v[2:5]
	v_mfma_f32_16x16x32_bf16 v[30:33], v[14:17], v[222:225], v[26:29]
	v_mfma_f32_16x16x32_bf16 v[26:29], v[18:21], v[218:221], v[154:157]
	v_mfma_f32_16x16x32_bf16 v[14:17], v[14:17], v[242:245], v[2:5]
	v_mfma_f32_16x16x32_bf16 v[2:5], v[18:21], v[238:241], v[6:9]
	v_mfma_f32_16x16x32_bf16 v[26:29], v[22:25], v[222:225], v[26:29]
	v_mfma_f32_16x16x32_bf16 v[10:13], v[22:25], v[242:245], v[2:5]
	v_mfma_f32_16x16x32_bf16 v[2:5], v[194:197], v[34:37], v[158:161]
	v_mfma_f32_16x16x32_bf16 v[58:61], v[198:201], v[38:41], v[2:5]
	v_mfma_f32_16x16x32_bf16 v[2:5], v[202:205], v[34:37], v[162:165]
	v_mfma_f32_16x16x32_bf16 v[50:53], v[206:209], v[38:41], v[2:5]
	v_mfma_f32_16x16x32_bf16 v[2:5], v[194:197], v[210:213], v[174:177]
	v_mfma_f32_16x16x32_bf16 v[38:41], v[198:201], v[214:217], v[2:5]
	v_mfma_f32_16x16x32_bf16 v[2:5], v[202:205], v[210:213], v[178:181]
	v_mfma_f32_16x16x32_bf16 v[34:37], v[206:209], v[214:217], v[2:5]
	v_mfma_f32_16x16x32_bf16 v[2:5], v[194:197], v[218:221], v[182:185]
	v_mfma_f32_16x16x32_bf16 v[22:25], v[198:201], v[222:225], v[2:5]
	v_mfma_f32_16x16x32_bf16 v[2:5], v[202:205], v[218:221], v[122:125]
	v_mfma_f32_16x16x32_bf16 v[18:21], v[206:209], v[222:225], v[2:5]
	v_mfma_f32_16x16x32_bf16 v[2:5], v[194:197], v[238:241], v[186:189]
	v_mfma_f32_16x16x32_bf16 v[6:9], v[198:201], v[242:245], v[2:5]
	v_mfma_f32_16x16x32_bf16 v[2:5], v[202:205], v[238:241], v[130:133]
	v_mfma_f32_16x16x32_bf16 v[2:5], v[206:209], v[242:245], v[2:5]
	s_barrier
	s_setprio 0
	s_andn2_b64 vcc, exec, s[48:49]
	s_cbranch_vccnz .LBB0_1228
	s_add_u32 s73, s28, 0x20000
	s_addc_u32 s74, s29, 0
	s_add_u32 s26, s26, 0x1c000
	s_addc_u32 s27, s27, 0
	s_mov_b32 s75, 4
.LBB0_1227:
	ds_read_b128 v[122:125], v114
	ds_read_b128 v[130:133], v114 offset:1024
	ds_read_b128 v[134:137], v114 offset:2048
	ds_read_b128 v[138:141], v114 offset:3072
	ds_read_b128 v[142:145], v115
	ds_read_b128 v[146:149], v115 offset:1024
	ds_read_b128 v[150:153], v115 offset:2048
	ds_read_b128 v[154:157], v115 offset:3072
	s_add_u32 s28, s26, 0x4000
	s_addc_u32 s29, s27, 0
	s_cmp_eq_u32 s56, s75
	s_cselect_b32 s34, s38, s28
	s_cselect_b32 s35, s39, s29
	s_cselect_b32 s30, s40, s73
	s_cselect_b32 s31, s41, s74
	s_add_u32 s28, s34, 0x8000
	s_addc_u32 s29, s35, 0
	s_mov_b32 m0, s65
	ds_read_b128 v[158:161], v237
	ds_read_b128 v[162:165], v237 offset:1024
	ds_read_b128 v[174:177], v237 offset:2048
	ds_read_b128 v[178:181], v237 offset:3072
	ds_read_b128 v[182:185], v237 offset:4096
	ds_read_b128 v[186:189], v237 offset:5120
	ds_read_b128 v[194:197], v237 offset:6144
	ds_read_b128 v[198:201], v237 offset:7168
	s_nop 0
	global_load_lds_dwordx4 v235, s[26:27]
	s_mov_b32 m0, s66
	s_nop 0
	global_load_lds_dwordx4 v226, s[26:27]
	s_waitcnt vmcnt(8)
	s_waitcnt lgkmcnt(0)
	s_setprio 1
	s_barrier
	s_waitcnt lgkmcnt(0)
	v_mfma_f32_16x16x32_bf16 v[166:169], v[122:125], v[158:161], v[166:169]
	v_mfma_f32_16x16x32_bf16 v[170:173], v[134:137], v[158:161], v[170:173]
	v_mfma_f32_16x16x32_bf16 v[110:113], v[122:125], v[174:177], v[110:113]
	v_mfma_f32_16x16x32_bf16 v[106:109], v[134:137], v[174:177], v[106:109]
	v_mfma_f32_16x16x32_bf16 v[94:97], v[122:125], v[182:185], v[94:97]
	v_mfma_f32_16x16x32_bf16 v[90:93], v[134:137], v[182:185], v[90:93]
	v_mfma_f32_16x16x32_bf16 v[78:81], v[122:125], v[194:197], v[78:81]
	v_mfma_f32_16x16x32_bf16 v[70:73], v[134:137], v[194:197], v[70:73]
	v_mfma_f32_16x16x32_bf16 v[166:169], v[130:133], v[162:165], v[166:169]
	v_mfma_f32_16x16x32_bf16 v[170:173], v[138:141], v[162:165], v[170:173]
	v_mfma_f32_16x16x32_bf16 v[110:113], v[130:133], v[178:181], v[110:113]
	v_mfma_f32_16x16x32_bf16 v[106:109], v[138:141], v[178:181], v[106:109]
	v_mfma_f32_16x16x32_bf16 v[94:97], v[130:133], v[186:189], v[94:97]
	v_mfma_f32_16x16x32_bf16 v[90:93], v[138:141], v[186:189], v[90:93]
	v_mfma_f32_16x16x32_bf16 v[78:81], v[130:133], v[198:201], v[78:81]
	v_mfma_f32_16x16x32_bf16 v[70:73], v[138:141], v[198:201], v[70:73]
	v_mfma_f32_16x16x32_bf16 v[126:129], v[142:145], v[158:161], v[126:129]
	v_mfma_f32_16x16x32_bf16 v[118:121], v[150:153], v[158:161], v[118:121]
	v_mfma_f32_16x16x32_bf16 v[102:105], v[142:145], v[174:177], v[102:105]
	v_mfma_f32_16x16x32_bf16 v[98:101], v[150:153], v[174:177], v[98:101]
	v_mfma_f32_16x16x32_bf16 v[86:89], v[142:145], v[182:185], v[86:89]
	v_mfma_f32_16x16x32_bf16 v[82:85], v[150:153], v[182:185], v[82:85]
	v_mfma_f32_16x16x32_bf16 v[62:65], v[142:145], v[194:197], v[62:65]
	v_mfma_f32_16x16x32_bf16 v[54:57], v[150:153], v[194:197], v[54:57]
	v_mfma_f32_16x16x32_bf16 v[126:129], v[146:149], v[162:165], v[126:129]
	v_mfma_f32_16x16x32_bf16 v[118:121], v[154:157], v[162:165], v[118:121]
	v_mfma_f32_16x16x32_bf16 v[102:105], v[146:149], v[178:181], v[102:105]
	v_mfma_f32_16x16x32_bf16 v[98:101], v[154:157], v[178:181], v[98:101]
	v_mfma_f32_16x16x32_bf16 v[86:89], v[146:149], v[186:189], v[86:89]
	v_mfma_f32_16x16x32_bf16 v[82:85], v[154:157], v[186:189], v[82:85]
	v_mfma_f32_16x16x32_bf16 v[62:65], v[146:149], v[198:201], v[62:65]
	v_mfma_f32_16x16x32_bf16 v[54:57], v[154:157], v[198:201], v[54:57]
	s_barrier
	s_setprio 0
	s_mov_b32 m0, s67
	ds_read_b128 v[158:161], v237 offset:16384
	ds_read_b128 v[162:165], v237 offset:17408
	ds_read_b128 v[174:177], v237 offset:18432
	ds_read_b128 v[178:181], v237 offset:19456
	ds_read_b128 v[182:185], v237 offset:20480
	ds_read_b128 v[186:189], v237 offset:21504
	ds_read_b128 v[194:197], v237 offset:22528
	ds_read_b128 v[198:201], v237 offset:23552
	s_add_u32 s76, s30, 0x4000
	global_load_lds_dwordx4 v227, s[30:31]
	s_mov_b32 m0, s68
	s_addc_u32 s77, s31, 0
	global_load_lds_dwordx4 v0, s[30:31]
	s_mov_b32 m0, s69
	s_nop 0
	global_load_lds_dwordx4 v227, s[76:77]
	s_mov_b32 m0, s70
	s_nop 0
	global_load_lds_dwordx4 v0, s[76:77]
	s_mov_b32 m0, s20
	s_nop 0
	global_load_lds_dwordx4 v235, s[34:35]
	s_mov_b32 m0, s25
	s_nop 0
	global_load_lds_dwordx4 v226, s[34:35]
	s_waitcnt vmcnt(8)
	s_waitcnt lgkmcnt(0)
	s_setprio 1
	s_barrier
	s_waitcnt lgkmcnt(0)
	v_mfma_f32_16x16x32_bf16 v[74:77], v[122:125], v[158:161], v[74:77]
	v_mfma_f32_16x16x32_bf16 v[66:69], v[134:137], v[158:161], v[66:69]
	v_mfma_f32_16x16x32_bf16 v[46:49], v[122:125], v[174:177], v[46:49]
	v_mfma_f32_16x16x32_bf16 v[42:45], v[134:137], v[174:177], v[42:45]
	v_mfma_f32_16x16x32_bf16 v[30:33], v[122:125], v[182:185], v[30:33]
	v_mfma_f32_16x16x32_bf16 v[26:29], v[134:137], v[182:185], v[26:29]
	v_mfma_f32_16x16x32_bf16 v[14:17], v[122:125], v[194:197], v[14:17]
	v_mfma_f32_16x16x32_bf16 v[10:13], v[134:137], v[194:197], v[10:13]
	v_mfma_f32_16x16x32_bf16 v[74:77], v[130:133], v[162:165], v[74:77]
	v_mfma_f32_16x16x32_bf16 v[66:69], v[138:141], v[162:165], v[66:69]
	v_mfma_f32_16x16x32_bf16 v[46:49], v[130:133], v[178:181], v[46:49]
	v_mfma_f32_16x16x32_bf16 v[42:45], v[138:141], v[178:181], v[42:45]
	v_mfma_f32_16x16x32_bf16 v[30:33], v[130:133], v[186:189], v[30:33]
	v_mfma_f32_16x16x32_bf16 v[26:29], v[138:141], v[186:189], v[26:29]
	v_mfma_f32_16x16x32_bf16 v[14:17], v[130:133], v[198:201], v[14:17]
	v_mfma_f32_16x16x32_bf16 v[10:13], v[138:141], v[198:201], v[10:13]
	v_mfma_f32_16x16x32_bf16 v[58:61], v[142:145], v[158:161], v[58:61]
	v_mfma_f32_16x16x32_bf16 v[50:53], v[150:153], v[158:161], v[50:53]
	v_mfma_f32_16x16x32_bf16 v[38:41], v[142:145], v[174:177], v[38:41]
	v_mfma_f32_16x16x32_bf16 v[34:37], v[150:153], v[174:177], v[34:37]
	v_mfma_f32_16x16x32_bf16 v[22:25], v[142:145], v[182:185], v[22:25]
	v_mfma_f32_16x16x32_bf16 v[18:21], v[150:153], v[182:185], v[18:21]
	v_mfma_f32_16x16x32_bf16 v[6:9], v[142:145], v[194:197], v[6:9]
	v_mfma_f32_16x16x32_bf16 v[2:5], v[150:153], v[194:197], v[2:5]
	v_mfma_f32_16x16x32_bf16 v[58:61], v[146:149], v[162:165], v[58:61]
	v_mfma_f32_16x16x32_bf16 v[50:53], v[154:157], v[162:165], v[50:53]
	v_mfma_f32_16x16x32_bf16 v[38:41], v[146:149], v[178:181], v[38:41]
	v_mfma_f32_16x16x32_bf16 v[34:37], v[154:157], v[178:181], v[34:37]
	v_mfma_f32_16x16x32_bf16 v[22:25], v[146:149], v[186:189], v[22:25]
	v_mfma_f32_16x16x32_bf16 v[18:21], v[154:157], v[186:189], v[18:21]
	v_mfma_f32_16x16x32_bf16 v[6:9], v[146:149], v[198:201], v[6:9]
	v_mfma_f32_16x16x32_bf16 v[2:5], v[154:157], v[198:201], v[2:5]
	s_barrier
	s_setprio 0
	ds_read_b128 v[122:125], v116
	ds_read_b128 v[130:133], v116 offset:1024
	ds_read_b128 v[134:137], v116 offset:2048
	ds_read_b128 v[138:141], v116 offset:3072
	ds_read_b128 v[142:145], v117
	ds_read_b128 v[146:149], v117 offset:1024
	ds_read_b128 v[150:153], v117 offset:2048
	ds_read_b128 v[154:157], v117 offset:3072
	s_add_u32 s34, s34, 0x4000
	s_addc_u32 s35, s35, 0
	s_mov_b32 m0, s54
	ds_read_b128 v[158:161], v237 offset:32768
	ds_read_b128 v[162:165], v237 offset:33792
	ds_read_b128 v[174:177], v237 offset:34816
	ds_read_b128 v[178:181], v237 offset:35840
	ds_read_b128 v[182:185], v237 offset:36864
	ds_read_b128 v[186:189], v237 offset:37888
	ds_read_b128 v[194:197], v237 offset:38912
	ds_read_b128 v[198:201], v237 offset:39936
	s_nop 0
	global_load_lds_dwordx4 v235, s[34:35]
	s_mov_b32 m0, s55
	s_nop 0
	global_load_lds_dwordx4 v226, s[34:35]
	s_waitcnt vmcnt(8)
	s_waitcnt lgkmcnt(0)
	s_setprio 1
	s_barrier
	s_waitcnt lgkmcnt(0)
	v_mfma_f32_16x16x32_bf16 v[166:169], v[122:125], v[158:161], v[166:169]
	v_mfma_f32_16x16x32_bf16 v[170:173], v[134:137], v[158:161], v[170:173]
	v_mfma_f32_16x16x32_bf16 v[110:113], v[122:125], v[174:177], v[110:113]
	v_mfma_f32_16x16x32_bf16 v[106:109], v[134:137], v[174:177], v[106:109]
	v_mfma_f32_16x16x32_bf16 v[94:97], v[122:125], v[182:185], v[94:97]
	v_mfma_f32_16x16x32_bf16 v[90:93], v[134:137], v[182:185], v[90:93]
	v_mfma_f32_16x16x32_bf16 v[78:81], v[122:125], v[194:197], v[78:81]
	v_mfma_f32_16x16x32_bf16 v[70:73], v[134:137], v[194:197], v[70:73]
	v_mfma_f32_16x16x32_bf16 v[166:169], v[130:133], v[162:165], v[166:169]
	v_mfma_f32_16x16x32_bf16 v[170:173], v[138:141], v[162:165], v[170:173]
	v_mfma_f32_16x16x32_bf16 v[110:113], v[130:133], v[178:181], v[110:113]
	v_mfma_f32_16x16x32_bf16 v[106:109], v[138:141], v[178:181], v[106:109]
	v_mfma_f32_16x16x32_bf16 v[94:97], v[130:133], v[186:189], v[94:97]
	v_mfma_f32_16x16x32_bf16 v[90:93], v[138:141], v[186:189], v[90:93]
	v_mfma_f32_16x16x32_bf16 v[78:81], v[130:133], v[198:201], v[78:81]
	v_mfma_f32_16x16x32_bf16 v[70:73], v[138:141], v[198:201], v[70:73]
	v_mfma_f32_16x16x32_bf16 v[126:129], v[142:145], v[158:161], v[126:129]
	v_mfma_f32_16x16x32_bf16 v[118:121], v[150:153], v[158:161], v[118:121]
	v_mfma_f32_16x16x32_bf16 v[102:105], v[142:145], v[174:177], v[102:105]
	v_mfma_f32_16x16x32_bf16 v[98:101], v[150:153], v[174:177], v[98:101]
	v_mfma_f32_16x16x32_bf16 v[86:89], v[142:145], v[182:185], v[86:89]
	v_mfma_f32_16x16x32_bf16 v[82:85], v[150:153], v[182:185], v[82:85]
	v_mfma_f32_16x16x32_bf16 v[62:65], v[142:145], v[194:197], v[62:65]
	v_mfma_f32_16x16x32_bf16 v[54:57], v[150:153], v[194:197], v[54:57]
	v_mfma_f32_16x16x32_bf16 v[126:129], v[146:149], v[162:165], v[126:129]
	v_mfma_f32_16x16x32_bf16 v[118:121], v[154:157], v[162:165], v[118:121]
	v_mfma_f32_16x16x32_bf16 v[102:105], v[146:149], v[178:181], v[102:105]
	v_mfma_f32_16x16x32_bf16 v[98:101], v[154:157], v[178:181], v[98:101]
	v_mfma_f32_16x16x32_bf16 v[86:89], v[146:149], v[186:189], v[86:89]
	v_mfma_f32_16x16x32_bf16 v[82:85], v[154:157], v[186:189], v[82:85]
	v_mfma_f32_16x16x32_bf16 v[62:65], v[146:149], v[198:201], v[62:65]
	v_mfma_f32_16x16x32_bf16 v[54:57], v[154:157], v[198:201], v[54:57]
	s_barrier
	s_setprio 0
	s_add_u32 s34, s30, 0x8000
	s_mov_b32 m0, s52
	s_addc_u32 s35, s31, 0
	ds_read_b128 v[158:161], v237 offset:49152
	ds_read_b128 v[162:165], v237 offset:50176
	ds_read_b128 v[174:177], v237 offset:51200
	ds_read_b128 v[178:181], v237 offset:52224
	ds_read_b128 v[182:185], v237 offset:53248
	ds_read_b128 v[186:189], v237 offset:54272
	ds_read_b128 v[194:197], v237 offset:55296
	ds_read_b128 v[198:201], v237 offset:56320
	s_add_u32 s30, s30, 0xc000
	global_load_lds_dwordx4 v227, s[34:35]
	s_mov_b32 m0, s53
	s_addc_u32 s31, s31, 0
	global_load_lds_dwordx4 v0, s[34:35]
	s_mov_b32 m0, s71
	s_nop 0
	global_load_lds_dwordx4 v227, s[30:31]
	s_mov_b32 m0, s72
	s_nop 0
	global_load_lds_dwordx4 v0, s[30:31]
	s_mov_b32 m0, s58
	s_nop 0
	global_load_lds_dwordx4 v235, s[28:29]
	s_mov_b32 m0, s59
	s_nop 0
	global_load_lds_dwordx4 v226, s[28:29]
	s_waitcnt vmcnt(8)
	s_waitcnt lgkmcnt(0)
	s_setprio 1
	s_barrier
	s_waitcnt lgkmcnt(0)
	v_mfma_f32_16x16x32_bf16 v[74:77], v[122:125], v[158:161], v[74:77]
	v_mfma_f32_16x16x32_bf16 v[66:69], v[134:137], v[158:161], v[66:69]
	v_mfma_f32_16x16x32_bf16 v[46:49], v[122:125], v[174:177], v[46:49]
	v_mfma_f32_16x16x32_bf16 v[42:45], v[134:137], v[174:177], v[42:45]
	v_mfma_f32_16x16x32_bf16 v[30:33], v[122:125], v[182:185], v[30:33]
	v_mfma_f32_16x16x32_bf16 v[26:29], v[134:137], v[182:185], v[26:29]
	v_mfma_f32_16x16x32_bf16 v[14:17], v[122:125], v[194:197], v[14:17]
	v_mfma_f32_16x16x32_bf16 v[10:13], v[134:137], v[194:197], v[10:13]
	v_mfma_f32_16x16x32_bf16 v[74:77], v[130:133], v[162:165], v[74:77]
	v_mfma_f32_16x16x32_bf16 v[66:69], v[138:141], v[162:165], v[66:69]
	v_mfma_f32_16x16x32_bf16 v[46:49], v[130:133], v[178:181], v[46:49]
	v_mfma_f32_16x16x32_bf16 v[42:45], v[138:141], v[178:181], v[42:45]
	v_mfma_f32_16x16x32_bf16 v[30:33], v[130:133], v[186:189], v[30:33]
	v_mfma_f32_16x16x32_bf16 v[26:29], v[138:141], v[186:189], v[26:29]
	v_mfma_f32_16x16x32_bf16 v[14:17], v[130:133], v[198:201], v[14:17]
	v_mfma_f32_16x16x32_bf16 v[10:13], v[138:141], v[198:201], v[10:13]
	v_mfma_f32_16x16x32_bf16 v[58:61], v[142:145], v[158:161], v[58:61]
	v_mfma_f32_16x16x32_bf16 v[50:53], v[150:153], v[158:161], v[50:53]
	v_mfma_f32_16x16x32_bf16 v[38:41], v[142:145], v[174:177], v[38:41]
	v_mfma_f32_16x16x32_bf16 v[34:37], v[150:153], v[174:177], v[34:37]
	v_mfma_f32_16x16x32_bf16 v[22:25], v[142:145], v[182:185], v[22:25]
	v_mfma_f32_16x16x32_bf16 v[18:21], v[150:153], v[182:185], v[18:21]
	v_mfma_f32_16x16x32_bf16 v[6:9], v[142:145], v[194:197], v[6:9]
	v_mfma_f32_16x16x32_bf16 v[2:5], v[150:153], v[194:197], v[2:5]
	v_mfma_f32_16x16x32_bf16 v[58:61], v[146:149], v[162:165], v[58:61]
	v_mfma_f32_16x16x32_bf16 v[50:53], v[154:157], v[162:165], v[50:53]
	v_mfma_f32_16x16x32_bf16 v[38:41], v[146:149], v[178:181], v[38:41]
	v_mfma_f32_16x16x32_bf16 v[34:37], v[154:157], v[178:181], v[34:37]
	v_mfma_f32_16x16x32_bf16 v[22:25], v[146:149], v[186:189], v[22:25]
	v_mfma_f32_16x16x32_bf16 v[18:21], v[154:157], v[186:189], v[18:21]
	v_mfma_f32_16x16x32_bf16 v[6:9], v[146:149], v[198:201], v[6:9]
	v_mfma_f32_16x16x32_bf16 v[2:5], v[154:157], v[198:201], v[2:5]
	s_barrier
	s_setprio 0
	s_add_i32 s28, s75, 2
	s_add_u32 s73, s73, 0x10000
	s_addc_u32 s74, s74, 0
	s_add_u32 s26, s26, 0x10000
	s_addc_u32 s27, s27, 0
	s_cmp_lt_i32 s75, s56
	s_mov_b32 s75, s28
	s_cbranch_scc1 .LBB0_1227
